# MFMA SrcB fragment registers renamed (differ mod 4 from SrcA) in 11 GEMM K-loops, nothing else
# baseline (speedup 1.0000x reference)
; #define PG8_STAGE(bufoff, gbase, voff) do { _Pragma("unroll") for (int _i = 0; _i < 2; ++_i) \
;         __builtin_amdgcn_global_load_lds((const __attribute__((address_space(1))) unsigned*)((const __attribute__((address_space(1))) char*)(gbase) + (unsigned)lnd_v((int)(voff)[_i])), (LAS unsigned*)(lds + (bufoff) + ldsw + _i * 8192), 16, 0, 0); } while (0)
; #define PG8_LDA(dst, b, h) do { _Pragma("unroll") for (int m = 0; m < 4; ++m) _Pragma("unroll") for (int k = 0; k < 2; ++k) dst[m][k] = *(const LAS bf16x8*)(lds + PG8_SA(b, h) + aoff + m * 2048 + k * 1024); } while (0)
; #define PG8_LDB(dst, b, h) do { _Pragma("unroll") for (int n = 0; n < 2; ++n) _Pragma("unroll") for (int k = 0; k < 2; ++k) dst[n][k] = *(const LAS bf16x8*)(lds + PG8_SB(b, h) + boff + n * 2048 + k * 1024); } while (0)
; #define PG8_MMA(ai, bj, At, Bt) do { __builtin_amdgcn_s_setprio(1); _Pragma("unroll") for (int m = 0; m < 4; ++m) _Pragma("unroll") for (int n = 0; n < 2; ++n) _Pragma("unroll") for (int k = 0; k < 2; ++k) \
;         acc[ai][bj][m][n] = __builtin_amdgcn_mfma_f32_16x16x32_bf16(Bt[n][k], At[m][k], acc[ai][bj][m][n], 0, 0, 0); __builtin_amdgcn_s_setprio(0); } while (0)
; #define PG8_WAIT_V(n) asm volatile("s_waitcnt vmcnt(" #n ")" ::: "memory")
; #define PG8_WAIT_L(n) asm volatile("s_waitcnt lgkmcnt(" #n ")" ::: "memory")
; #define PG8_BAR __builtin_amdgcn_s_barrier()
; #define PG8_SCHED __builtin_amdgcn_sched_barrier(0)
; template <class Desc, class Epi>
; __device__ __forceinline__ void gemm_phase(const int wv_, LAS unsigned char* lds, const Desc& d, const Epi& E) {
;     ...
;             PG8_LDB(B0, 0, 0); PG8_LDB(B1, 0, 1); PG8_SCHED; PG8_LDA(At, 0, 0); PG8_STAGE(PG8_SA(1, 1), a1, voffA1);
;             PG8_WAIT_V(8); PG8_WAIT_L(0); PG8_BAR; PG8_MMA(0, 0, At, B0); PG8_MMA(0, 1, At, B1); PG8_BAR; PG8_SCHED;
;             PG8_LDA(At, 0, 1); PG8_STAGE(PG8_SB(0, 0), b2, voffB); PG8_STAGE(PG8_SB(0, 1), b2 + hstepB, voffB); PG8_STAGE(PG8_SA(0, 0), a2, sA0);
;             PG8_WAIT_V(8); PG8_WAIT_L(0); PG8_BAR; PG8_MMA(1, 0, At, B0); PG8_MMA(1, 1, At, B1); PG8_BAR; PG8_SCHED;
.LBB0_662:
	ds_read_b128 v[154:157], v148
	ds_read_b128 v[158:161], v148 offset:1024
	ds_read_b128 v[162:165], v148 offset:2048
	ds_read_b128 v[166:169], v148 offset:3072
	ds_read_b128 v[170:173], v149
	ds_read_b128 v[174:177], v149 offset:1024
	ds_read_b128 v[178:181], v149 offset:2048
	ds_read_b128 v[182:185], v149 offset:3072
	s_add_u32 s2, s0, 0x80
	s_addc_u32 s3, s1, 0
	s_cmp_eq_u32 s60, 12
	s_cselect_b32 s3, s17, s3
	s_cselect_b32 s2, s16, s2
	s_cselect_b32 s27, s23, s59
	s_cselect_b32 s26, s22, s58
	v_mov_b32_e32 v128, v133
	s_mov_b32 m0, s42
	ds_read_b128 v[188:191], v150
	ds_read_b128 v[192:195], v150 offset:1024
	ds_read_b128 v[196:199], v150 offset:2048
	ds_read_b128 v[200:203], v150 offset:3072
	ds_read_b128 v[204:207], v150 offset:4096
	ds_read_b128 v[208:211], v150 offset:5120
	ds_read_b128 v[212:215], v150 offset:6144
	ds_read_b128 v[220:223], v150 offset:7168
	s_nop 0
	global_load_lds_dwordx4 v128, s[0:1]
	v_mov_b32_e32 v128, v136
	s_mov_b32 m0, s43
	s_nop 0
	global_load_lds_dwordx4 v128, s[0:1]
	s_waitcnt vmcnt(8)
	s_waitcnt lgkmcnt(0)
	s_barrier
	s_setprio 1
	s_waitcnt lgkmcnt(0)
	v_mfma_f32_16x16x32_bf16 v[124:127], v[154:157], v[188:191], v[124:127]
	v_mfma_f32_16x16x32_bf16 v[120:123], v[162:165], v[188:191], v[120:123]
	v_mfma_f32_16x16x32_bf16 v[108:111], v[154:157], v[196:199], v[108:111]
	v_mfma_f32_16x16x32_bf16 v[104:107], v[162:165], v[196:199], v[104:107]
	v_mfma_f32_16x16x32_bf16 v[92:95], v[154:157], v[204:207], v[92:95]
	v_mfma_f32_16x16x32_bf16 v[88:91], v[162:165], v[204:207], v[88:91]
	v_mfma_f32_16x16x32_bf16 v[76:79], v[154:157], v[212:215], v[76:79]
	v_mfma_f32_16x16x32_bf16 v[72:75], v[162:165], v[212:215], v[72:75]
	v_mfma_f32_16x16x32_bf16 v[124:127], v[158:161], v[192:195], v[124:127]
	v_mfma_f32_16x16x32_bf16 v[120:123], v[166:169], v[192:195], v[120:123]
	v_mfma_f32_16x16x32_bf16 v[108:111], v[158:161], v[200:203], v[108:111]
	v_mfma_f32_16x16x32_bf16 v[104:107], v[166:169], v[200:203], v[104:107]
	v_mfma_f32_16x16x32_bf16 v[92:95], v[158:161], v[208:211], v[92:95]
	v_mfma_f32_16x16x32_bf16 v[88:91], v[166:169], v[208:211], v[88:91]
	v_mfma_f32_16x16x32_bf16 v[76:79], v[158:161], v[220:223], v[76:79]
	v_mfma_f32_16x16x32_bf16 v[72:75], v[166:169], v[220:223], v[72:75]
	s_setprio 0
	s_setprio 1
	v_mfma_f32_16x16x32_bf16 v[116:119], v[170:173], v[188:191], v[116:119]
	v_mfma_f32_16x16x32_bf16 v[112:115], v[178:181], v[188:191], v[112:115]
	v_mfma_f32_16x16x32_bf16 v[100:103], v[170:173], v[196:199], v[100:103]
	v_mfma_f32_16x16x32_bf16 v[96:99], v[178:181], v[196:199], v[96:99]
	v_mfma_f32_16x16x32_bf16 v[84:87], v[170:173], v[204:207], v[84:87]
	v_mfma_f32_16x16x32_bf16 v[80:83], v[178:181], v[204:207], v[80:83]
	v_mfma_f32_16x16x32_bf16 v[68:71], v[170:173], v[212:215], v[68:71]
	v_mfma_f32_16x16x32_bf16 v[64:67], v[178:181], v[212:215], v[64:67]
	v_mfma_f32_16x16x32_bf16 v[116:119], v[174:177], v[192:195], v[116:119]
	v_mfma_f32_16x16x32_bf16 v[112:115], v[182:185], v[192:195], v[112:115]
	v_mfma_f32_16x16x32_bf16 v[100:103], v[174:177], v[200:203], v[100:103]
	v_mfma_f32_16x16x32_bf16 v[96:99], v[182:185], v[200:203], v[96:99]
	v_mfma_f32_16x16x32_bf16 v[84:87], v[174:177], v[208:211], v[84:87]
	v_mfma_f32_16x16x32_bf16 v[80:83], v[182:185], v[208:211], v[80:83]
	v_mfma_f32_16x16x32_bf16 v[68:71], v[174:177], v[220:223], v[68:71]
	v_mfma_f32_16x16x32_bf16 v[64:67], v[182:185], v[220:223], v[64:67]
	s_setprio 0
	s_barrier
	v_mov_b32_e32 v128, v134
	s_mov_b32 m0, s44
	ds_read_b128 v[188:191], v150 offset:16384
	ds_read_b128 v[192:195], v150 offset:17408
	ds_read_b128 v[196:199], v150 offset:18432
	ds_read_b128 v[200:203], v150 offset:19456
	ds_read_b128 v[204:207], v150 offset:20480
	ds_read_b128 v[208:211], v150 offset:21504
	ds_read_b128 v[212:215], v150 offset:22528
	ds_read_b128 v[220:223], v150 offset:23552
	s_add_u32 s62, s26, 0x40000
	global_load_lds_dwordx4 v128, s[26:27]
	v_mov_b32_e32 v128, v137
	s_mov_b32 m0, s45
	s_addc_u32 s63, s27, 0
	global_load_lds_dwordx4 v128, s[26:27]
	v_mov_b32_e32 v128, v134
	s_mov_b32 m0, s46
	s_nop 0
	global_load_lds_dwordx4 v128, s[62:63]
	v_mov_b32_e32 v128, v137
	s_mov_b32 m0, s47
	s_nop 0
	global_load_lds_dwordx4 v128, s[62:63]
	v_mov_b32_e32 v128, v132
	s_mov_b32 m0, s36
	s_nop 0
	global_load_lds_dwordx4 v128, s[2:3]
	v_mov_b32_e32 v128, v135
	s_mov_b32 m0, s37
	s_nop 0
	global_load_lds_dwordx4 v128, s[2:3]
	s_waitcnt vmcnt(8)
	s_waitcnt lgkmcnt(0)
	s_barrier
	s_setprio 1
	s_waitcnt lgkmcnt(0)
	v_mfma_f32_16x16x32_bf16 v[60:63], v[154:157], v[188:191], v[60:63]
	v_mfma_f32_16x16x32_bf16 v[56:59], v[162:165], v[188:191], v[56:59]
	v_mfma_f32_16x16x32_bf16 v[44:47], v[154:157], v[196:199], v[44:47]
	v_mfma_f32_16x16x32_bf16 v[32:35], v[162:165], v[196:199], v[32:35]
	v_mfma_f32_16x16x32_bf16 v[16:19], v[154:157], v[204:207], v[16:19]
	v_mfma_f32_16x16x32_bf16 v[8:11], v[162:165], v[204:207], v[8:11]
	v_mfma_f32_16x16x32_bf16 v[4:7], v[154:157], v[212:215], v[4:7]
	v_mfma_f32_16x16x32_bf16 v[0:3], v[162:165], v[212:215], v[0:3]
	v_mfma_f32_16x16x32_bf16 v[60:63], v[158:161], v[192:195], v[60:63]
	v_mfma_f32_16x16x32_bf16 v[56:59], v[166:169], v[192:195], v[56:59]
	v_mfma_f32_16x16x32_bf16 v[44:47], v[158:161], v[200:203], v[44:47]
	v_mfma_f32_16x16x32_bf16 v[32:35], v[166:169], v[200:203], v[32:35]
	v_mfma_f32_16x16x32_bf16 v[16:19], v[158:161], v[208:211], v[16:19]
	v_mfma_f32_16x16x32_bf16 v[8:11], v[166:169], v[208:211], v[8:11]
	v_mfma_f32_16x16x32_bf16 v[4:7], v[158:161], v[220:223], v[4:7]
	v_mfma_f32_16x16x32_bf16 v[0:3], v[166:169], v[220:223], v[0:3]
	s_setprio 0
	s_setprio 1
	v_mfma_f32_16x16x32_bf16 v[52:55], v[170:173], v[188:191], v[52:55]
	v_mfma_f32_16x16x32_bf16 v[48:51], v[178:181], v[188:191], v[48:51]
	v_mfma_f32_16x16x32_bf16 v[28:31], v[170:173], v[196:199], v[28:31]
	v_mfma_f32_16x16x32_bf16 v[12:15], v[178:181], v[196:199], v[12:15]
	v_mfma_f32_16x16x32_bf16 v[36:39], v[170:173], v[204:207], v[36:39]
	v_mfma_f32_16x16x32_bf16 v[40:43], v[178:181], v[204:207], v[40:43]
	v_mfma_f32_16x16x32_bf16 v[20:23], v[170:173], v[212:215], v[20:23]
	v_mfma_f32_16x16x32_bf16 v[24:27], v[178:181], v[212:215], v[24:27]
	v_mfma_f32_16x16x32_bf16 v[52:55], v[174:177], v[192:195], v[52:55]
	v_mfma_f32_16x16x32_bf16 v[48:51], v[182:185], v[192:195], v[48:51]
	v_mfma_f32_16x16x32_bf16 v[28:31], v[174:177], v[200:203], v[28:31]
	v_mfma_f32_16x16x32_bf16 v[12:15], v[182:185], v[200:203], v[12:15]
	v_mfma_f32_16x16x32_bf16 v[36:39], v[174:177], v[208:211], v[36:39]
	v_mfma_f32_16x16x32_bf16 v[40:43], v[182:185], v[208:211], v[40:43]
	v_mfma_f32_16x16x32_bf16 v[20:23], v[174:177], v[220:223], v[20:23]
	v_mfma_f32_16x16x32_bf16 v[24:27], v[182:185], v[220:223], v[24:27]
	s_setprio 0
	s_barrier
; #define PG8_STAGE(bufoff, gbase, voff) do { _Pragma("unroll") for (int _i = 0; _i < 2; ++_i) \
;         __builtin_amdgcn_global_load_lds((const __attribute__((address_space(1))) unsigned*)((const __attribute__((address_space(1))) char*)(gbase) + (unsigned)lnd_v((int)(voff)[_i])), (LAS unsigned*)(lds + (bufoff) + ldsw + _i * 8192), 16, 0, 0); } while (0)
; #define PG8_LDA(dst, b, h) do { _Pragma("unroll") for (int m = 0; m < 4; ++m) _Pragma("unroll") for (int k = 0; k < 2; ++k) dst[m][k] = *(const LAS bf16x8*)(lds + PG8_SA(b, h) + aoff + m * 2048 + k * 1024); } while (0)
; #define PG8_LDB(dst, b, h) do { _Pragma("unroll") for (int n = 0; n < 2; ++n) _Pragma("unroll") for (int k = 0; k < 2; ++k) dst[n][k] = *(const LAS bf16x8*)(lds + PG8_SB(b, h) + boff + n * 2048 + k * 1024); } while (0)
; #define PG8_MMA(ai, bj, At, Bt) do { __builtin_amdgcn_s_setprio(1); _Pragma("unroll") for (int m = 0; m < 4; ++m) _Pragma("unroll") for (int n = 0; n < 2; ++n) _Pragma("unroll") for (int k = 0; k < 2; ++k) \
;         acc[ai][bj][m][n] = __builtin_amdgcn_mfma_f32_16x16x32_bf16(Bt[n][k], At[m][k], acc[ai][bj][m][n], 0, 0, 0); __builtin_amdgcn_s_setprio(0); } while (0)
; #define PG8_WAIT_V(n) asm volatile("s_waitcnt vmcnt(" #n ")" ::: "memory")
; #define PG8_WAIT_L(n) asm volatile("s_waitcnt lgkmcnt(" #n ")" ::: "memory")
; #define PG8_BAR __builtin_amdgcn_s_barrier()
; #define PG8_SCHED __builtin_amdgcn_sched_barrier(0)
; template <class Desc, class Epi>
; __device__ __forceinline__ void gemm_phase(const int wv_, LAS unsigned char* lds, const Desc& d, const Epi& E) {
;     ...
;             PG8_LDB(B0, 1, 0); PG8_LDB(B1, 1, 1); PG8_SCHED; PG8_LDA(At, 1, 0); PG8_STAGE(PG8_SA(0, 1), a2, sA1);
;             PG8_WAIT_V(8); PG8_WAIT_L(0); PG8_BAR; PG8_MMA(0, 0, At, B0); PG8_MMA(0, 1, At, B1); PG8_BAR; PG8_SCHED;
	ds_read_b128 v[154:157], v151
	ds_read_b128 v[158:161], v151 offset:1024
	ds_read_b128 v[162:165], v151 offset:2048
	ds_read_b128 v[166:169], v151 offset:3072
	ds_read_b128 v[170:173], v152
	ds_read_b128 v[174:177], v152 offset:1024
	ds_read_b128 v[178:181], v152 offset:2048
	ds_read_b128 v[182:185], v152 offset:3072
	v_mov_b32_e32 v128, v133
	s_mov_b32 m0, s38
	ds_read_b128 v[188:191], v150 offset:32768
	ds_read_b128 v[192:195], v150 offset:33792
	ds_read_b128 v[196:199], v150 offset:34816
	ds_read_b128 v[200:203], v150 offset:35840
	ds_read_b128 v[204:207], v150 offset:36864
	ds_read_b128 v[208:211], v150 offset:37888
	ds_read_b128 v[212:215], v150 offset:38912
	ds_read_b128 v[220:223], v150 offset:39936
	s_nop 0
	global_load_lds_dwordx4 v128, s[2:3]
	v_mov_b32_e32 v128, v136
	s_mov_b32 m0, s39
	s_nop 0
	global_load_lds_dwordx4 v128, s[2:3]
	s_waitcnt vmcnt(8)
	s_waitcnt lgkmcnt(0)
	s_barrier
	s_setprio 1
	s_waitcnt lgkmcnt(0)
	v_mfma_f32_16x16x32_bf16 v[124:127], v[154:157], v[188:191], v[124:127]
	v_mfma_f32_16x16x32_bf16 v[120:123], v[162:165], v[188:191], v[120:123]
	v_mfma_f32_16x16x32_bf16 v[108:111], v[154:157], v[196:199], v[108:111]
	v_mfma_f32_16x16x32_bf16 v[104:107], v[162:165], v[196:199], v[104:107]
	v_mfma_f32_16x16x32_bf16 v[92:95], v[154:157], v[204:207], v[92:95]
	v_mfma_f32_16x16x32_bf16 v[88:91], v[162:165], v[204:207], v[88:91]
	v_mfma_f32_16x16x32_bf16 v[76:79], v[154:157], v[212:215], v[76:79]
	v_mfma_f32_16x16x32_bf16 v[72:75], v[162:165], v[212:215], v[72:75]
	v_mfma_f32_16x16x32_bf16 v[124:127], v[158:161], v[192:195], v[124:127]
	v_mfma_f32_16x16x32_bf16 v[120:123], v[166:169], v[192:195], v[120:123]
	v_mfma_f32_16x16x32_bf16 v[108:111], v[158:161], v[200:203], v[108:111]
	v_mfma_f32_16x16x32_bf16 v[104:107], v[166:169], v[200:203], v[104:107]
	v_mfma_f32_16x16x32_bf16 v[92:95], v[158:161], v[208:211], v[92:95]
	v_mfma_f32_16x16x32_bf16 v[88:91], v[166:169], v[208:211], v[88:91]
	v_mfma_f32_16x16x32_bf16 v[76:79], v[158:161], v[220:223], v[76:79]
	v_mfma_f32_16x16x32_bf16 v[72:75], v[166:169], v[220:223], v[72:75]
	s_setprio 0
	s_setprio 1
	v_mfma_f32_16x16x32_bf16 v[116:119], v[170:173], v[188:191], v[116:119]
	v_mfma_f32_16x16x32_bf16 v[112:115], v[178:181], v[188:191], v[112:115]
	v_mfma_f32_16x16x32_bf16 v[100:103], v[170:173], v[196:199], v[100:103]
	v_mfma_f32_16x16x32_bf16 v[96:99], v[178:181], v[196:199], v[96:99]
	v_mfma_f32_16x16x32_bf16 v[84:87], v[170:173], v[204:207], v[84:87]
	v_mfma_f32_16x16x32_bf16 v[80:83], v[178:181], v[204:207], v[80:83]
	v_mfma_f32_16x16x32_bf16 v[68:71], v[170:173], v[212:215], v[68:71]
	v_mfma_f32_16x16x32_bf16 v[64:67], v[178:181], v[212:215], v[64:67]
	v_mfma_f32_16x16x32_bf16 v[116:119], v[174:177], v[192:195], v[116:119]
	v_mfma_f32_16x16x32_bf16 v[112:115], v[182:185], v[192:195], v[112:115]
	v_mfma_f32_16x16x32_bf16 v[100:103], v[174:177], v[200:203], v[100:103]
	v_mfma_f32_16x16x32_bf16 v[96:99], v[182:185], v[200:203], v[96:99]
	v_mfma_f32_16x16x32_bf16 v[84:87], v[174:177], v[208:211], v[84:87]
	v_mfma_f32_16x16x32_bf16 v[80:83], v[182:185], v[208:211], v[80:83]
	v_mfma_f32_16x16x32_bf16 v[68:71], v[174:177], v[220:223], v[68:71]
	v_mfma_f32_16x16x32_bf16 v[64:67], v[182:185], v[220:223], v[64:67]
	s_setprio 0
	s_barrier
; #define PG8_STAGE(bufoff, gbase, voff) do { _Pragma("unroll") for (int _i = 0; _i < 2; ++_i) \
;         __builtin_amdgcn_global_load_lds((const __attribute__((address_space(1))) unsigned*)((const __attribute__((address_space(1))) char*)(gbase) + (unsigned)lnd_v((int)(voff)[_i])), (LAS unsigned*)(lds + (bufoff) + ldsw + _i * 8192), 16, 0, 0); } while (0)
; #define PG8_LDA(dst, b, h) do { _Pragma("unroll") for (int m = 0; m < 4; ++m) _Pragma("unroll") for (int k = 0; k < 2; ++k) dst[m][k] = *(const LAS bf16x8*)(lds + PG8_SA(b, h) + aoff + m * 2048 + k * 1024); } while (0)
; #define PG8_MMA(ai, bj, At, Bt) do { __builtin_amdgcn_s_setprio(1); _Pragma("unroll") for (int m = 0; m < 4; ++m) _Pragma("unroll") for (int n = 0; n < 2; ++n) _Pragma("unroll") for (int k = 0; k < 2; ++k) \
;         acc[ai][bj][m][n] = __builtin_amdgcn_mfma_f32_16x16x32_bf16(Bt[n][k], At[m][k], acc[ai][bj][m][n], 0, 0, 0); __builtin_amdgcn_s_setprio(0); } while (0)
; #define PG8_WAIT_V(n) asm volatile("s_waitcnt vmcnt(" #n ")" ::: "memory")
; #define PG8_WAIT_L(n) asm volatile("s_waitcnt lgkmcnt(" #n ")" ::: "memory")
; #define PG8_BAR __builtin_amdgcn_s_barrier()
; #define PG8_SCHED __builtin_amdgcn_sched_barrier(0)
; template <class Desc, class Epi>
; __device__ __forceinline__ void gemm_phase(const int wv_, LAS unsigned char* lds, const Desc& d, const Epi& E) {
;     ...
;             PG8_LDA(At, 1, 1); PG8_STAGE(PG8_SB(1, 0), b3, voffB); PG8_STAGE(PG8_SB(1, 1), b3 + hstepB, voffB); PG8_STAGE(PG8_SA(1, 0), a3, sA0);
;             PG8_WAIT_V(8); PG8_WAIT_L(0); PG8_BAR; PG8_MMA(1, 0, At, B0); PG8_MMA(1, 1, At, B1); PG8_BAR; PG8_SCHED;
;         }
	v_mov_b32_e32 v128, v134
	ds_read_b128 v[188:191], v150 offset:49152
	ds_read_b128 v[192:195], v150 offset:50176
	ds_read_b128 v[196:199], v150 offset:51200
	ds_read_b128 v[200:203], v150 offset:52224
	ds_read_b128 v[204:207], v150 offset:53248
	ds_read_b128 v[208:211], v150 offset:54272
	ds_read_b128 v[212:215], v150 offset:55296
	ds_read_b128 v[220:223], v150 offset:56320
	s_mov_b32 m0, s48
	v_lshl_add_u64 v[130:131], s[26:27], 0, v[128:129]
	v_lshl_add_u64 v[130:131], v[130:131], 0, s[8:9]
	v_mov_b32_e32 v128, v137
	global_load_lds_dwordx4 v[130:131], off
	s_mov_b32 m0, s49
	v_lshl_add_u64 v[130:131], s[26:27], 0, v[128:129]
	v_lshl_add_u64 v[130:131], v[130:131], 0, s[8:9]
	s_add_u32 s26, s26, 0x40080
	v_mov_b32_e32 v128, v134
	global_load_lds_dwordx4 v[130:131], off
	s_addc_u32 s27, s27, 0
	s_mov_b32 m0, s50
	s_nop 0
	global_load_lds_dwordx4 v128, s[26:27]
	v_mov_b32_e32 v128, v137
	s_mov_b32 m0, s51
	s_nop 0
	global_load_lds_dwordx4 v128, s[26:27]
	v_mov_b32_e32 v128, v132
	s_mov_b32 m0, s40
	v_lshl_add_u64 v[130:131], s[2:3], 0, v[128:129]
	v_lshl_add_u64 v[130:131], v[130:131], 0, s[8:9]
	v_mov_b32_e32 v128, v135
	global_load_lds_dwordx4 v[130:131], off
	s_mov_b32 m0, s41
	v_lshl_add_u64 v[130:131], s[2:3], 0, v[128:129]
	v_lshl_add_u64 v[130:131], v[130:131], 0, s[8:9]
	global_load_lds_dwordx4 v[130:131], off
	s_waitcnt vmcnt(8)
	s_waitcnt lgkmcnt(0)
	s_barrier
	s_setprio 1
	s_waitcnt lgkmcnt(0)
	v_mfma_f32_16x16x32_bf16 v[60:63], v[154:157], v[188:191], v[60:63]
	v_mfma_f32_16x16x32_bf16 v[56:59], v[162:165], v[188:191], v[56:59]
	v_mfma_f32_16x16x32_bf16 v[44:47], v[154:157], v[196:199], v[44:47]
	v_mfma_f32_16x16x32_bf16 v[32:35], v[162:165], v[196:199], v[32:35]
	v_mfma_f32_16x16x32_bf16 v[16:19], v[154:157], v[204:207], v[16:19]
	v_mfma_f32_16x16x32_bf16 v[8:11], v[162:165], v[204:207], v[8:11]
	v_mfma_f32_16x16x32_bf16 v[4:7], v[154:157], v[212:215], v[4:7]
	v_mfma_f32_16x16x32_bf16 v[0:3], v[162:165], v[212:215], v[0:3]
	v_mfma_f32_16x16x32_bf16 v[60:63], v[158:161], v[192:195], v[60:63]
	v_mfma_f32_16x16x32_bf16 v[56:59], v[166:169], v[192:195], v[56:59]
	v_mfma_f32_16x16x32_bf16 v[44:47], v[158:161], v[200:203], v[44:47]
	v_mfma_f32_16x16x32_bf16 v[32:35], v[166:169], v[200:203], v[32:35]
	v_mfma_f32_16x16x32_bf16 v[16:19], v[158:161], v[208:211], v[16:19]
	v_mfma_f32_16x16x32_bf16 v[8:11], v[166:169], v[208:211], v[8:11]
	v_mfma_f32_16x16x32_bf16 v[4:7], v[158:161], v[220:223], v[4:7]
	v_mfma_f32_16x16x32_bf16 v[0:3], v[166:169], v[220:223], v[0:3]
	s_setprio 0
	s_setprio 1
	v_mfma_f32_16x16x32_bf16 v[52:55], v[170:173], v[188:191], v[52:55]
	v_mfma_f32_16x16x32_bf16 v[48:51], v[178:181], v[188:191], v[48:51]
	v_mfma_f32_16x16x32_bf16 v[28:31], v[170:173], v[196:199], v[28:31]
	v_mfma_f32_16x16x32_bf16 v[12:15], v[178:181], v[196:199], v[12:15]
	v_mfma_f32_16x16x32_bf16 v[36:39], v[170:173], v[204:207], v[36:39]
	v_mfma_f32_16x16x32_bf16 v[40:43], v[178:181], v[204:207], v[40:43]
	v_mfma_f32_16x16x32_bf16 v[20:23], v[170:173], v[212:215], v[20:23]
	v_mfma_f32_16x16x32_bf16 v[24:27], v[178:181], v[212:215], v[24:27]
	v_mfma_f32_16x16x32_bf16 v[52:55], v[174:177], v[192:195], v[52:55]
	v_mfma_f32_16x16x32_bf16 v[48:51], v[182:185], v[192:195], v[48:51]
	v_mfma_f32_16x16x32_bf16 v[28:31], v[174:177], v[200:203], v[28:31]
	v_mfma_f32_16x16x32_bf16 v[12:15], v[182:185], v[200:203], v[12:15]
	v_mfma_f32_16x16x32_bf16 v[36:39], v[174:177], v[208:211], v[36:39]
	v_mfma_f32_16x16x32_bf16 v[40:43], v[182:185], v[208:211], v[40:43]
	v_mfma_f32_16x16x32_bf16 v[20:23], v[174:177], v[220:223], v[20:23]
	v_mfma_f32_16x16x32_bf16 v[24:27], v[182:185], v[220:223], v[24:27]
	s_setprio 0
	s_barrier
	s_add_i32 s60, s60, 2
	s_add_u32 s0, s0, 0x100
	s_addc_u32 s1, s1, 0
	s_add_u32 s58, s58, 0x100
	s_addc_u32 s59, s59, 0
	s_cmp_gt_u32 s60, 13
	s_cbranch_scc0 .LBB0_662
	s_and_b64 vcc, exec, s[14:15]
	s_cbranch_vccz .LBB0_665
	s_barrier

; #define PG8_STAGE(bufoff, gbase, voff) do { _Pragma("unroll") for (int _i = 0; _i < 2; ++_i) \
;         __builtin_amdgcn_global_load_lds((const __attribute__((address_space(1))) unsigned*)((const __attribute__((address_space(1))) char*)(gbase) + (unsigned)lnd_v((int)(voff)[_i])), (LAS unsigned*)(lds + (bufoff) + ldsw + _i * 8192), 16, 0, 0); } while (0)
; #define PG8_LDA(dst, b, h) do { _Pragma("unroll") for (int m = 0; m < 4; ++m) _Pragma("unroll") for (int k = 0; k < 2; ++k) dst[m][k] = *(const LAS bf16x8*)(lds + PG8_SA(b, h) + aoff + m * 2048 + k * 1024); } while (0)
; #define PG8_LDB(dst, b, h) do { _Pragma("unroll") for (int n = 0; n < 2; ++n) _Pragma("unroll") for (int k = 0; k < 2; ++k) dst[n][k] = *(const LAS bf16x8*)(lds + PG8_SB(b, h) + boff + n * 2048 + k * 1024); } while (0)
; #define PG8_MMA(ai, bj, At, Bt) do { __builtin_amdgcn_s_setprio(1); _Pragma("unroll") for (int m = 0; m < 4; ++m) _Pragma("unroll") for (int n = 0; n < 2; ++n) _Pragma("unroll") for (int k = 0; k < 2; ++k) \
;         acc[ai][bj][m][n] = __builtin_amdgcn_mfma_f32_16x16x32_bf16(Bt[n][k], At[m][k], acc[ai][bj][m][n], 0, 0, 0); __builtin_amdgcn_s_setprio(0); } while (0)
; #define PG8_WAIT_V(n) asm volatile("s_waitcnt vmcnt(" #n ")" ::: "memory")
; #define PG8_WAIT_L(n) asm volatile("s_waitcnt lgkmcnt(" #n ")" ::: "memory")
; #define PG8_BAR __builtin_amdgcn_s_barrier()
; #define PG8_SCHED __builtin_amdgcn_sched_barrier(0)
; template <class Desc, class Epi>
; __device__ __forceinline__ void gemm_phase(const int wv_, LAS unsigned char* lds, const Desc& d, const Epi& E) {
;     ...
;             PG8_LDB(B0, 0, 0); PG8_LDB(B1, 0, 1); PG8_SCHED; PG8_LDA(At, 0, 0); PG8_STAGE(PG8_SA(1, 1), a1, voffA1);
;             PG8_WAIT_V(8); PG8_WAIT_L(0); PG8_BAR; PG8_MMA(0, 0, At, B0); PG8_MMA(0, 1, At, B1); PG8_BAR; PG8_SCHED;
;             PG8_LDA(At, 0, 1); PG8_STAGE(PG8_SB(0, 0), b2, voffB); PG8_STAGE(PG8_SB(0, 1), b2 + hstepB, voffB); PG8_STAGE(PG8_SA(0, 0), a2, sA0);
.LBB0_747:
	s_add_u32 s4, s2, 0x80
	s_addc_u32 s5, s3, 0
	s_add_i32 s63, 0, 0x10000
	s_cmp_eq_u32 s45, 12
	s_cselect_b32 s5, s47, s5
	s_cselect_b32 s4, s46, s4
	v_add_u32_e32 v96, s63, v139
	s_cselect_b32 s21, s49, s43
	s_cselect_b32 s20, s48, s29
	s_add_i32 s66, 0, 0x14000
	ds_read_b128 v[150:153], v96
	ds_read_b128 v[154:157], v96 offset:1024
	ds_read_b128 v[158:161], v96 offset:2048
	ds_read_b128 v[162:165], v96 offset:3072
	v_add_u32_e32 v96, s66, v139
	ds_read_b128 v[166:169], v96
	ds_read_b128 v[170:173], v96 offset:1024
	ds_read_b128 v[174:177], v96 offset:2048
	ds_read_b128 v[178:181], v96 offset:3072
	v_mov_b32_e32 v96, v133
	ds_read_b128 v[184:187], v149
	ds_read_b128 v[188:191], v149 offset:1024
	ds_read_b128 v[192:195], v149 offset:2048
	ds_read_b128 v[196:199], v149 offset:3072
	ds_read_b128 v[200:203], v149 offset:4096
	ds_read_b128 v[204:207], v149 offset:5120
	ds_read_b128 v[208:211], v149 offset:6144
	ds_read_b128 v[212:215], v149 offset:7168
	s_add_i32 m0, s55, 0xc000
	s_nop 0
	global_load_lds_dwordx4 v96, s[2:3]
	v_mov_b32_e32 v96, v136
	s_add_i32 m0, s55, 0xe000
	s_nop 0
	global_load_lds_dwordx4 v96, s[2:3]
	s_waitcnt vmcnt(8)
	s_waitcnt lgkmcnt(0)
	s_barrier
	s_setprio 1
	s_waitcnt lgkmcnt(0)
	v_mfma_f32_16x16x32_bf16 v[126:129], v[150:153], v[184:187], v[126:129]
	v_mfma_f32_16x16x32_bf16 v[122:125], v[158:161], v[184:187], v[122:125]
	v_mfma_f32_16x16x32_bf16 v[110:113], v[150:153], v[192:195], v[110:113]
	v_mfma_f32_16x16x32_bf16 v[106:109], v[158:161], v[192:195], v[106:109]
	v_mfma_f32_16x16x32_bf16 v[92:95], v[150:153], v[200:203], v[92:95]
	v_mfma_f32_16x16x32_bf16 v[88:91], v[158:161], v[200:203], v[88:91]
	v_mfma_f32_16x16x32_bf16 v[76:79], v[150:153], v[208:211], v[76:79]
	v_mfma_f32_16x16x32_bf16 v[72:75], v[158:161], v[208:211], v[72:75]
	v_mfma_f32_16x16x32_bf16 v[126:129], v[154:157], v[188:191], v[126:129]
	v_mfma_f32_16x16x32_bf16 v[122:125], v[162:165], v[188:191], v[122:125]
	v_mfma_f32_16x16x32_bf16 v[110:113], v[154:157], v[196:199], v[110:113]
	v_mfma_f32_16x16x32_bf16 v[106:109], v[162:165], v[196:199], v[106:109]
	v_mfma_f32_16x16x32_bf16 v[92:95], v[154:157], v[204:207], v[92:95]
	v_mfma_f32_16x16x32_bf16 v[88:91], v[162:165], v[204:207], v[88:91]
	v_mfma_f32_16x16x32_bf16 v[76:79], v[154:157], v[212:215], v[76:79]
	v_mfma_f32_16x16x32_bf16 v[72:75], v[162:165], v[212:215], v[72:75]
	s_setprio 0
	s_setprio 1
	v_mfma_f32_16x16x32_bf16 v[118:121], v[166:169], v[184:187], v[118:121]
	v_mfma_f32_16x16x32_bf16 v[114:117], v[174:177], v[184:187], v[114:117]
	v_mfma_f32_16x16x32_bf16 v[102:105], v[166:169], v[192:195], v[102:105]
	v_mfma_f32_16x16x32_bf16 v[98:101], v[174:177], v[192:195], v[98:101]
	v_mfma_f32_16x16x32_bf16 v[84:87], v[166:169], v[200:203], v[84:87]
	v_mfma_f32_16x16x32_bf16 v[80:83], v[174:177], v[200:203], v[80:83]
	v_mfma_f32_16x16x32_bf16 v[68:71], v[166:169], v[208:211], v[68:71]
	v_mfma_f32_16x16x32_bf16 v[64:67], v[174:177], v[208:211], v[64:67]
	v_mfma_f32_16x16x32_bf16 v[118:121], v[170:173], v[188:191], v[118:121]
	v_mfma_f32_16x16x32_bf16 v[114:117], v[178:181], v[188:191], v[114:117]
	v_mfma_f32_16x16x32_bf16 v[102:105], v[170:173], v[196:199], v[102:105]
	v_mfma_f32_16x16x32_bf16 v[98:101], v[178:181], v[196:199], v[98:101]
	v_mfma_f32_16x16x32_bf16 v[84:87], v[170:173], v[204:207], v[84:87]
	v_mfma_f32_16x16x32_bf16 v[80:83], v[178:181], v[204:207], v[80:83]
	v_mfma_f32_16x16x32_bf16 v[68:71], v[170:173], v[212:215], v[68:71]
	v_mfma_f32_16x16x32_bf16 v[64:67], v[178:181], v[212:215], v[64:67]
	s_setprio 0
	s_barrier
	v_mov_b32_e32 v96, v134
	s_add_i32 s63, s63, s54
	ds_read_b128 v[184:187], v149 offset:16384
	ds_read_b128 v[188:191], v149 offset:17408
	ds_read_b128 v[192:195], v149 offset:18432
	ds_read_b128 v[196:199], v149 offset:19456
	ds_read_b128 v[200:203], v149 offset:20480
	ds_read_b128 v[204:207], v149 offset:21504
	ds_read_b128 v[208:211], v149 offset:22528
	ds_read_b128 v[212:215], v149 offset:23552
	s_mov_b32 m0, s63
	s_nop 0
	global_load_lds_dwordx4 v96, s[20:21]
	v_mov_b32_e32 v96, v137
	s_add_i32 m0, s63, 0x2000
	s_add_u32 s64, s20, 0x40000
	global_load_lds_dwordx4 v96, s[20:21]
	s_addc_u32 s65, s21, 0
	v_mov_b32_e32 v96, v134
	s_add_i32 s63, s66, s54
	s_mov_b32 m0, s63
	s_nop 0
	global_load_lds_dwordx4 v96, s[64:65]
	v_mov_b32_e32 v96, v137
	s_add_i32 m0, s63, 0x2000
	s_nop 0
	global_load_lds_dwordx4 v96, s[64:65]
	v_mov_b32_e32 v96, v132
	s_mov_b32 m0, s55
	s_nop 0
	global_load_lds_dwordx4 v96, s[4:5]
	v_mov_b32_e32 v96, v135
	s_mov_b32 m0, s56
	s_nop 0
	global_load_lds_dwordx4 v96, s[4:5]
	s_waitcnt vmcnt(8)
	s_waitcnt lgkmcnt(0)
	s_barrier
; #define PG8_STAGE(bufoff, gbase, voff) do { _Pragma("unroll") for (int _i = 0; _i < 2; ++_i) \
;         __builtin_amdgcn_global_load_lds((const __attribute__((address_space(1))) unsigned*)((const __attribute__((address_space(1))) char*)(gbase) + (unsigned)lnd_v((int)(voff)[_i])), (LAS unsigned*)(lds + (bufoff) + ldsw + _i * 8192), 16, 0, 0); } while (0)
; #define PG8_LDA(dst, b, h) do { _Pragma("unroll") for (int m = 0; m < 4; ++m) _Pragma("unroll") for (int k = 0; k < 2; ++k) dst[m][k] = *(const LAS bf16x8*)(lds + PG8_SA(b, h) + aoff + m * 2048 + k * 1024); } while (0)
; #define PG8_LDB(dst, b, h) do { _Pragma("unroll") for (int n = 0; n < 2; ++n) _Pragma("unroll") for (int k = 0; k < 2; ++k) dst[n][k] = *(const LAS bf16x8*)(lds + PG8_SB(b, h) + boff + n * 2048 + k * 1024); } while (0)
; #define PG8_MMA(ai, bj, At, Bt) do { __builtin_amdgcn_s_setprio(1); _Pragma("unroll") for (int m = 0; m < 4; ++m) _Pragma("unroll") for (int n = 0; n < 2; ++n) _Pragma("unroll") for (int k = 0; k < 2; ++k) \
;         acc[ai][bj][m][n] = __builtin_amdgcn_mfma_f32_16x16x32_bf16(Bt[n][k], At[m][k], acc[ai][bj][m][n], 0, 0, 0); __builtin_amdgcn_s_setprio(0); } while (0)
; #define PG8_WAIT_V(n) asm volatile("s_waitcnt vmcnt(" #n ")" ::: "memory")
; #define PG8_WAIT_L(n) asm volatile("s_waitcnt lgkmcnt(" #n ")" ::: "memory")
; #define PG8_BAR __builtin_amdgcn_s_barrier()
; #define PG8_SCHED __builtin_amdgcn_sched_barrier(0)
; template <class Desc, class Epi>
; __device__ __forceinline__ void gemm_phase(const int wv_, LAS unsigned char* lds, const Desc& d, const Epi& E) {
;     ...
;             PG8_WAIT_V(8); PG8_WAIT_L(0); PG8_BAR; PG8_MMA(1, 0, At, B0); PG8_MMA(1, 1, At, B1); PG8_BAR; PG8_SCHED;
;             PG8_LDB(B0, 1, 0); PG8_LDB(B1, 1, 1); PG8_SCHED; PG8_LDA(At, 1, 0); PG8_STAGE(PG8_SA(0, 1), a2, sA1);
;             PG8_WAIT_V(8); PG8_WAIT_L(0); PG8_BAR; PG8_MMA(0, 0, At, B0); PG8_MMA(0, 1, At, B1); PG8_BAR; PG8_SCHED;
	s_setprio 1
	s_waitcnt lgkmcnt(0)
	v_mfma_f32_16x16x32_bf16 v[60:63], v[150:153], v[184:187], v[60:63]
	v_mfma_f32_16x16x32_bf16 v[56:59], v[158:161], v[184:187], v[56:59]
	v_mfma_f32_16x16x32_bf16 v[44:47], v[150:153], v[192:195], v[44:47]
	v_mfma_f32_16x16x32_bf16 v[32:35], v[158:161], v[192:195], v[32:35]
	v_mfma_f32_16x16x32_bf16 v[16:19], v[150:153], v[200:203], v[16:19]
	v_mfma_f32_16x16x32_bf16 v[8:11], v[158:161], v[200:203], v[8:11]
	v_mfma_f32_16x16x32_bf16 v[4:7], v[150:153], v[208:211], v[4:7]
	v_mfma_f32_16x16x32_bf16 v[0:3], v[158:161], v[208:211], v[0:3]
	v_mfma_f32_16x16x32_bf16 v[60:63], v[154:157], v[188:191], v[60:63]
	v_mfma_f32_16x16x32_bf16 v[56:59], v[162:165], v[188:191], v[56:59]
	v_mfma_f32_16x16x32_bf16 v[44:47], v[154:157], v[196:199], v[44:47]
	v_mfma_f32_16x16x32_bf16 v[32:35], v[162:165], v[196:199], v[32:35]
	v_mfma_f32_16x16x32_bf16 v[16:19], v[154:157], v[204:207], v[16:19]
	v_mfma_f32_16x16x32_bf16 v[8:11], v[162:165], v[204:207], v[8:11]
	v_mfma_f32_16x16x32_bf16 v[4:7], v[154:157], v[212:215], v[4:7]
	v_mfma_f32_16x16x32_bf16 v[0:3], v[162:165], v[212:215], v[0:3]
	s_setprio 0
	s_setprio 1
	v_mfma_f32_16x16x32_bf16 v[52:55], v[166:169], v[184:187], v[52:55]
	v_mfma_f32_16x16x32_bf16 v[48:51], v[174:177], v[184:187], v[48:51]
	v_mfma_f32_16x16x32_bf16 v[28:31], v[166:169], v[192:195], v[28:31]
	v_mfma_f32_16x16x32_bf16 v[12:15], v[174:177], v[192:195], v[12:15]
	v_mfma_f32_16x16x32_bf16 v[36:39], v[166:169], v[200:203], v[36:39]
	v_mfma_f32_16x16x32_bf16 v[40:43], v[174:177], v[200:203], v[40:43]
	v_mfma_f32_16x16x32_bf16 v[20:23], v[166:169], v[208:211], v[20:23]
	v_mfma_f32_16x16x32_bf16 v[24:27], v[174:177], v[208:211], v[24:27]
	v_mfma_f32_16x16x32_bf16 v[52:55], v[170:173], v[188:191], v[52:55]
	v_mfma_f32_16x16x32_bf16 v[48:51], v[178:181], v[188:191], v[48:51]
	v_mfma_f32_16x16x32_bf16 v[28:31], v[170:173], v[196:199], v[28:31]
	v_mfma_f32_16x16x32_bf16 v[12:15], v[178:181], v[196:199], v[12:15]
	v_mfma_f32_16x16x32_bf16 v[36:39], v[170:173], v[204:207], v[36:39]
	v_mfma_f32_16x16x32_bf16 v[40:43], v[178:181], v[204:207], v[40:43]
	v_mfma_f32_16x16x32_bf16 v[20:23], v[170:173], v[212:215], v[20:23]
	v_mfma_f32_16x16x32_bf16 v[24:27], v[178:181], v[212:215], v[24:27]
	s_setprio 0
	s_barrier
	s_add_i32 s63, 0, 0x18000
	v_add_u32_e32 v96, s63, v139
	s_add_i32 s64, 0, 0x1c000
	ds_read_b128 v[150:153], v96
	ds_read_b128 v[154:157], v96 offset:1024
	ds_read_b128 v[158:161], v96 offset:2048
	ds_read_b128 v[162:165], v96 offset:3072
	v_add_u32_e32 v96, s64, v139
	ds_read_b128 v[166:169], v96
	ds_read_b128 v[170:173], v96 offset:1024
	ds_read_b128 v[174:177], v96 offset:2048
	ds_read_b128 v[178:181], v96 offset:3072
	v_mov_b32_e32 v96, v133
	s_mov_b32 m0, s57
	ds_read_b128 v[184:187], v149 offset:32768
	ds_read_b128 v[188:191], v149 offset:33792
	ds_read_b128 v[192:195], v149 offset:34816
	ds_read_b128 v[196:199], v149 offset:35840
	ds_read_b128 v[200:203], v149 offset:36864
	ds_read_b128 v[204:207], v149 offset:37888
	ds_read_b128 v[208:211], v149 offset:38912
	ds_read_b128 v[212:215], v149 offset:39936
	s_nop 0
	global_load_lds_dwordx4 v96, s[4:5]
	v_mov_b32_e32 v96, v136
	s_mov_b32 m0, s58
	s_nop 0
	global_load_lds_dwordx4 v96, s[4:5]
	s_waitcnt vmcnt(8)
	s_waitcnt lgkmcnt(0)
	s_barrier
	s_setprio 1
	s_waitcnt lgkmcnt(0)
	v_mfma_f32_16x16x32_bf16 v[126:129], v[150:153], v[184:187], v[126:129]
	v_mfma_f32_16x16x32_bf16 v[122:125], v[158:161], v[184:187], v[122:125]
	v_mfma_f32_16x16x32_bf16 v[110:113], v[150:153], v[192:195], v[110:113]
	v_mfma_f32_16x16x32_bf16 v[106:109], v[158:161], v[192:195], v[106:109]
	v_mfma_f32_16x16x32_bf16 v[92:95], v[150:153], v[200:203], v[92:95]
	v_mfma_f32_16x16x32_bf16 v[88:91], v[158:161], v[200:203], v[88:91]
	v_mfma_f32_16x16x32_bf16 v[76:79], v[150:153], v[208:211], v[76:79]
	v_mfma_f32_16x16x32_bf16 v[72:75], v[158:161], v[208:211], v[72:75]
	v_mfma_f32_16x16x32_bf16 v[126:129], v[154:157], v[188:191], v[126:129]
	v_mfma_f32_16x16x32_bf16 v[122:125], v[162:165], v[188:191], v[122:125]
	v_mfma_f32_16x16x32_bf16 v[110:113], v[154:157], v[196:199], v[110:113]
	v_mfma_f32_16x16x32_bf16 v[106:109], v[162:165], v[196:199], v[106:109]
	v_mfma_f32_16x16x32_bf16 v[92:95], v[154:157], v[204:207], v[92:95]
	v_mfma_f32_16x16x32_bf16 v[88:91], v[162:165], v[204:207], v[88:91]
	v_mfma_f32_16x16x32_bf16 v[76:79], v[154:157], v[212:215], v[76:79]
	v_mfma_f32_16x16x32_bf16 v[72:75], v[162:165], v[212:215], v[72:75]
	s_setprio 0
	s_setprio 1
	v_mfma_f32_16x16x32_bf16 v[118:121], v[166:169], v[184:187], v[118:121]
	v_mfma_f32_16x16x32_bf16 v[114:117], v[174:177], v[184:187], v[114:117]
	v_mfma_f32_16x16x32_bf16 v[102:105], v[166:169], v[192:195], v[102:105]
	v_mfma_f32_16x16x32_bf16 v[98:101], v[174:177], v[192:195], v[98:101]
	v_mfma_f32_16x16x32_bf16 v[84:87], v[166:169], v[200:203], v[84:87]
	v_mfma_f32_16x16x32_bf16 v[80:83], v[174:177], v[200:203], v[80:83]
	v_mfma_f32_16x16x32_bf16 v[68:71], v[166:169], v[208:211], v[68:71]
	v_mfma_f32_16x16x32_bf16 v[64:67], v[174:177], v[208:211], v[64:67]
	v_mfma_f32_16x16x32_bf16 v[118:121], v[170:173], v[188:191], v[118:121]
	v_mfma_f32_16x16x32_bf16 v[114:117], v[178:181], v[188:191], v[114:117]
	v_mfma_f32_16x16x32_bf16 v[102:105], v[170:173], v[196:199], v[102:105]
	v_mfma_f32_16x16x32_bf16 v[98:101], v[178:181], v[196:199], v[98:101]
	v_mfma_f32_16x16x32_bf16 v[84:87], v[170:173], v[204:207], v[84:87]
	v_mfma_f32_16x16x32_bf16 v[80:83], v[178:181], v[204:207], v[80:83]
	v_mfma_f32_16x16x32_bf16 v[68:71], v[170:173], v[212:215], v[68:71]
	v_mfma_f32_16x16x32_bf16 v[64:67], v[178:181], v[212:215], v[64:67]
	s_setprio 0
	s_barrier
; #define PG8_STAGE(bufoff, gbase, voff) do { _Pragma("unroll") for (int _i = 0; _i < 2; ++_i) \
;         __builtin_amdgcn_global_load_lds((const __attribute__((address_space(1))) unsigned*)((const __attribute__((address_space(1))) char*)(gbase) + (unsigned)lnd_v((int)(voff)[_i])), (LAS unsigned*)(lds + (bufoff) + ldsw + _i * 8192), 16, 0, 0); } while (0)
; #define PG8_LDA(dst, b, h) do { _Pragma("unroll") for (int m = 0; m < 4; ++m) _Pragma("unroll") for (int k = 0; k < 2; ++k) dst[m][k] = *(const LAS bf16x8*)(lds + PG8_SA(b, h) + aoff + m * 2048 + k * 1024); } while (0)
; #define PG8_MMA(ai, bj, At, Bt) do { __builtin_amdgcn_s_setprio(1); _Pragma("unroll") for (int m = 0; m < 4; ++m) _Pragma("unroll") for (int n = 0; n < 2; ++n) _Pragma("unroll") for (int k = 0; k < 2; ++k) \
;         acc[ai][bj][m][n] = __builtin_amdgcn_mfma_f32_16x16x32_bf16(Bt[n][k], At[m][k], acc[ai][bj][m][n], 0, 0, 0); __builtin_amdgcn_s_setprio(0); } while (0)
; #define PG8_WAIT_V(n) asm volatile("s_waitcnt vmcnt(" #n ")" ::: "memory")
; #define PG8_WAIT_L(n) asm volatile("s_waitcnt lgkmcnt(" #n ")" ::: "memory")
; #define PG8_BAR __builtin_amdgcn_s_barrier()
; #define PG8_SCHED __builtin_amdgcn_sched_barrier(0)
; template <class Desc, class Epi>
; __device__ __forceinline__ void gemm_phase(const int wv_, LAS unsigned char* lds, const Desc& d, const Epi& E) {
;     ...
;             PG8_LDA(At, 1, 1); PG8_STAGE(PG8_SB(1, 0), b3, voffB); PG8_STAGE(PG8_SB(1, 1), b3 + hstepB, voffB); PG8_STAGE(PG8_SA(1, 0), a3, sA0);
;             PG8_WAIT_V(8); PG8_WAIT_L(0); PG8_BAR; PG8_MMA(1, 0, At, B0); PG8_MMA(1, 1, At, B1); PG8_BAR; PG8_SCHED;
;         }
	v_mov_b32_e32 v96, v134
	ds_read_b128 v[184:187], v149 offset:49152
	ds_read_b128 v[188:191], v149 offset:50176
	ds_read_b128 v[192:195], v149 offset:51200
	ds_read_b128 v[196:199], v149 offset:52224
	ds_read_b128 v[200:203], v149 offset:53248
	ds_read_b128 v[204:207], v149 offset:54272
	ds_read_b128 v[208:211], v149 offset:55296
	ds_read_b128 v[212:215], v149 offset:56320
	s_add_i32 s63, s63, s54
	v_lshl_add_u64 v[130:131], s[20:21], 0, v[96:97]
	v_lshl_add_u64 v[130:131], v[130:131], 0, s[30:31]
	s_mov_b32 m0, s63
	v_mov_b32_e32 v96, v137
	global_load_lds_dwordx4 v[130:131], off
	s_add_i32 m0, s63, 0x2000
	s_nop 0
	v_lshl_add_u64 v[130:131], s[20:21], 0, v[96:97]
	s_add_u32 s20, s20, 0x40080
	v_lshl_add_u64 v[130:131], v[130:131], 0, s[30:31]
	s_addc_u32 s21, s21, 0
	v_mov_b32_e32 v96, v134
	s_add_i32 s63, s64, s54
	global_load_lds_dwordx4 v[130:131], off
	s_mov_b32 m0, s63
	s_nop 0
	global_load_lds_dwordx4 v96, s[20:21]
	v_mov_b32_e32 v96, v137
	s_add_i32 m0, s63, 0x2000
	s_nop 0
	global_load_lds_dwordx4 v96, s[20:21]
	v_mov_b32_e32 v96, v132
	s_mov_b32 m0, s59
	v_lshl_add_u64 v[130:131], s[4:5], 0, v[96:97]
	v_lshl_add_u64 v[130:131], v[130:131], 0, s[30:31]
	v_mov_b32_e32 v96, v135
	global_load_lds_dwordx4 v[130:131], off
	s_mov_b32 m0, s60
	v_lshl_add_u64 v[130:131], s[4:5], 0, v[96:97]
	v_lshl_add_u64 v[130:131], v[130:131], 0, s[30:31]
	global_load_lds_dwordx4 v[130:131], off
	s_waitcnt vmcnt(8)
	s_waitcnt lgkmcnt(0)
	s_barrier
	s_setprio 1
	s_waitcnt lgkmcnt(0)
	v_mfma_f32_16x16x32_bf16 v[60:63], v[150:153], v[184:187], v[60:63]
	v_mfma_f32_16x16x32_bf16 v[56:59], v[158:161], v[184:187], v[56:59]
	v_mfma_f32_16x16x32_bf16 v[44:47], v[150:153], v[192:195], v[44:47]
	v_mfma_f32_16x16x32_bf16 v[32:35], v[158:161], v[192:195], v[32:35]
	v_mfma_f32_16x16x32_bf16 v[16:19], v[150:153], v[200:203], v[16:19]
	v_mfma_f32_16x16x32_bf16 v[8:11], v[158:161], v[200:203], v[8:11]
	v_mfma_f32_16x16x32_bf16 v[4:7], v[150:153], v[208:211], v[4:7]
	v_mfma_f32_16x16x32_bf16 v[0:3], v[158:161], v[208:211], v[0:3]
	v_mfma_f32_16x16x32_bf16 v[60:63], v[154:157], v[188:191], v[60:63]
	v_mfma_f32_16x16x32_bf16 v[56:59], v[162:165], v[188:191], v[56:59]
	v_mfma_f32_16x16x32_bf16 v[44:47], v[154:157], v[196:199], v[44:47]
	v_mfma_f32_16x16x32_bf16 v[32:35], v[162:165], v[196:199], v[32:35]
	v_mfma_f32_16x16x32_bf16 v[16:19], v[154:157], v[204:207], v[16:19]
	v_mfma_f32_16x16x32_bf16 v[8:11], v[162:165], v[204:207], v[8:11]
	v_mfma_f32_16x16x32_bf16 v[4:7], v[154:157], v[212:215], v[4:7]
	v_mfma_f32_16x16x32_bf16 v[0:3], v[162:165], v[212:215], v[0:3]
	s_setprio 0
	s_setprio 1
	v_mfma_f32_16x16x32_bf16 v[52:55], v[166:169], v[184:187], v[52:55]
	v_mfma_f32_16x16x32_bf16 v[48:51], v[174:177], v[184:187], v[48:51]
	v_mfma_f32_16x16x32_bf16 v[28:31], v[166:169], v[192:195], v[28:31]
	v_mfma_f32_16x16x32_bf16 v[12:15], v[174:177], v[192:195], v[12:15]
	v_mfma_f32_16x16x32_bf16 v[36:39], v[166:169], v[200:203], v[36:39]
	v_mfma_f32_16x16x32_bf16 v[40:43], v[174:177], v[200:203], v[40:43]
	v_mfma_f32_16x16x32_bf16 v[20:23], v[166:169], v[208:211], v[20:23]
	v_mfma_f32_16x16x32_bf16 v[24:27], v[174:177], v[208:211], v[24:27]
	v_mfma_f32_16x16x32_bf16 v[52:55], v[170:173], v[188:191], v[52:55]
	v_mfma_f32_16x16x32_bf16 v[48:51], v[178:181], v[188:191], v[48:51]
	v_mfma_f32_16x16x32_bf16 v[28:31], v[170:173], v[196:199], v[28:31]
	v_mfma_f32_16x16x32_bf16 v[12:15], v[178:181], v[196:199], v[12:15]
	v_mfma_f32_16x16x32_bf16 v[36:39], v[170:173], v[204:207], v[36:39]
	v_mfma_f32_16x16x32_bf16 v[40:43], v[178:181], v[204:207], v[40:43]
	v_mfma_f32_16x16x32_bf16 v[20:23], v[170:173], v[212:215], v[20:23]
	v_mfma_f32_16x16x32_bf16 v[24:27], v[178:181], v[212:215], v[24:27]
	s_setprio 0
	s_barrier
	s_add_i32 s45, s45, 2
	s_add_u32 s2, s2, 0x100
	s_addc_u32 s3, s3, 0
	s_add_u32 s29, s29, 0x100
	s_addc_u32 s43, s43, 0
	s_cmp_gt_u32 s45, 13
	s_cbranch_scc0 .LBB0_747
	s_and_b64 vcc, exec, s[40:41]
	s_cbranch_vccz .LBB0_750
	s_barrier

; #define PG8_AOFF(ord, U, O0, O1) do { _Pragma("unroll") for (int _i = 0; _i < 2; ++_i) { \
;         O0[_i] = d.rowbyte(U, (int)tix[(ord) * 256 + Rr[_i]]) + (unsigned)(Cc[_i] * 2); O1[_i] = d.rowbyte(U, (int)tix[(ord) * 256 + HALF + Rr[_i]]) + (unsigned)(Cc[_i] * 2); } } while (0)
; #define PG8_STAGE(bufoff, gbase, voff) do { _Pragma("unroll") for (int _i = 0; _i < 2; ++_i) \
;         __builtin_amdgcn_global_load_lds((const __attribute__((address_space(1))) unsigned*)((const __attribute__((address_space(1))) char*)(gbase) + (unsigned)lnd_v((int)(voff)[_i])), (LAS unsigned*)(lds + (bufoff) + ldsw + _i * 8192), 16, 0, 0); } while (0)
; #define PG8_BAR __builtin_amdgcn_s_barrier()
; template <class Desc, class Epi>
; __device__ __forceinline__ void gemm_phase(const int wv_, LAS unsigned char* lds, const Desc& d, const Epi& E) {
;     ...
;         const int inext = bid + (ui + 1) * nblk; const bool has_next = inext < d.nunits;
;         if (has_next) d.unit(inext, nxt);
;         if constexpr (Desc::GATHER) { if (has_next) PG8_AOFF(ui + 1, nxt, voffAn, voffAn1); else { voffAn[0] = voffA[0]; voffAn[1] = voffA[1]; voffAn1[0] = voffA1[0]; voffAn1[1] = voffA1[1]; } }
;         const char* nA = has_next ? (const char*)nxt.a : cA; const char* nB = has_next ? (const char*)nxt.b : cB;
;         for (int t = 0; t < nt; t += 2) {
;             const bool last = (t == nt - 2);
;             unsigned sA0[2], sA1[2];
;             if constexpr (Desc::GATHER) { sA0[0] = last ? voffAn[0] : voffA[0]; sA0[1] = last ? voffAn[1] : voffA[1]; sA1[0] = last ? voffAn1[0] : voffA1[0]; sA1[1] = last ? voffAn1[1] : voffA1[1]; }
;             else { sA0[0] = voffA[0]; sA0[1] = voffA[1]; sA1[0] = voffA1[0]; sA1[1] = voffA1[1]; }
;             const char* a1 = cA + (size_t)(t + 1) * kstep;
;             const char* a2 = last ? nA : cA + (size_t)(t + 2) * kstep; const char* b2 = last ? nB : cB + (size_t)(t + 2) * kstep;
;             const char* a3 = a2 + kstep; const char* b3 = b2 + kstep;
;             PG8_LDB(B0, 0, 0); PG8_LDB(B1, 0, 1); PG8_SCHED; PG8_LDA(At, 0, 0); PG8_STAGE(PG8_SA(1, 1), a1, voffA1);
;             PG8_WAIT_V(8); PG8_WAIT_L(0); PG8_BAR; PG8_MMA(0, 0, At, B0); PG8_MMA(0, 1, At, B1); PG8_BAR; PG8_SCHED;
;             PG8_LDA(At, 0, 1); PG8_STAGE(PG8_SB(0, 0), b2, voffB); PG8_STAGE(PG8_SB(0, 1), b2 + hstepB, voffB); PG8_STAGE(PG8_SA(0, 0), a2, sA0);
.LBB0_917:
	s_add_u32 s54, s52, s22
	s_addc_u32 s55, s53, 0
	s_add_u32 s23, s54, 0x100
	s_addc_u32 s24, s55, 0
	s_and_b64 s[4:5], s[20:21], exec
	s_cselect_b32 s4, s44, s23
	s_cselect_b32 s5, s45, s24
	s_add_u32 s22, s50, s22
	s_addc_u32 s23, s51, 0
	s_add_u32 s22, s22, 0x100
	s_addc_u32 s23, s23, 0
	s_add_i32 s80, 0, 0x10000
	s_and_b64 s[20:21], s[20:21], exec
	s_cselect_b32 s21, s47, s23
	s_cselect_b32 s20, s46, s22
	s_add_i32 s23, 0, 0x14000
	v_add_u32_e32 v96, s80, v139
	s_add_i32 s82, s80, s60
	ds_read_b128 v[150:153], v96
	ds_read_b128 v[154:157], v96 offset:1024
	ds_read_b128 v[158:161], v96 offset:2048
	ds_read_b128 v[162:165], v96 offset:3072
	v_add_u32_e32 v96, s23, v139
	s_add_i32 m0, s61, 0xc000
	s_add_i32 s83, s61, 0xe000
	s_add_i32 s78, s82, 0x2000
	ds_read_b128 v[166:169], v96
	ds_read_b128 v[170:173], v96 offset:1024
	ds_read_b128 v[174:177], v96 offset:2048
	ds_read_b128 v[178:181], v96 offset:3072
	s_add_u32 s24, s20, 0x40000
	s_addc_u32 s25, s21, 0
	s_add_i32 s76, 0, 0x18000
	s_add_i32 s79, s23, s60
	s_add_i32 s74, s76, s60
	s_add_i32 s77, s79, 0x2000
	s_add_i32 s75, 0, 0x1c000
	s_add_i32 s29, s74, 0x2000
	s_add_u32 s22, s20, 0x40080
	s_addc_u32 s23, s21, 0
	s_add_i32 s81, s75, s60
	s_add_i32 s80, s81, 0x2000
	v_mov_b32_e32 v96, v133
	ds_read_b128 v[184:187], v149
	ds_read_b128 v[188:191], v149 offset:1024
	ds_read_b128 v[192:195], v149 offset:2048
	ds_read_b128 v[196:199], v149 offset:3072
	ds_read_b128 v[200:203], v149 offset:4096
	ds_read_b128 v[204:207], v149 offset:5120
	ds_read_b128 v[208:211], v149 offset:6144
	ds_read_b128 v[212:215], v149 offset:7168
	s_nop 0
	v_lshl_add_u64 v[130:131], s[54:55], 0, v[96:97]
	v_lshl_add_u64 v[130:131], v[130:131], 0, s[30:31]
	v_mov_b32_e32 v96, v136
	global_load_lds_dwordx4 v[130:131], off
	s_mov_b32 m0, s83
	v_lshl_add_u64 v[130:131], s[54:55], 0, v[96:97]
	v_lshl_add_u64 v[130:131], v[130:131], 0, s[30:31]
	global_load_lds_dwordx4 v[130:131], off
	s_waitcnt vmcnt(8)
	s_waitcnt lgkmcnt(0)
	s_barrier
	s_setprio 1
	s_waitcnt lgkmcnt(0)
	v_mfma_f32_16x16x32_bf16 v[126:129], v[150:153], v[184:187], v[126:129]
	v_mfma_f32_16x16x32_bf16 v[122:125], v[158:161], v[184:187], v[122:125]
	v_mfma_f32_16x16x32_bf16 v[110:113], v[150:153], v[192:195], v[110:113]
	v_mfma_f32_16x16x32_bf16 v[106:109], v[158:161], v[192:195], v[106:109]
	v_mfma_f32_16x16x32_bf16 v[92:95], v[150:153], v[200:203], v[92:95]
	v_mfma_f32_16x16x32_bf16 v[88:91], v[158:161], v[200:203], v[88:91]
	v_mfma_f32_16x16x32_bf16 v[76:79], v[150:153], v[208:211], v[76:79]
	v_mfma_f32_16x16x32_bf16 v[72:75], v[158:161], v[208:211], v[72:75]
	v_mfma_f32_16x16x32_bf16 v[126:129], v[154:157], v[188:191], v[126:129]
	v_mfma_f32_16x16x32_bf16 v[122:125], v[162:165], v[188:191], v[122:125]
	v_mfma_f32_16x16x32_bf16 v[110:113], v[154:157], v[196:199], v[110:113]
	v_mfma_f32_16x16x32_bf16 v[106:109], v[162:165], v[196:199], v[106:109]
	v_mfma_f32_16x16x32_bf16 v[92:95], v[154:157], v[204:207], v[92:95]
	v_mfma_f32_16x16x32_bf16 v[88:91], v[162:165], v[204:207], v[88:91]
	v_mfma_f32_16x16x32_bf16 v[76:79], v[154:157], v[212:215], v[76:79]
	v_mfma_f32_16x16x32_bf16 v[72:75], v[162:165], v[212:215], v[72:75]
	s_setprio 0
	s_setprio 1
	v_mfma_f32_16x16x32_bf16 v[118:121], v[166:169], v[184:187], v[118:121]
	v_mfma_f32_16x16x32_bf16 v[114:117], v[174:177], v[184:187], v[114:117]
	v_mfma_f32_16x16x32_bf16 v[102:105], v[166:169], v[192:195], v[102:105]
	v_mfma_f32_16x16x32_bf16 v[98:101], v[174:177], v[192:195], v[98:101]
	v_mfma_f32_16x16x32_bf16 v[84:87], v[166:169], v[200:203], v[84:87]
	v_mfma_f32_16x16x32_bf16 v[80:83], v[174:177], v[200:203], v[80:83]
	v_mfma_f32_16x16x32_bf16 v[68:71], v[166:169], v[208:211], v[68:71]
	v_mfma_f32_16x16x32_bf16 v[64:67], v[174:177], v[208:211], v[64:67]
	v_mfma_f32_16x16x32_bf16 v[118:121], v[170:173], v[188:191], v[118:121]
	v_mfma_f32_16x16x32_bf16 v[114:117], v[178:181], v[188:191], v[114:117]
	v_mfma_f32_16x16x32_bf16 v[102:105], v[170:173], v[196:199], v[102:105]
	v_mfma_f32_16x16x32_bf16 v[98:101], v[178:181], v[196:199], v[98:101]
	v_mfma_f32_16x16x32_bf16 v[84:87], v[170:173], v[204:207], v[84:87]
	v_mfma_f32_16x16x32_bf16 v[80:83], v[178:181], v[204:207], v[80:83]
	v_mfma_f32_16x16x32_bf16 v[68:71], v[170:173], v[212:215], v[68:71]
	v_mfma_f32_16x16x32_bf16 v[64:67], v[178:181], v[212:215], v[64:67]
	s_setprio 0
	s_barrier
	v_mov_b32_e32 v96, v134
	s_mov_b32 m0, s82
	ds_read_b128 v[184:187], v149 offset:16384
	ds_read_b128 v[188:191], v149 offset:17408
	ds_read_b128 v[192:195], v149 offset:18432
	ds_read_b128 v[196:199], v149 offset:19456
	ds_read_b128 v[200:203], v149 offset:20480
	ds_read_b128 v[204:207], v149 offset:21504
	ds_read_b128 v[208:211], v149 offset:22528
	ds_read_b128 v[212:215], v149 offset:23552
	s_nop 0
	global_load_lds_dwordx4 v96, s[20:21]
	v_mov_b32_e32 v96, v137
	s_mov_b32 m0, s78
	s_nop 0
	global_load_lds_dwordx4 v96, s[20:21]
	v_mov_b32_e32 v96, v134
	s_mov_b32 m0, s79
	s_nop 0
	global_load_lds_dwordx4 v96, s[24:25]
	v_mov_b32_e32 v96, v137
	s_mov_b32 m0, s77
	s_nop 0
	global_load_lds_dwordx4 v96, s[24:25]
	v_mov_b32_e32 v96, v132
	s_mov_b32 m0, s61
	s_nop 0
	global_load_lds_dwordx4 v96, s[4:5]
	v_mov_b32_e32 v96, v135
	s_mov_b32 m0, s63
	s_nop 0
	global_load_lds_dwordx4 v96, s[4:5]
	s_waitcnt vmcnt(8)
	s_waitcnt lgkmcnt(0)
	s_barrier
; #define PG8_STAGE(bufoff, gbase, voff) do { _Pragma("unroll") for (int _i = 0; _i < 2; ++_i) \
;         __builtin_amdgcn_global_load_lds((const __attribute__((address_space(1))) unsigned*)((const __attribute__((address_space(1))) char*)(gbase) + (unsigned)lnd_v((int)(voff)[_i])), (LAS unsigned*)(lds + (bufoff) + ldsw + _i * 8192), 16, 0, 0); } while (0)
; #define PG8_LDA(dst, b, h) do { _Pragma("unroll") for (int m = 0; m < 4; ++m) _Pragma("unroll") for (int k = 0; k < 2; ++k) dst[m][k] = *(const LAS bf16x8*)(lds + PG8_SA(b, h) + aoff + m * 2048 + k * 1024); } while (0)
; #define PG8_LDB(dst, b, h) do { _Pragma("unroll") for (int n = 0; n < 2; ++n) _Pragma("unroll") for (int k = 0; k < 2; ++k) dst[n][k] = *(const LAS bf16x8*)(lds + PG8_SB(b, h) + boff + n * 2048 + k * 1024); } while (0)
; #define PG8_MMA(ai, bj, At, Bt) do { __builtin_amdgcn_s_setprio(1); _Pragma("unroll") for (int m = 0; m < 4; ++m) _Pragma("unroll") for (int n = 0; n < 2; ++n) _Pragma("unroll") for (int k = 0; k < 2; ++k) \
;         acc[ai][bj][m][n] = __builtin_amdgcn_mfma_f32_16x16x32_bf16(Bt[n][k], At[m][k], acc[ai][bj][m][n], 0, 0, 0); __builtin_amdgcn_s_setprio(0); } while (0)
; #define PG8_WAIT_V(n) asm volatile("s_waitcnt vmcnt(" #n ")" ::: "memory")
; #define PG8_WAIT_L(n) asm volatile("s_waitcnt lgkmcnt(" #n ")" ::: "memory")
; #define PG8_BAR __builtin_amdgcn_s_barrier()
; #define PG8_SCHED __builtin_amdgcn_sched_barrier(0)
; template <class Desc, class Epi>
; __device__ __forceinline__ void gemm_phase(const int wv_, LAS unsigned char* lds, const Desc& d, const Epi& E) {
;     ...
;             PG8_WAIT_V(8); PG8_WAIT_L(0); PG8_BAR; PG8_MMA(1, 0, At, B0); PG8_MMA(1, 1, At, B1); PG8_BAR; PG8_SCHED;
;             PG8_LDB(B0, 1, 0); PG8_LDB(B1, 1, 1); PG8_SCHED; PG8_LDA(At, 1, 0); PG8_STAGE(PG8_SA(0, 1), a2, sA1);
;             PG8_WAIT_V(8); PG8_WAIT_L(0); PG8_BAR; PG8_MMA(0, 0, At, B0); PG8_MMA(0, 1, At, B1); PG8_BAR; PG8_SCHED;
	s_setprio 1
	s_waitcnt lgkmcnt(0)
	v_mfma_f32_16x16x32_bf16 v[60:63], v[150:153], v[184:187], v[60:63]
	v_mfma_f32_16x16x32_bf16 v[56:59], v[158:161], v[184:187], v[56:59]
	v_mfma_f32_16x16x32_bf16 v[44:47], v[150:153], v[192:195], v[44:47]
	v_mfma_f32_16x16x32_bf16 v[32:35], v[158:161], v[192:195], v[32:35]
	v_mfma_f32_16x16x32_bf16 v[16:19], v[150:153], v[200:203], v[16:19]
	v_mfma_f32_16x16x32_bf16 v[8:11], v[158:161], v[200:203], v[8:11]
	v_mfma_f32_16x16x32_bf16 v[4:7], v[150:153], v[208:211], v[4:7]
	v_mfma_f32_16x16x32_bf16 v[0:3], v[158:161], v[208:211], v[0:3]
	v_mfma_f32_16x16x32_bf16 v[60:63], v[154:157], v[188:191], v[60:63]
	v_mfma_f32_16x16x32_bf16 v[56:59], v[162:165], v[188:191], v[56:59]
	v_mfma_f32_16x16x32_bf16 v[44:47], v[154:157], v[196:199], v[44:47]
	v_mfma_f32_16x16x32_bf16 v[32:35], v[162:165], v[196:199], v[32:35]
	v_mfma_f32_16x16x32_bf16 v[16:19], v[154:157], v[204:207], v[16:19]
	v_mfma_f32_16x16x32_bf16 v[8:11], v[162:165], v[204:207], v[8:11]
	v_mfma_f32_16x16x32_bf16 v[4:7], v[154:157], v[212:215], v[4:7]
	v_mfma_f32_16x16x32_bf16 v[0:3], v[162:165], v[212:215], v[0:3]
	s_setprio 0
	s_setprio 1
	v_mfma_f32_16x16x32_bf16 v[52:55], v[166:169], v[184:187], v[52:55]
	v_mfma_f32_16x16x32_bf16 v[48:51], v[174:177], v[184:187], v[48:51]
	v_mfma_f32_16x16x32_bf16 v[28:31], v[166:169], v[192:195], v[28:31]
	v_mfma_f32_16x16x32_bf16 v[12:15], v[174:177], v[192:195], v[12:15]
	v_mfma_f32_16x16x32_bf16 v[36:39], v[166:169], v[200:203], v[36:39]
	v_mfma_f32_16x16x32_bf16 v[40:43], v[174:177], v[200:203], v[40:43]
	v_mfma_f32_16x16x32_bf16 v[20:23], v[166:169], v[208:211], v[20:23]
	v_mfma_f32_16x16x32_bf16 v[24:27], v[174:177], v[208:211], v[24:27]
	v_mfma_f32_16x16x32_bf16 v[52:55], v[170:173], v[188:191], v[52:55]
	v_mfma_f32_16x16x32_bf16 v[48:51], v[178:181], v[188:191], v[48:51]
	v_mfma_f32_16x16x32_bf16 v[28:31], v[170:173], v[196:199], v[28:31]
	v_mfma_f32_16x16x32_bf16 v[12:15], v[178:181], v[196:199], v[12:15]
	v_mfma_f32_16x16x32_bf16 v[36:39], v[170:173], v[204:207], v[36:39]
	v_mfma_f32_16x16x32_bf16 v[40:43], v[178:181], v[204:207], v[40:43]
	v_mfma_f32_16x16x32_bf16 v[20:23], v[170:173], v[212:215], v[20:23]
	v_mfma_f32_16x16x32_bf16 v[24:27], v[178:181], v[212:215], v[24:27]
	s_setprio 0
	s_barrier
	v_add_u32_e32 v96, s76, v139
	ds_read_b128 v[150:153], v96
	ds_read_b128 v[154:157], v96 offset:1024
	ds_read_b128 v[158:161], v96 offset:2048
	ds_read_b128 v[162:165], v96 offset:3072
	v_add_u32_e32 v96, s75, v139
	ds_read_b128 v[166:169], v96
	ds_read_b128 v[170:173], v96 offset:1024
	ds_read_b128 v[174:177], v96 offset:2048
	ds_read_b128 v[178:181], v96 offset:3072
	v_mov_b32_e32 v96, v133
	s_mov_b32 m0, s64
	ds_read_b128 v[184:187], v149 offset:32768
	ds_read_b128 v[188:191], v149 offset:33792
	ds_read_b128 v[192:195], v149 offset:34816
	ds_read_b128 v[196:199], v149 offset:35840
	ds_read_b128 v[200:203], v149 offset:36864
	ds_read_b128 v[204:207], v149 offset:37888
	ds_read_b128 v[208:211], v149 offset:38912
	ds_read_b128 v[212:215], v149 offset:39936
	s_nop 0
	global_load_lds_dwordx4 v96, s[4:5]
	v_mov_b32_e32 v96, v136
	s_mov_b32 m0, s65
	s_nop 0
	global_load_lds_dwordx4 v96, s[4:5]
	s_waitcnt vmcnt(8)
	s_waitcnt lgkmcnt(0)
	s_barrier
	s_setprio 1
	s_waitcnt lgkmcnt(0)
	v_mfma_f32_16x16x32_bf16 v[126:129], v[150:153], v[184:187], v[126:129]
	v_mfma_f32_16x16x32_bf16 v[122:125], v[158:161], v[184:187], v[122:125]
	v_mfma_f32_16x16x32_bf16 v[110:113], v[150:153], v[192:195], v[110:113]
	v_mfma_f32_16x16x32_bf16 v[106:109], v[158:161], v[192:195], v[106:109]
	v_mfma_f32_16x16x32_bf16 v[92:95], v[150:153], v[200:203], v[92:95]
	v_mfma_f32_16x16x32_bf16 v[88:91], v[158:161], v[200:203], v[88:91]
	v_mfma_f32_16x16x32_bf16 v[76:79], v[150:153], v[208:211], v[76:79]
	v_mfma_f32_16x16x32_bf16 v[72:75], v[158:161], v[208:211], v[72:75]
	v_mfma_f32_16x16x32_bf16 v[126:129], v[154:157], v[188:191], v[126:129]
	v_mfma_f32_16x16x32_bf16 v[122:125], v[162:165], v[188:191], v[122:125]
	v_mfma_f32_16x16x32_bf16 v[110:113], v[154:157], v[196:199], v[110:113]
	v_mfma_f32_16x16x32_bf16 v[106:109], v[162:165], v[196:199], v[106:109]
	v_mfma_f32_16x16x32_bf16 v[92:95], v[154:157], v[204:207], v[92:95]
	v_mfma_f32_16x16x32_bf16 v[88:91], v[162:165], v[204:207], v[88:91]
	v_mfma_f32_16x16x32_bf16 v[76:79], v[154:157], v[212:215], v[76:79]
	v_mfma_f32_16x16x32_bf16 v[72:75], v[162:165], v[212:215], v[72:75]
	s_setprio 0
	s_setprio 1
	v_mfma_f32_16x16x32_bf16 v[118:121], v[166:169], v[184:187], v[118:121]
	v_mfma_f32_16x16x32_bf16 v[114:117], v[174:177], v[184:187], v[114:117]
	v_mfma_f32_16x16x32_bf16 v[102:105], v[166:169], v[192:195], v[102:105]
	v_mfma_f32_16x16x32_bf16 v[98:101], v[174:177], v[192:195], v[98:101]
	v_mfma_f32_16x16x32_bf16 v[84:87], v[166:169], v[200:203], v[84:87]
	v_mfma_f32_16x16x32_bf16 v[80:83], v[174:177], v[200:203], v[80:83]
	v_mfma_f32_16x16x32_bf16 v[68:71], v[166:169], v[208:211], v[68:71]
	v_mfma_f32_16x16x32_bf16 v[64:67], v[174:177], v[208:211], v[64:67]
	v_mfma_f32_16x16x32_bf16 v[118:121], v[170:173], v[188:191], v[118:121]
	v_mfma_f32_16x16x32_bf16 v[114:117], v[178:181], v[188:191], v[114:117]
	v_mfma_f32_16x16x32_bf16 v[102:105], v[170:173], v[196:199], v[102:105]
	v_mfma_f32_16x16x32_bf16 v[98:101], v[178:181], v[196:199], v[98:101]
	v_mfma_f32_16x16x32_bf16 v[84:87], v[170:173], v[204:207], v[84:87]
	v_mfma_f32_16x16x32_bf16 v[80:83], v[178:181], v[204:207], v[80:83]
	v_mfma_f32_16x16x32_bf16 v[68:71], v[170:173], v[212:215], v[68:71]
	v_mfma_f32_16x16x32_bf16 v[64:67], v[178:181], v[212:215], v[64:67]
	s_setprio 0
	s_barrier
; #define PG8_STAGE(bufoff, gbase, voff) do { _Pragma("unroll") for (int _i = 0; _i < 2; ++_i) \
;         __builtin_amdgcn_global_load_lds((const __attribute__((address_space(1))) unsigned*)((const __attribute__((address_space(1))) char*)(gbase) + (unsigned)lnd_v((int)(voff)[_i])), (LAS unsigned*)(lds + (bufoff) + ldsw + _i * 8192), 16, 0, 0); } while (0)
; #define PG8_LDA(dst, b, h) do { _Pragma("unroll") for (int m = 0; m < 4; ++m) _Pragma("unroll") for (int k = 0; k < 2; ++k) dst[m][k] = *(const LAS bf16x8*)(lds + PG8_SA(b, h) + aoff + m * 2048 + k * 1024); } while (0)
; #define PG8_MMA(ai, bj, At, Bt) do { __builtin_amdgcn_s_setprio(1); _Pragma("unroll") for (int m = 0; m < 4; ++m) _Pragma("unroll") for (int n = 0; n < 2; ++n) _Pragma("unroll") for (int k = 0; k < 2; ++k) \
;         acc[ai][bj][m][n] = __builtin_amdgcn_mfma_f32_16x16x32_bf16(Bt[n][k], At[m][k], acc[ai][bj][m][n], 0, 0, 0); __builtin_amdgcn_s_setprio(0); } while (0)
; #define PG8_WAIT_V(n) asm volatile("s_waitcnt vmcnt(" #n ")" ::: "memory")
; #define PG8_WAIT_L(n) asm volatile("s_waitcnt lgkmcnt(" #n ")" ::: "memory")
; #define PG8_BAR __builtin_amdgcn_s_barrier()
; #define PG8_SCHED __builtin_amdgcn_sched_barrier(0)
; template <class Desc, class Epi>
; __device__ __forceinline__ void gemm_phase(const int wv_, LAS unsigned char* lds, const Desc& d, const Epi& E) {
;     ...
;             PG8_LDA(At, 1, 1); PG8_STAGE(PG8_SB(1, 0), b3, voffB); PG8_STAGE(PG8_SB(1, 1), b3 + hstepB, voffB); PG8_STAGE(PG8_SA(1, 0), a3, sA0);
;             PG8_WAIT_V(8); PG8_WAIT_L(0); PG8_BAR; PG8_MMA(1, 0, At, B0); PG8_MMA(1, 1, At, B1); PG8_BAR; PG8_SCHED;
;         }
;         if (wr == 0) PG8_BAR;
	v_mov_b32_e32 v96, v134
	ds_read_b128 v[184:187], v149 offset:49152
	ds_read_b128 v[188:191], v149 offset:50176
	ds_read_b128 v[192:195], v149 offset:51200
	ds_read_b128 v[196:199], v149 offset:52224
	ds_read_b128 v[200:203], v149 offset:53248
	ds_read_b128 v[204:207], v149 offset:54272
	ds_read_b128 v[208:211], v149 offset:55296
	ds_read_b128 v[212:215], v149 offset:56320
	s_mov_b32 m0, s74
	v_lshl_add_u64 v[130:131], s[20:21], 0, v[96:97]
	v_lshl_add_u64 v[130:131], v[130:131], 0, s[30:31]
	v_mov_b32_e32 v96, v137
	global_load_lds_dwordx4 v[130:131], off
	s_mov_b32 m0, s29
	v_lshl_add_u64 v[130:131], s[20:21], 0, v[96:97]
	v_lshl_add_u64 v[130:131], v[130:131], 0, s[30:31]
	v_mov_b32_e32 v96, v134
	global_load_lds_dwordx4 v[130:131], off
	s_mov_b32 m0, s81
	s_nop 0
	global_load_lds_dwordx4 v96, s[22:23]
	v_mov_b32_e32 v96, v137
	s_mov_b32 m0, s80
	s_nop 0
	global_load_lds_dwordx4 v96, s[22:23]
	v_mov_b32_e32 v96, v132
	s_mov_b32 m0, s68
	v_lshl_add_u64 v[130:131], s[4:5], 0, v[96:97]
	v_lshl_add_u64 v[130:131], v[130:131], 0, s[30:31]
	v_mov_b32_e32 v96, v135
	global_load_lds_dwordx4 v[130:131], off
	s_mov_b32 m0, s69
	v_lshl_add_u64 v[130:131], s[4:5], 0, v[96:97]
	v_lshl_add_u64 v[130:131], v[130:131], 0, s[30:31]
	global_load_lds_dwordx4 v[130:131], off
	s_waitcnt vmcnt(8)
	s_waitcnt lgkmcnt(0)
	s_barrier
	s_setprio 1
	s_waitcnt lgkmcnt(0)
	v_mfma_f32_16x16x32_bf16 v[60:63], v[150:153], v[184:187], v[60:63]
	v_mfma_f32_16x16x32_bf16 v[56:59], v[158:161], v[184:187], v[56:59]
	v_mfma_f32_16x16x32_bf16 v[44:47], v[150:153], v[192:195], v[44:47]
	v_mfma_f32_16x16x32_bf16 v[32:35], v[158:161], v[192:195], v[32:35]
	v_mfma_f32_16x16x32_bf16 v[16:19], v[150:153], v[200:203], v[16:19]
	v_mfma_f32_16x16x32_bf16 v[8:11], v[158:161], v[200:203], v[8:11]
	v_mfma_f32_16x16x32_bf16 v[4:7], v[150:153], v[208:211], v[4:7]
	v_mfma_f32_16x16x32_bf16 v[0:3], v[158:161], v[208:211], v[0:3]
	v_mfma_f32_16x16x32_bf16 v[60:63], v[154:157], v[188:191], v[60:63]
	v_mfma_f32_16x16x32_bf16 v[56:59], v[162:165], v[188:191], v[56:59]
	v_mfma_f32_16x16x32_bf16 v[44:47], v[154:157], v[196:199], v[44:47]
	v_mfma_f32_16x16x32_bf16 v[32:35], v[162:165], v[196:199], v[32:35]
	v_mfma_f32_16x16x32_bf16 v[16:19], v[154:157], v[204:207], v[16:19]
	v_mfma_f32_16x16x32_bf16 v[8:11], v[162:165], v[204:207], v[8:11]
	v_mfma_f32_16x16x32_bf16 v[4:7], v[154:157], v[212:215], v[4:7]
	v_mfma_f32_16x16x32_bf16 v[0:3], v[162:165], v[212:215], v[0:3]
	s_setprio 0
	s_setprio 1
	v_mfma_f32_16x16x32_bf16 v[52:55], v[166:169], v[184:187], v[52:55]
	v_mfma_f32_16x16x32_bf16 v[48:51], v[174:177], v[184:187], v[48:51]
	v_mfma_f32_16x16x32_bf16 v[28:31], v[166:169], v[192:195], v[28:31]
	v_mfma_f32_16x16x32_bf16 v[12:15], v[174:177], v[192:195], v[12:15]
	v_mfma_f32_16x16x32_bf16 v[36:39], v[166:169], v[200:203], v[36:39]
	v_mfma_f32_16x16x32_bf16 v[40:43], v[174:177], v[200:203], v[40:43]
	v_mfma_f32_16x16x32_bf16 v[20:23], v[166:169], v[208:211], v[20:23]
	v_mfma_f32_16x16x32_bf16 v[24:27], v[174:177], v[208:211], v[24:27]
	v_mfma_f32_16x16x32_bf16 v[52:55], v[170:173], v[188:191], v[52:55]
	v_mfma_f32_16x16x32_bf16 v[48:51], v[178:181], v[188:191], v[48:51]
	v_mfma_f32_16x16x32_bf16 v[28:31], v[170:173], v[196:199], v[28:31]
	v_mfma_f32_16x16x32_bf16 v[12:15], v[178:181], v[196:199], v[12:15]
	v_mfma_f32_16x16x32_bf16 v[36:39], v[170:173], v[204:207], v[36:39]
	v_mfma_f32_16x16x32_bf16 v[40:43], v[178:181], v[204:207], v[40:43]
	v_mfma_f32_16x16x32_bf16 v[20:23], v[170:173], v[212:215], v[20:23]
	v_mfma_f32_16x16x32_bf16 v[24:27], v[178:181], v[212:215], v[24:27]
	s_setprio 0
	s_barrier
	s_movk_i32 s22, 0x100
	s_andn2_b64 vcc, exec, s[2:3]
	s_mov_b64 s[20:21], -1
	s_mov_b64 s[2:3], 0
	s_cbranch_vccz .LBB0_917
	s_and_b64 vcc, exec, s[42:43]
	s_cbranch_vccz .LBB0_920
	s_barrier

; #define PG8_AOFF(ord, U, O0, O1) do { _Pragma("unroll") for (int _i = 0; _i < 2; ++_i) { \
;         O0[_i] = d.rowbyte(U, (int)tix[(ord) * 256 + Rr[_i]]) + (unsigned)(Cc[_i] * 2); O1[_i] = d.rowbyte(U, (int)tix[(ord) * 256 + HALF + Rr[_i]]) + (unsigned)(Cc[_i] * 2); } } while (0)
; #define PG8_STAGE(bufoff, gbase, voff) do { _Pragma("unroll") for (int _i = 0; _i < 2; ++_i) \
;         __builtin_amdgcn_global_load_lds((const __attribute__((address_space(1))) unsigned*)((const __attribute__((address_space(1))) char*)(gbase) + (unsigned)lnd_v((int)(voff)[_i])), (LAS unsigned*)(lds + (bufoff) + ldsw + _i * 8192), 16, 0, 0); } while (0)
; #define PG8_BAR __builtin_amdgcn_s_barrier()
; template <class Desc, class Epi>
; __device__ __forceinline__ void gemm_phase(const int wv_, LAS unsigned char* lds, const Desc& d, const Epi& E) {
;     ...
;         const int inext = bid + (ui + 1) * nblk; const bool has_next = inext < d.nunits;
;         if (has_next) d.unit(inext, nxt);
;         if constexpr (Desc::GATHER) { if (has_next) PG8_AOFF(ui + 1, nxt, voffAn, voffAn1); else { voffAn[0] = voffA[0]; voffAn[1] = voffA[1]; voffAn1[0] = voffA1[0]; voffAn1[1] = voffA1[1]; } }
;         const char* nA = has_next ? (const char*)nxt.a : cA; const char* nB = has_next ? (const char*)nxt.b : cB;
;         for (int t = 0; t < nt; t += 2) {
;             const bool last = (t == nt - 2);
;             unsigned sA0[2], sA1[2];
;             if constexpr (Desc::GATHER) { sA0[0] = last ? voffAn[0] : voffA[0]; sA0[1] = last ? voffAn[1] : voffA[1]; sA1[0] = last ? voffAn1[0] : voffA1[0]; sA1[1] = last ? voffAn1[1] : voffA1[1]; }
;             else { sA0[0] = voffA[0]; sA0[1] = voffA[1]; sA1[0] = voffA1[0]; sA1[1] = voffA1[1]; }
;             const char* a1 = cA + (size_t)(t + 1) * kstep;
;             const char* a2 = last ? nA : cA + (size_t)(t + 2) * kstep; const char* b2 = last ? nB : cB + (size_t)(t + 2) * kstep;
;             const char* a3 = a2 + kstep; const char* b3 = b2 + kstep;
;             PG8_LDB(B0, 0, 0); PG8_LDB(B1, 0, 1); PG8_SCHED; PG8_LDA(At, 0, 0); PG8_STAGE(PG8_SA(1, 1), a1, voffA1);
;             PG8_WAIT_V(8); PG8_WAIT_L(0); PG8_BAR; PG8_MMA(0, 0, At, B0); PG8_MMA(0, 1, At, B1); PG8_BAR; PG8_SCHED;
;             PG8_LDA(At, 0, 1); PG8_STAGE(PG8_SB(0, 0), b2, voffB); PG8_STAGE(PG8_SB(0, 1), b2 + hstepB, voffB); PG8_STAGE(PG8_SA(0, 0), a2, sA0);
.LBB0_937:
	s_add_u32 s52, s50, s22
	s_addc_u32 s53, s51, 0
	s_add_u32 s23, s52, 0x100
	s_addc_u32 s24, s53, 0
	s_and_b64 s[4:5], s[20:21], exec
	s_cselect_b32 s4, s42, s23
	s_cselect_b32 s5, s43, s24
	s_add_u32 s22, s48, s22
	s_addc_u32 s23, s49, 0
	s_add_u32 s22, s22, 0x100
	s_addc_u32 s23, s23, 0
	s_add_i32 s77, 0, 0x10000
	s_and_b64 s[20:21], s[20:21], exec
	s_cselect_b32 s21, s45, s23
	s_cselect_b32 s20, s44, s22
	s_add_i32 s23, 0, 0x14000
	v_add_u32_e32 v96, s77, v139
	s_add_i32 s79, s77, s59
	ds_read_b128 v[150:153], v96
	ds_read_b128 v[154:157], v96 offset:1024
	ds_read_b128 v[158:161], v96 offset:2048
	ds_read_b128 v[162:165], v96 offset:3072
	v_add_u32_e32 v96, s23, v139
	s_add_i32 m0, s60, 0xc000
	s_add_i32 s80, s60, 0xe000
	s_add_i32 s75, s79, 0x2000
	ds_read_b128 v[166:169], v96
	ds_read_b128 v[170:173], v96 offset:1024
	ds_read_b128 v[174:177], v96 offset:2048
	ds_read_b128 v[178:181], v96 offset:3072
	s_add_u32 s24, s20, 0x40000
	s_addc_u32 s25, s21, 0
	s_add_i32 s73, 0, 0x18000
	s_add_i32 s76, s23, s59
	s_add_i32 s71, s73, s59
	s_add_i32 s74, s76, 0x2000
	s_add_i32 s72, 0, 0x1c000
	s_add_i32 s29, s71, 0x2000
	s_add_u32 s22, s20, 0x40080
	s_addc_u32 s23, s21, 0
	s_add_i32 s78, s72, s59
	s_add_i32 s77, s78, 0x2000
	v_mov_b32_e32 v96, v133
	ds_read_b128 v[184:187], v149
	ds_read_b128 v[188:191], v149 offset:1024
	ds_read_b128 v[192:195], v149 offset:2048
	ds_read_b128 v[196:199], v149 offset:3072
	ds_read_b128 v[200:203], v149 offset:4096
	ds_read_b128 v[204:207], v149 offset:5120
	ds_read_b128 v[208:211], v149 offset:6144
	ds_read_b128 v[212:215], v149 offset:7168
	s_nop 0
	v_lshl_add_u64 v[130:131], s[52:53], 0, v[96:97]
	v_lshl_add_u64 v[130:131], v[130:131], 0, s[30:31]
	v_mov_b32_e32 v96, v136
	global_load_lds_dwordx4 v[130:131], off
	s_mov_b32 m0, s80
	v_lshl_add_u64 v[130:131], s[52:53], 0, v[96:97]
	v_lshl_add_u64 v[130:131], v[130:131], 0, s[30:31]
	global_load_lds_dwordx4 v[130:131], off
	s_waitcnt vmcnt(8)
	s_waitcnt lgkmcnt(0)
	s_barrier
	s_setprio 1
	s_waitcnt lgkmcnt(0)
	v_mfma_f32_16x16x32_bf16 v[126:129], v[150:153], v[184:187], v[126:129]
	v_mfma_f32_16x16x32_bf16 v[122:125], v[158:161], v[184:187], v[122:125]
	v_mfma_f32_16x16x32_bf16 v[110:113], v[150:153], v[192:195], v[110:113]
	v_mfma_f32_16x16x32_bf16 v[106:109], v[158:161], v[192:195], v[106:109]
	v_mfma_f32_16x16x32_bf16 v[92:95], v[150:153], v[200:203], v[92:95]
	v_mfma_f32_16x16x32_bf16 v[88:91], v[158:161], v[200:203], v[88:91]
	v_mfma_f32_16x16x32_bf16 v[76:79], v[150:153], v[208:211], v[76:79]
	v_mfma_f32_16x16x32_bf16 v[72:75], v[158:161], v[208:211], v[72:75]
	v_mfma_f32_16x16x32_bf16 v[126:129], v[154:157], v[188:191], v[126:129]
	v_mfma_f32_16x16x32_bf16 v[122:125], v[162:165], v[188:191], v[122:125]
	v_mfma_f32_16x16x32_bf16 v[110:113], v[154:157], v[196:199], v[110:113]
	v_mfma_f32_16x16x32_bf16 v[106:109], v[162:165], v[196:199], v[106:109]
	v_mfma_f32_16x16x32_bf16 v[92:95], v[154:157], v[204:207], v[92:95]
	v_mfma_f32_16x16x32_bf16 v[88:91], v[162:165], v[204:207], v[88:91]
	v_mfma_f32_16x16x32_bf16 v[76:79], v[154:157], v[212:215], v[76:79]
	v_mfma_f32_16x16x32_bf16 v[72:75], v[162:165], v[212:215], v[72:75]
	s_setprio 0
	s_setprio 1
	v_mfma_f32_16x16x32_bf16 v[118:121], v[166:169], v[184:187], v[118:121]
	v_mfma_f32_16x16x32_bf16 v[114:117], v[174:177], v[184:187], v[114:117]
	v_mfma_f32_16x16x32_bf16 v[102:105], v[166:169], v[192:195], v[102:105]
	v_mfma_f32_16x16x32_bf16 v[98:101], v[174:177], v[192:195], v[98:101]
	v_mfma_f32_16x16x32_bf16 v[84:87], v[166:169], v[200:203], v[84:87]
	v_mfma_f32_16x16x32_bf16 v[80:83], v[174:177], v[200:203], v[80:83]
	v_mfma_f32_16x16x32_bf16 v[68:71], v[166:169], v[208:211], v[68:71]
	v_mfma_f32_16x16x32_bf16 v[64:67], v[174:177], v[208:211], v[64:67]
	v_mfma_f32_16x16x32_bf16 v[118:121], v[170:173], v[188:191], v[118:121]
	v_mfma_f32_16x16x32_bf16 v[114:117], v[178:181], v[188:191], v[114:117]
	v_mfma_f32_16x16x32_bf16 v[102:105], v[170:173], v[196:199], v[102:105]
	v_mfma_f32_16x16x32_bf16 v[98:101], v[178:181], v[196:199], v[98:101]
	v_mfma_f32_16x16x32_bf16 v[84:87], v[170:173], v[204:207], v[84:87]
	v_mfma_f32_16x16x32_bf16 v[80:83], v[178:181], v[204:207], v[80:83]
	v_mfma_f32_16x16x32_bf16 v[68:71], v[170:173], v[212:215], v[68:71]
	v_mfma_f32_16x16x32_bf16 v[64:67], v[178:181], v[212:215], v[64:67]
	s_setprio 0
	s_barrier
	v_mov_b32_e32 v96, v134
	s_mov_b32 m0, s79
	ds_read_b128 v[184:187], v149 offset:16384
	ds_read_b128 v[188:191], v149 offset:17408
	ds_read_b128 v[192:195], v149 offset:18432
	ds_read_b128 v[196:199], v149 offset:19456
	ds_read_b128 v[200:203], v149 offset:20480
	ds_read_b128 v[204:207], v149 offset:21504
	ds_read_b128 v[208:211], v149 offset:22528
	ds_read_b128 v[212:215], v149 offset:23552
	s_nop 0
	global_load_lds_dwordx4 v96, s[20:21]
	v_mov_b32_e32 v96, v137
	s_mov_b32 m0, s75
	s_nop 0
	global_load_lds_dwordx4 v96, s[20:21]
	v_mov_b32_e32 v96, v134
	s_mov_b32 m0, s76
	s_nop 0
	global_load_lds_dwordx4 v96, s[24:25]
	v_mov_b32_e32 v96, v137
	s_mov_b32 m0, s74
	s_nop 0
	global_load_lds_dwordx4 v96, s[24:25]
	v_mov_b32_e32 v96, v132
	s_mov_b32 m0, s60
	s_nop 0
	global_load_lds_dwordx4 v96, s[4:5]
	v_mov_b32_e32 v96, v135
	s_mov_b32 m0, s61
	s_nop 0
	global_load_lds_dwordx4 v96, s[4:5]
	s_waitcnt vmcnt(8)
	s_waitcnt lgkmcnt(0)
	s_barrier
; #define PG8_STAGE(bufoff, gbase, voff) do { _Pragma("unroll") for (int _i = 0; _i < 2; ++_i) \
;         __builtin_amdgcn_global_load_lds((const __attribute__((address_space(1))) unsigned*)((const __attribute__((address_space(1))) char*)(gbase) + (unsigned)lnd_v((int)(voff)[_i])), (LAS unsigned*)(lds + (bufoff) + ldsw + _i * 8192), 16, 0, 0); } while (0)
; #define PG8_LDA(dst, b, h) do { _Pragma("unroll") for (int m = 0; m < 4; ++m) _Pragma("unroll") for (int k = 0; k < 2; ++k) dst[m][k] = *(const LAS bf16x8*)(lds + PG8_SA(b, h) + aoff + m * 2048 + k * 1024); } while (0)
; #define PG8_LDB(dst, b, h) do { _Pragma("unroll") for (int n = 0; n < 2; ++n) _Pragma("unroll") for (int k = 0; k < 2; ++k) dst[n][k] = *(const LAS bf16x8*)(lds + PG8_SB(b, h) + boff + n * 2048 + k * 1024); } while (0)
; #define PG8_MMA(ai, bj, At, Bt) do { __builtin_amdgcn_s_setprio(1); _Pragma("unroll") for (int m = 0; m < 4; ++m) _Pragma("unroll") for (int n = 0; n < 2; ++n) _Pragma("unroll") for (int k = 0; k < 2; ++k) \
;         acc[ai][bj][m][n] = __builtin_amdgcn_mfma_f32_16x16x32_bf16(Bt[n][k], At[m][k], acc[ai][bj][m][n], 0, 0, 0); __builtin_amdgcn_s_setprio(0); } while (0)
; #define PG8_WAIT_V(n) asm volatile("s_waitcnt vmcnt(" #n ")" ::: "memory")
; #define PG8_WAIT_L(n) asm volatile("s_waitcnt lgkmcnt(" #n ")" ::: "memory")
; #define PG8_BAR __builtin_amdgcn_s_barrier()
; #define PG8_SCHED __builtin_amdgcn_sched_barrier(0)
; template <class Desc, class Epi>
; __device__ __forceinline__ void gemm_phase(const int wv_, LAS unsigned char* lds, const Desc& d, const Epi& E) {
;     ...
;             PG8_WAIT_V(8); PG8_WAIT_L(0); PG8_BAR; PG8_MMA(1, 0, At, B0); PG8_MMA(1, 1, At, B1); PG8_BAR; PG8_SCHED;
;             PG8_LDB(B0, 1, 0); PG8_LDB(B1, 1, 1); PG8_SCHED; PG8_LDA(At, 1, 0); PG8_STAGE(PG8_SA(0, 1), a2, sA1);
;             PG8_WAIT_V(8); PG8_WAIT_L(0); PG8_BAR; PG8_MMA(0, 0, At, B0); PG8_MMA(0, 1, At, B1); PG8_BAR; PG8_SCHED;
	s_setprio 1
	s_waitcnt lgkmcnt(0)
	v_mfma_f32_16x16x32_bf16 v[60:63], v[150:153], v[184:187], v[60:63]
	v_mfma_f32_16x16x32_bf16 v[56:59], v[158:161], v[184:187], v[56:59]
	v_mfma_f32_16x16x32_bf16 v[44:47], v[150:153], v[192:195], v[44:47]
	v_mfma_f32_16x16x32_bf16 v[32:35], v[158:161], v[192:195], v[32:35]
	v_mfma_f32_16x16x32_bf16 v[16:19], v[150:153], v[200:203], v[16:19]
	v_mfma_f32_16x16x32_bf16 v[8:11], v[158:161], v[200:203], v[8:11]
	v_mfma_f32_16x16x32_bf16 v[4:7], v[150:153], v[208:211], v[4:7]
	v_mfma_f32_16x16x32_bf16 v[0:3], v[158:161], v[208:211], v[0:3]
	v_mfma_f32_16x16x32_bf16 v[60:63], v[154:157], v[188:191], v[60:63]
	v_mfma_f32_16x16x32_bf16 v[56:59], v[162:165], v[188:191], v[56:59]
	v_mfma_f32_16x16x32_bf16 v[44:47], v[154:157], v[196:199], v[44:47]
	v_mfma_f32_16x16x32_bf16 v[32:35], v[162:165], v[196:199], v[32:35]
	v_mfma_f32_16x16x32_bf16 v[16:19], v[154:157], v[204:207], v[16:19]
	v_mfma_f32_16x16x32_bf16 v[8:11], v[162:165], v[204:207], v[8:11]
	v_mfma_f32_16x16x32_bf16 v[4:7], v[154:157], v[212:215], v[4:7]
	v_mfma_f32_16x16x32_bf16 v[0:3], v[162:165], v[212:215], v[0:3]
	s_setprio 0
	s_setprio 1
	v_mfma_f32_16x16x32_bf16 v[52:55], v[166:169], v[184:187], v[52:55]
	v_mfma_f32_16x16x32_bf16 v[48:51], v[174:177], v[184:187], v[48:51]
	v_mfma_f32_16x16x32_bf16 v[28:31], v[166:169], v[192:195], v[28:31]
	v_mfma_f32_16x16x32_bf16 v[12:15], v[174:177], v[192:195], v[12:15]
	v_mfma_f32_16x16x32_bf16 v[36:39], v[166:169], v[200:203], v[36:39]
	v_mfma_f32_16x16x32_bf16 v[40:43], v[174:177], v[200:203], v[40:43]
	v_mfma_f32_16x16x32_bf16 v[20:23], v[166:169], v[208:211], v[20:23]
	v_mfma_f32_16x16x32_bf16 v[24:27], v[174:177], v[208:211], v[24:27]
	v_mfma_f32_16x16x32_bf16 v[52:55], v[170:173], v[188:191], v[52:55]
	v_mfma_f32_16x16x32_bf16 v[48:51], v[178:181], v[188:191], v[48:51]
	v_mfma_f32_16x16x32_bf16 v[28:31], v[170:173], v[196:199], v[28:31]
	v_mfma_f32_16x16x32_bf16 v[12:15], v[178:181], v[196:199], v[12:15]
	v_mfma_f32_16x16x32_bf16 v[36:39], v[170:173], v[204:207], v[36:39]
	v_mfma_f32_16x16x32_bf16 v[40:43], v[178:181], v[204:207], v[40:43]
	v_mfma_f32_16x16x32_bf16 v[20:23], v[170:173], v[212:215], v[20:23]
	v_mfma_f32_16x16x32_bf16 v[24:27], v[178:181], v[212:215], v[24:27]
	s_setprio 0
	s_barrier
	v_add_u32_e32 v96, s73, v139
	ds_read_b128 v[150:153], v96
	ds_read_b128 v[154:157], v96 offset:1024
	ds_read_b128 v[158:161], v96 offset:2048
	ds_read_b128 v[162:165], v96 offset:3072
	v_add_u32_e32 v96, s72, v139
	ds_read_b128 v[166:169], v96
	ds_read_b128 v[170:173], v96 offset:1024
	ds_read_b128 v[174:177], v96 offset:2048
	ds_read_b128 v[178:181], v96 offset:3072
	v_mov_b32_e32 v96, v133
	s_mov_b32 m0, s63
	ds_read_b128 v[184:187], v149 offset:32768
	ds_read_b128 v[188:191], v149 offset:33792
	ds_read_b128 v[192:195], v149 offset:34816
	ds_read_b128 v[196:199], v149 offset:35840
	ds_read_b128 v[200:203], v149 offset:36864
	ds_read_b128 v[204:207], v149 offset:37888
	ds_read_b128 v[208:211], v149 offset:38912
	ds_read_b128 v[212:215], v149 offset:39936
	s_nop 0
	global_load_lds_dwordx4 v96, s[4:5]
	v_mov_b32_e32 v96, v136
	s_mov_b32 m0, s64
	s_nop 0
	global_load_lds_dwordx4 v96, s[4:5]
	s_waitcnt vmcnt(8)
	s_waitcnt lgkmcnt(0)
	s_barrier
	s_setprio 1
	s_waitcnt lgkmcnt(0)
	v_mfma_f32_16x16x32_bf16 v[126:129], v[150:153], v[184:187], v[126:129]
	v_mfma_f32_16x16x32_bf16 v[122:125], v[158:161], v[184:187], v[122:125]
	v_mfma_f32_16x16x32_bf16 v[110:113], v[150:153], v[192:195], v[110:113]
	v_mfma_f32_16x16x32_bf16 v[106:109], v[158:161], v[192:195], v[106:109]
	v_mfma_f32_16x16x32_bf16 v[92:95], v[150:153], v[200:203], v[92:95]
	v_mfma_f32_16x16x32_bf16 v[88:91], v[158:161], v[200:203], v[88:91]
	v_mfma_f32_16x16x32_bf16 v[76:79], v[150:153], v[208:211], v[76:79]
	v_mfma_f32_16x16x32_bf16 v[72:75], v[158:161], v[208:211], v[72:75]
	v_mfma_f32_16x16x32_bf16 v[126:129], v[154:157], v[188:191], v[126:129]
	v_mfma_f32_16x16x32_bf16 v[122:125], v[162:165], v[188:191], v[122:125]
	v_mfma_f32_16x16x32_bf16 v[110:113], v[154:157], v[196:199], v[110:113]
	v_mfma_f32_16x16x32_bf16 v[106:109], v[162:165], v[196:199], v[106:109]
	v_mfma_f32_16x16x32_bf16 v[92:95], v[154:157], v[204:207], v[92:95]
	v_mfma_f32_16x16x32_bf16 v[88:91], v[162:165], v[204:207], v[88:91]
	v_mfma_f32_16x16x32_bf16 v[76:79], v[154:157], v[212:215], v[76:79]
	v_mfma_f32_16x16x32_bf16 v[72:75], v[162:165], v[212:215], v[72:75]
	s_setprio 0
	s_setprio 1
	v_mfma_f32_16x16x32_bf16 v[118:121], v[166:169], v[184:187], v[118:121]
	v_mfma_f32_16x16x32_bf16 v[114:117], v[174:177], v[184:187], v[114:117]
	v_mfma_f32_16x16x32_bf16 v[102:105], v[166:169], v[192:195], v[102:105]
	v_mfma_f32_16x16x32_bf16 v[98:101], v[174:177], v[192:195], v[98:101]
	v_mfma_f32_16x16x32_bf16 v[84:87], v[166:169], v[200:203], v[84:87]
	v_mfma_f32_16x16x32_bf16 v[80:83], v[174:177], v[200:203], v[80:83]
	v_mfma_f32_16x16x32_bf16 v[68:71], v[166:169], v[208:211], v[68:71]
	v_mfma_f32_16x16x32_bf16 v[64:67], v[174:177], v[208:211], v[64:67]
	v_mfma_f32_16x16x32_bf16 v[118:121], v[170:173], v[188:191], v[118:121]
	v_mfma_f32_16x16x32_bf16 v[114:117], v[178:181], v[188:191], v[114:117]
	v_mfma_f32_16x16x32_bf16 v[102:105], v[170:173], v[196:199], v[102:105]
	v_mfma_f32_16x16x32_bf16 v[98:101], v[178:181], v[196:199], v[98:101]
	v_mfma_f32_16x16x32_bf16 v[84:87], v[170:173], v[204:207], v[84:87]
	v_mfma_f32_16x16x32_bf16 v[80:83], v[178:181], v[204:207], v[80:83]
	v_mfma_f32_16x16x32_bf16 v[68:71], v[170:173], v[212:215], v[68:71]
	v_mfma_f32_16x16x32_bf16 v[64:67], v[178:181], v[212:215], v[64:67]
	s_setprio 0
	s_barrier
; #define PG8_STAGE(bufoff, gbase, voff) do { _Pragma("unroll") for (int _i = 0; _i < 2; ++_i) \
;         __builtin_amdgcn_global_load_lds((const __attribute__((address_space(1))) unsigned*)((const __attribute__((address_space(1))) char*)(gbase) + (unsigned)lnd_v((int)(voff)[_i])), (LAS unsigned*)(lds + (bufoff) + ldsw + _i * 8192), 16, 0, 0); } while (0)
; #define PG8_LDA(dst, b, h) do { _Pragma("unroll") for (int m = 0; m < 4; ++m) _Pragma("unroll") for (int k = 0; k < 2; ++k) dst[m][k] = *(const LAS bf16x8*)(lds + PG8_SA(b, h) + aoff + m * 2048 + k * 1024); } while (0)
; #define PG8_MMA(ai, bj, At, Bt) do { __builtin_amdgcn_s_setprio(1); _Pragma("unroll") for (int m = 0; m < 4; ++m) _Pragma("unroll") for (int n = 0; n < 2; ++n) _Pragma("unroll") for (int k = 0; k < 2; ++k) \
;         acc[ai][bj][m][n] = __builtin_amdgcn_mfma_f32_16x16x32_bf16(Bt[n][k], At[m][k], acc[ai][bj][m][n], 0, 0, 0); __builtin_amdgcn_s_setprio(0); } while (0)
; #define PG8_WAIT_V(n) asm volatile("s_waitcnt vmcnt(" #n ")" ::: "memory")
; #define PG8_WAIT_L(n) asm volatile("s_waitcnt lgkmcnt(" #n ")" ::: "memory")
; #define PG8_BAR __builtin_amdgcn_s_barrier()
; #define PG8_SCHED __builtin_amdgcn_sched_barrier(0)
; template <class Desc, class Epi>
; __device__ __forceinline__ void gemm_phase(const int wv_, LAS unsigned char* lds, const Desc& d, const Epi& E) {
;     ...
;             PG8_LDA(At, 1, 1); PG8_STAGE(PG8_SB(1, 0), b3, voffB); PG8_STAGE(PG8_SB(1, 1), b3 + hstepB, voffB); PG8_STAGE(PG8_SA(1, 0), a3, sA0);
;             PG8_WAIT_V(8); PG8_WAIT_L(0); PG8_BAR; PG8_MMA(1, 0, At, B0); PG8_MMA(1, 1, At, B1); PG8_BAR; PG8_SCHED;
;         }
;         if (wr == 0) PG8_BAR;
	v_mov_b32_e32 v96, v134
	ds_read_b128 v[184:187], v149 offset:49152
	ds_read_b128 v[188:191], v149 offset:50176
	ds_read_b128 v[192:195], v149 offset:51200
	ds_read_b128 v[196:199], v149 offset:52224
	ds_read_b128 v[200:203], v149 offset:53248
	ds_read_b128 v[204:207], v149 offset:54272
	ds_read_b128 v[208:211], v149 offset:55296
	ds_read_b128 v[212:215], v149 offset:56320
	s_mov_b32 m0, s71
	v_lshl_add_u64 v[130:131], s[20:21], 0, v[96:97]
	v_lshl_add_u64 v[130:131], v[130:131], 0, s[30:31]
	v_mov_b32_e32 v96, v137
	global_load_lds_dwordx4 v[130:131], off
	s_mov_b32 m0, s29
	v_lshl_add_u64 v[130:131], s[20:21], 0, v[96:97]
	v_lshl_add_u64 v[130:131], v[130:131], 0, s[30:31]
	v_mov_b32_e32 v96, v134
	global_load_lds_dwordx4 v[130:131], off
	s_mov_b32 m0, s78
	s_nop 0
	global_load_lds_dwordx4 v96, s[22:23]
	v_mov_b32_e32 v96, v137
	s_mov_b32 m0, s77
	s_nop 0
	global_load_lds_dwordx4 v96, s[22:23]
	v_mov_b32_e32 v96, v132
	s_mov_b32 m0, s65
	v_lshl_add_u64 v[130:131], s[4:5], 0, v[96:97]
	v_lshl_add_u64 v[130:131], v[130:131], 0, s[30:31]
	v_mov_b32_e32 v96, v135
	global_load_lds_dwordx4 v[130:131], off
	s_mov_b32 m0, s66
	v_lshl_add_u64 v[130:131], s[4:5], 0, v[96:97]
	v_lshl_add_u64 v[130:131], v[130:131], 0, s[30:31]
	global_load_lds_dwordx4 v[130:131], off
	s_waitcnt vmcnt(8)
	s_waitcnt lgkmcnt(0)
	s_barrier
	s_setprio 1
	s_waitcnt lgkmcnt(0)
	v_mfma_f32_16x16x32_bf16 v[60:63], v[150:153], v[184:187], v[60:63]
	v_mfma_f32_16x16x32_bf16 v[56:59], v[158:161], v[184:187], v[56:59]
	v_mfma_f32_16x16x32_bf16 v[44:47], v[150:153], v[192:195], v[44:47]
	v_mfma_f32_16x16x32_bf16 v[32:35], v[158:161], v[192:195], v[32:35]
	v_mfma_f32_16x16x32_bf16 v[16:19], v[150:153], v[200:203], v[16:19]
	v_mfma_f32_16x16x32_bf16 v[8:11], v[158:161], v[200:203], v[8:11]
	v_mfma_f32_16x16x32_bf16 v[4:7], v[150:153], v[208:211], v[4:7]
	v_mfma_f32_16x16x32_bf16 v[0:3], v[158:161], v[208:211], v[0:3]
	v_mfma_f32_16x16x32_bf16 v[60:63], v[154:157], v[188:191], v[60:63]
	v_mfma_f32_16x16x32_bf16 v[56:59], v[162:165], v[188:191], v[56:59]
	v_mfma_f32_16x16x32_bf16 v[44:47], v[154:157], v[196:199], v[44:47]
	v_mfma_f32_16x16x32_bf16 v[32:35], v[162:165], v[196:199], v[32:35]
	v_mfma_f32_16x16x32_bf16 v[16:19], v[154:157], v[204:207], v[16:19]
	v_mfma_f32_16x16x32_bf16 v[8:11], v[162:165], v[204:207], v[8:11]
	v_mfma_f32_16x16x32_bf16 v[4:7], v[154:157], v[212:215], v[4:7]
	v_mfma_f32_16x16x32_bf16 v[0:3], v[162:165], v[212:215], v[0:3]
	s_setprio 0
	s_setprio 1
	v_mfma_f32_16x16x32_bf16 v[52:55], v[166:169], v[184:187], v[52:55]
	v_mfma_f32_16x16x32_bf16 v[48:51], v[174:177], v[184:187], v[48:51]
	v_mfma_f32_16x16x32_bf16 v[28:31], v[166:169], v[192:195], v[28:31]
	v_mfma_f32_16x16x32_bf16 v[12:15], v[174:177], v[192:195], v[12:15]
	v_mfma_f32_16x16x32_bf16 v[36:39], v[166:169], v[200:203], v[36:39]
	v_mfma_f32_16x16x32_bf16 v[40:43], v[174:177], v[200:203], v[40:43]
	v_mfma_f32_16x16x32_bf16 v[20:23], v[166:169], v[208:211], v[20:23]
	v_mfma_f32_16x16x32_bf16 v[24:27], v[174:177], v[208:211], v[24:27]
	v_mfma_f32_16x16x32_bf16 v[52:55], v[170:173], v[188:191], v[52:55]
	v_mfma_f32_16x16x32_bf16 v[48:51], v[178:181], v[188:191], v[48:51]
	v_mfma_f32_16x16x32_bf16 v[28:31], v[170:173], v[196:199], v[28:31]
	v_mfma_f32_16x16x32_bf16 v[12:15], v[178:181], v[196:199], v[12:15]
	v_mfma_f32_16x16x32_bf16 v[36:39], v[170:173], v[204:207], v[36:39]
	v_mfma_f32_16x16x32_bf16 v[40:43], v[178:181], v[204:207], v[40:43]
	v_mfma_f32_16x16x32_bf16 v[20:23], v[170:173], v[212:215], v[20:23]
	v_mfma_f32_16x16x32_bf16 v[24:27], v[178:181], v[212:215], v[24:27]
	s_setprio 0
	s_barrier
	s_movk_i32 s22, 0x100
	s_andn2_b64 vcc, exec, s[2:3]
	s_mov_b64 s[20:21], -1
	s_mov_b64 s[2:3], 0
	s_cbranch_vccz .LBB0_937
	s_and_b64 vcc, exec, s[40:41]
	s_cbranch_vccz .LBB0_940
	s_barrier

; #define PG8_AOFF(ord, U, O0, O1) do { _Pragma("unroll") for (int _i = 0; _i < 2; ++_i) { \
;         O0[_i] = d.rowbyte(U, (int)tix[(ord) * 256 + Rr[_i]]) + (unsigned)(Cc[_i] * 2); O1[_i] = d.rowbyte(U, (int)tix[(ord) * 256 + HALF + Rr[_i]]) + (unsigned)(Cc[_i] * 2); } } while (0)
; #define PG8_STAGE(bufoff, gbase, voff) do { _Pragma("unroll") for (int _i = 0; _i < 2; ++_i) \
;         __builtin_amdgcn_global_load_lds((const __attribute__((address_space(1))) unsigned*)((const __attribute__((address_space(1))) char*)(gbase) + (unsigned)lnd_v((int)(voff)[_i])), (LAS unsigned*)(lds + (bufoff) + ldsw + _i * 8192), 16, 0, 0); } while (0)
; #define PG8_BAR __builtin_amdgcn_s_barrier()
; template <class Desc, class Epi>
; __device__ __forceinline__ void gemm_phase(const int wv_, LAS unsigned char* lds, const Desc& d, const Epi& E) {
;     ...
;         const int inext = bid + (ui + 1) * nblk; const bool has_next = inext < d.nunits;
;         if (has_next) d.unit(inext, nxt);
;         if constexpr (Desc::GATHER) { if (has_next) PG8_AOFF(ui + 1, nxt, voffAn, voffAn1); else { voffAn[0] = voffA[0]; voffAn[1] = voffA[1]; voffAn1[0] = voffA1[0]; voffAn1[1] = voffA1[1]; } }
;         const char* nA = has_next ? (const char*)nxt.a : cA; const char* nB = has_next ? (const char*)nxt.b : cB;
;         for (int t = 0; t < nt; t += 2) {
;             const bool last = (t == nt - 2);
;             unsigned sA0[2], sA1[2];
;             if constexpr (Desc::GATHER) { sA0[0] = last ? voffAn[0] : voffA[0]; sA0[1] = last ? voffAn[1] : voffA[1]; sA1[0] = last ? voffAn1[0] : voffA1[0]; sA1[1] = last ? voffAn1[1] : voffA1[1]; }
;             else { sA0[0] = voffA[0]; sA0[1] = voffA[1]; sA1[0] = voffA1[0]; sA1[1] = voffA1[1]; }
;             const char* a1 = cA + (size_t)(t + 1) * kstep;
;             const char* a2 = last ? nA : cA + (size_t)(t + 2) * kstep; const char* b2 = last ? nB : cB + (size_t)(t + 2) * kstep;
;             const char* a3 = a2 + kstep; const char* b3 = b2 + kstep;
;             PG8_LDB(B0, 0, 0); PG8_LDB(B1, 0, 1); PG8_SCHED; PG8_LDA(At, 0, 0); PG8_STAGE(PG8_SA(1, 1), a1, voffA1);
;             PG8_WAIT_V(8); PG8_WAIT_L(0); PG8_BAR; PG8_MMA(0, 0, At, B0); PG8_MMA(0, 1, At, B1); PG8_BAR; PG8_SCHED;
;             PG8_LDA(At, 0, 1); PG8_STAGE(PG8_SB(0, 0), b2, voffB); PG8_STAGE(PG8_SB(0, 1), b2 + hstepB, voffB); PG8_STAGE(PG8_SA(0, 0), a2, sA0);
.LBB0_1075:
	s_add_u32 s4, s2, 0x80
	s_addc_u32 s5, s3, 0
	s_add_i32 s47, 0, 0x10000
	s_cmp_eq_u32 s29, 12
	s_cselect_b32 s5, s51, s5
	s_cselect_b32 s4, s50, s4
	v_add_u32_e32 v96, s47, v226
	s_cselect_b32 s21, s53, s26
	s_cselect_b32 s20, s52, s1
	s_add_i32 s49, 0, 0x14000
	ds_read_b128 v[118:121], v96
	ds_read_b128 v[126:129], v96 offset:1024
	ds_read_b128 v[130:133], v96 offset:2048
	ds_read_b128 v[134:137], v96 offset:3072
	v_add_u32_e32 v96, s49, v226
	ds_read_b128 v[142:145], v96
	ds_read_b128 v[150:153], v96 offset:1024
	ds_read_b128 v[154:157], v96 offset:2048
	ds_read_b128 v[158:161], v96 offset:3072
	v_mov_b32_e32 v96, v220
	ds_read_b128 v[164:167], v231
	ds_read_b128 v[168:171], v231 offset:1024
	ds_read_b128 v[172:175], v231 offset:2048
	ds_read_b128 v[176:179], v231 offset:3072
	ds_read_b128 v[180:183], v231 offset:4096
	ds_read_b128 v[184:187], v231 offset:5120
	ds_read_b128 v[188:191], v231 offset:6144
	ds_read_b128 v[236:239], v231 offset:7168
	s_add_i32 m0, s60, 0xc000
	s_nop 0
	global_load_lds_dwordx4 v96, s[2:3]
	v_mov_b32_e32 v96, v223
	s_add_i32 m0, s60, 0xe000
	s_nop 0
	global_load_lds_dwordx4 v96, s[2:3]
	s_waitcnt vmcnt(8)
	s_waitcnt lgkmcnt(0)
	s_barrier
	s_setprio 1
	s_waitcnt lgkmcnt(0)
	v_mfma_f32_16x16x32_bf16 v[146:149], v[118:121], v[164:167], v[146:149]
	v_mfma_f32_16x16x32_bf16 v[138:141], v[130:133], v[164:167], v[138:141]
	v_mfma_f32_16x16x32_bf16 v[110:113], v[118:121], v[172:175], v[110:113]
	v_mfma_f32_16x16x32_bf16 v[106:109], v[130:133], v[172:175], v[106:109]
	v_mfma_f32_16x16x32_bf16 v[92:95], v[118:121], v[180:183], v[92:95]
	v_mfma_f32_16x16x32_bf16 v[88:91], v[130:133], v[180:183], v[88:91]
	v_mfma_f32_16x16x32_bf16 v[76:79], v[118:121], v[188:191], v[76:79]
	v_mfma_f32_16x16x32_bf16 v[72:75], v[130:133], v[188:191], v[72:75]
	v_mfma_f32_16x16x32_bf16 v[146:149], v[126:129], v[168:171], v[146:149]
	v_mfma_f32_16x16x32_bf16 v[138:141], v[134:137], v[168:171], v[138:141]
	v_mfma_f32_16x16x32_bf16 v[110:113], v[126:129], v[176:179], v[110:113]
	v_mfma_f32_16x16x32_bf16 v[106:109], v[134:137], v[176:179], v[106:109]
	v_mfma_f32_16x16x32_bf16 v[92:95], v[126:129], v[184:187], v[92:95]
	v_mfma_f32_16x16x32_bf16 v[88:91], v[134:137], v[184:187], v[88:91]
	v_mfma_f32_16x16x32_bf16 v[76:79], v[126:129], v[236:239], v[76:79]
	v_mfma_f32_16x16x32_bf16 v[72:75], v[134:137], v[236:239], v[72:75]
	s_setprio 0
	s_setprio 1
	v_mfma_f32_16x16x32_bf16 v[122:125], v[142:145], v[164:167], v[122:125]
	v_mfma_f32_16x16x32_bf16 v[114:117], v[154:157], v[164:167], v[114:117]
	v_mfma_f32_16x16x32_bf16 v[102:105], v[142:145], v[172:175], v[102:105]
	v_mfma_f32_16x16x32_bf16 v[98:101], v[154:157], v[172:175], v[98:101]
	v_mfma_f32_16x16x32_bf16 v[84:87], v[142:145], v[180:183], v[84:87]
	v_mfma_f32_16x16x32_bf16 v[80:83], v[154:157], v[180:183], v[80:83]
	v_mfma_f32_16x16x32_bf16 v[68:71], v[142:145], v[188:191], v[68:71]
	v_mfma_f32_16x16x32_bf16 v[64:67], v[154:157], v[188:191], v[64:67]
	v_mfma_f32_16x16x32_bf16 v[122:125], v[150:153], v[168:171], v[122:125]
	v_mfma_f32_16x16x32_bf16 v[114:117], v[158:161], v[168:171], v[114:117]
	v_mfma_f32_16x16x32_bf16 v[102:105], v[150:153], v[176:179], v[102:105]
	v_mfma_f32_16x16x32_bf16 v[98:101], v[158:161], v[176:179], v[98:101]
	v_mfma_f32_16x16x32_bf16 v[84:87], v[150:153], v[184:187], v[84:87]
	v_mfma_f32_16x16x32_bf16 v[80:83], v[158:161], v[184:187], v[80:83]
	v_mfma_f32_16x16x32_bf16 v[68:71], v[150:153], v[236:239], v[68:71]
	v_mfma_f32_16x16x32_bf16 v[64:67], v[158:161], v[236:239], v[64:67]
	s_setprio 0
	s_barrier
	v_mov_b32_e32 v96, v221
	s_add_i32 s47, s47, s59
	ds_read_b128 v[164:167], v231 offset:16384
	ds_read_b128 v[168:171], v231 offset:17408
	ds_read_b128 v[172:175], v231 offset:18432
	ds_read_b128 v[176:179], v231 offset:19456
	ds_read_b128 v[180:183], v231 offset:20480
	ds_read_b128 v[184:187], v231 offset:21504
	ds_read_b128 v[188:191], v231 offset:22528
	ds_read_b128 v[236:239], v231 offset:23552
	s_mov_b32 m0, s47
	s_nop 0
	global_load_lds_dwordx4 v96, s[20:21]
	v_mov_b32_e32 v96, v224
	s_add_i32 m0, s47, 0x2000
	s_add_u32 s70, s20, 0x40000
	global_load_lds_dwordx4 v96, s[20:21]
	s_addc_u32 s71, s21, 0
	v_mov_b32_e32 v96, v221
	s_add_i32 s47, s49, s59
	s_mov_b32 m0, s47
	s_nop 0
	global_load_lds_dwordx4 v96, s[70:71]
	v_mov_b32_e32 v96, v224
	s_add_i32 m0, s47, 0x2000
	s_nop 0
	global_load_lds_dwordx4 v96, s[70:71]
	v_mov_b32_e32 v96, v219
	s_mov_b32 m0, s60
	s_nop 0
	global_load_lds_dwordx4 v96, s[4:5]
	v_mov_b32_e32 v96, v222
	s_mov_b32 m0, s62
	s_nop 0
	global_load_lds_dwordx4 v96, s[4:5]
	s_waitcnt vmcnt(8)
	s_waitcnt lgkmcnt(0)
	s_barrier
; #define PG8_STAGE(bufoff, gbase, voff) do { _Pragma("unroll") for (int _i = 0; _i < 2; ++_i) \
;         __builtin_amdgcn_global_load_lds((const __attribute__((address_space(1))) unsigned*)((const __attribute__((address_space(1))) char*)(gbase) + (unsigned)lnd_v((int)(voff)[_i])), (LAS unsigned*)(lds + (bufoff) + ldsw + _i * 8192), 16, 0, 0); } while (0)
; #define PG8_LDA(dst, b, h) do { _Pragma("unroll") for (int m = 0; m < 4; ++m) _Pragma("unroll") for (int k = 0; k < 2; ++k) dst[m][k] = *(const LAS bf16x8*)(lds + PG8_SA(b, h) + aoff + m * 2048 + k * 1024); } while (0)
; #define PG8_LDB(dst, b, h) do { _Pragma("unroll") for (int n = 0; n < 2; ++n) _Pragma("unroll") for (int k = 0; k < 2; ++k) dst[n][k] = *(const LAS bf16x8*)(lds + PG8_SB(b, h) + boff + n * 2048 + k * 1024); } while (0)
; #define PG8_MMA(ai, bj, At, Bt) do { __builtin_amdgcn_s_setprio(1); _Pragma("unroll") for (int m = 0; m < 4; ++m) _Pragma("unroll") for (int n = 0; n < 2; ++n) _Pragma("unroll") for (int k = 0; k < 2; ++k) \
;         acc[ai][bj][m][n] = __builtin_amdgcn_mfma_f32_16x16x32_bf16(Bt[n][k], At[m][k], acc[ai][bj][m][n], 0, 0, 0); __builtin_amdgcn_s_setprio(0); } while (0)
; #define PG8_WAIT_V(n) asm volatile("s_waitcnt vmcnt(" #n ")" ::: "memory")
; #define PG8_WAIT_L(n) asm volatile("s_waitcnt lgkmcnt(" #n ")" ::: "memory")
; #define PG8_BAR __builtin_amdgcn_s_barrier()
; #define PG8_SCHED __builtin_amdgcn_sched_barrier(0)
; template <class Desc, class Epi>
; __device__ __forceinline__ void gemm_phase(const int wv_, LAS unsigned char* lds, const Desc& d, const Epi& E) {
;     ...
;             PG8_WAIT_V(8); PG8_WAIT_L(0); PG8_BAR; PG8_MMA(1, 0, At, B0); PG8_MMA(1, 1, At, B1); PG8_BAR; PG8_SCHED;
;             PG8_LDB(B0, 1, 0); PG8_LDB(B1, 1, 1); PG8_SCHED; PG8_LDA(At, 1, 0); PG8_STAGE(PG8_SA(0, 1), a2, sA1);
;             PG8_WAIT_V(8); PG8_WAIT_L(0); PG8_BAR; PG8_MMA(0, 0, At, B0); PG8_MMA(0, 1, At, B1); PG8_BAR; PG8_SCHED;
	s_setprio 1
	s_waitcnt lgkmcnt(0)
	v_mfma_f32_16x16x32_bf16 v[60:63], v[118:121], v[164:167], v[60:63]
	v_mfma_f32_16x16x32_bf16 v[56:59], v[130:133], v[164:167], v[56:59]
	v_mfma_f32_16x16x32_bf16 v[44:47], v[118:121], v[172:175], v[44:47]
	v_mfma_f32_16x16x32_bf16 v[40:43], v[130:133], v[172:175], v[40:43]
	v_mfma_f32_16x16x32_bf16 v[20:23], v[118:121], v[180:183], v[20:23]
	v_mfma_f32_16x16x32_bf16 v[16:19], v[130:133], v[180:183], v[16:19]
	v_mfma_f32_16x16x32_bf16 v[4:7], v[118:121], v[188:191], v[4:7]
	v_mfma_f32_16x16x32_bf16 v[0:3], v[130:133], v[188:191], v[0:3]
	v_mfma_f32_16x16x32_bf16 v[60:63], v[126:129], v[168:171], v[60:63]
	v_mfma_f32_16x16x32_bf16 v[56:59], v[134:137], v[168:171], v[56:59]
	v_mfma_f32_16x16x32_bf16 v[44:47], v[126:129], v[176:179], v[44:47]
	v_mfma_f32_16x16x32_bf16 v[40:43], v[134:137], v[176:179], v[40:43]
	v_mfma_f32_16x16x32_bf16 v[20:23], v[126:129], v[184:187], v[20:23]
	v_mfma_f32_16x16x32_bf16 v[16:19], v[134:137], v[184:187], v[16:19]
	v_mfma_f32_16x16x32_bf16 v[4:7], v[126:129], v[236:239], v[4:7]
	v_mfma_f32_16x16x32_bf16 v[0:3], v[134:137], v[236:239], v[0:3]
	s_setprio 0
	s_setprio 1
	v_mfma_f32_16x16x32_bf16 v[52:55], v[142:145], v[164:167], v[52:55]
	v_mfma_f32_16x16x32_bf16 v[48:51], v[154:157], v[164:167], v[48:51]
	v_mfma_f32_16x16x32_bf16 v[36:39], v[142:145], v[172:175], v[36:39]
	v_mfma_f32_16x16x32_bf16 v[32:35], v[154:157], v[172:175], v[32:35]
	v_mfma_f32_16x16x32_bf16 v[28:31], v[142:145], v[180:183], v[28:31]
	v_mfma_f32_16x16x32_bf16 v[24:27], v[154:157], v[180:183], v[24:27]
	v_mfma_f32_16x16x32_bf16 v[12:15], v[142:145], v[188:191], v[12:15]
	v_mfma_f32_16x16x32_bf16 v[8:11], v[154:157], v[188:191], v[8:11]
	v_mfma_f32_16x16x32_bf16 v[52:55], v[150:153], v[168:171], v[52:55]
	v_mfma_f32_16x16x32_bf16 v[48:51], v[158:161], v[168:171], v[48:51]
	v_mfma_f32_16x16x32_bf16 v[36:39], v[150:153], v[176:179], v[36:39]
	v_mfma_f32_16x16x32_bf16 v[32:35], v[158:161], v[176:179], v[32:35]
	v_mfma_f32_16x16x32_bf16 v[28:31], v[150:153], v[184:187], v[28:31]
	v_mfma_f32_16x16x32_bf16 v[24:27], v[158:161], v[184:187], v[24:27]
	v_mfma_f32_16x16x32_bf16 v[12:15], v[150:153], v[236:239], v[12:15]
	v_mfma_f32_16x16x32_bf16 v[8:11], v[158:161], v[236:239], v[8:11]
	s_setprio 0
	s_barrier
	s_add_i32 s47, 0, 0x18000
	v_add_u32_e32 v96, s47, v226
	s_add_i32 s49, 0, 0x1c000
	ds_read_b128 v[118:121], v96
	ds_read_b128 v[126:129], v96 offset:1024
	ds_read_b128 v[130:133], v96 offset:2048
	ds_read_b128 v[134:137], v96 offset:3072
	v_add_u32_e32 v96, s49, v226
	ds_read_b128 v[142:145], v96
	ds_read_b128 v[150:153], v96 offset:1024
	ds_read_b128 v[154:157], v96 offset:2048
	ds_read_b128 v[158:161], v96 offset:3072
	v_mov_b32_e32 v96, v220
	s_mov_b32 m0, s63
	ds_read_b128 v[164:167], v231 offset:32768
	ds_read_b128 v[168:171], v231 offset:33792
	ds_read_b128 v[172:175], v231 offset:34816
	ds_read_b128 v[176:179], v231 offset:35840
	ds_read_b128 v[180:183], v231 offset:36864
	ds_read_b128 v[184:187], v231 offset:37888
	ds_read_b128 v[188:191], v231 offset:38912
	ds_read_b128 v[236:239], v231 offset:39936
	s_nop 0
	global_load_lds_dwordx4 v96, s[4:5]
	v_mov_b32_e32 v96, v223
	s_mov_b32 m0, s64
	s_nop 0
	global_load_lds_dwordx4 v96, s[4:5]
	s_waitcnt vmcnt(8)
	s_waitcnt lgkmcnt(0)
	s_barrier
	s_setprio 1
	s_waitcnt lgkmcnt(0)
	v_mfma_f32_16x16x32_bf16 v[146:149], v[118:121], v[164:167], v[146:149]
	v_mfma_f32_16x16x32_bf16 v[138:141], v[130:133], v[164:167], v[138:141]
	v_mfma_f32_16x16x32_bf16 v[110:113], v[118:121], v[172:175], v[110:113]
	v_mfma_f32_16x16x32_bf16 v[106:109], v[130:133], v[172:175], v[106:109]
	v_mfma_f32_16x16x32_bf16 v[92:95], v[118:121], v[180:183], v[92:95]
	v_mfma_f32_16x16x32_bf16 v[88:91], v[130:133], v[180:183], v[88:91]
	v_mfma_f32_16x16x32_bf16 v[76:79], v[118:121], v[188:191], v[76:79]
	v_mfma_f32_16x16x32_bf16 v[72:75], v[130:133], v[188:191], v[72:75]
	v_mfma_f32_16x16x32_bf16 v[146:149], v[126:129], v[168:171], v[146:149]
	v_mfma_f32_16x16x32_bf16 v[138:141], v[134:137], v[168:171], v[138:141]
	v_mfma_f32_16x16x32_bf16 v[110:113], v[126:129], v[176:179], v[110:113]
	v_mfma_f32_16x16x32_bf16 v[106:109], v[134:137], v[176:179], v[106:109]
	v_mfma_f32_16x16x32_bf16 v[92:95], v[126:129], v[184:187], v[92:95]
	v_mfma_f32_16x16x32_bf16 v[88:91], v[134:137], v[184:187], v[88:91]
	v_mfma_f32_16x16x32_bf16 v[76:79], v[126:129], v[236:239], v[76:79]
	v_mfma_f32_16x16x32_bf16 v[72:75], v[134:137], v[236:239], v[72:75]
	s_setprio 0
	s_setprio 1
	v_mfma_f32_16x16x32_bf16 v[122:125], v[142:145], v[164:167], v[122:125]
	v_mfma_f32_16x16x32_bf16 v[114:117], v[154:157], v[164:167], v[114:117]
	v_mfma_f32_16x16x32_bf16 v[102:105], v[142:145], v[172:175], v[102:105]
	v_mfma_f32_16x16x32_bf16 v[98:101], v[154:157], v[172:175], v[98:101]
	v_mfma_f32_16x16x32_bf16 v[84:87], v[142:145], v[180:183], v[84:87]
	v_mfma_f32_16x16x32_bf16 v[80:83], v[154:157], v[180:183], v[80:83]
	v_mfma_f32_16x16x32_bf16 v[68:71], v[142:145], v[188:191], v[68:71]
	v_mfma_f32_16x16x32_bf16 v[64:67], v[154:157], v[188:191], v[64:67]
	v_mfma_f32_16x16x32_bf16 v[122:125], v[150:153], v[168:171], v[122:125]
	v_mfma_f32_16x16x32_bf16 v[114:117], v[158:161], v[168:171], v[114:117]
	v_mfma_f32_16x16x32_bf16 v[102:105], v[150:153], v[176:179], v[102:105]
	v_mfma_f32_16x16x32_bf16 v[98:101], v[158:161], v[176:179], v[98:101]
	v_mfma_f32_16x16x32_bf16 v[84:87], v[150:153], v[184:187], v[84:87]
	v_mfma_f32_16x16x32_bf16 v[80:83], v[158:161], v[184:187], v[80:83]
	v_mfma_f32_16x16x32_bf16 v[68:71], v[150:153], v[236:239], v[68:71]
	v_mfma_f32_16x16x32_bf16 v[64:67], v[158:161], v[236:239], v[64:67]
	s_setprio 0
	s_barrier
; #define PG8_STAGE(bufoff, gbase, voff) do { _Pragma("unroll") for (int _i = 0; _i < 2; ++_i) \
;         __builtin_amdgcn_global_load_lds((const __attribute__((address_space(1))) unsigned*)((const __attribute__((address_space(1))) char*)(gbase) + (unsigned)lnd_v((int)(voff)[_i])), (LAS unsigned*)(lds + (bufoff) + ldsw + _i * 8192), 16, 0, 0); } while (0)
; #define PG8_LDA(dst, b, h) do { _Pragma("unroll") for (int m = 0; m < 4; ++m) _Pragma("unroll") for (int k = 0; k < 2; ++k) dst[m][k] = *(const LAS bf16x8*)(lds + PG8_SA(b, h) + aoff + m * 2048 + k * 1024); } while (0)
; #define PG8_MMA(ai, bj, At, Bt) do { __builtin_amdgcn_s_setprio(1); _Pragma("unroll") for (int m = 0; m < 4; ++m) _Pragma("unroll") for (int n = 0; n < 2; ++n) _Pragma("unroll") for (int k = 0; k < 2; ++k) \
;         acc[ai][bj][m][n] = __builtin_amdgcn_mfma_f32_16x16x32_bf16(Bt[n][k], At[m][k], acc[ai][bj][m][n], 0, 0, 0); __builtin_amdgcn_s_setprio(0); } while (0)
; #define PG8_WAIT_V(n) asm volatile("s_waitcnt vmcnt(" #n ")" ::: "memory")
; #define PG8_WAIT_L(n) asm volatile("s_waitcnt lgkmcnt(" #n ")" ::: "memory")
; #define PG8_BAR __builtin_amdgcn_s_barrier()
; #define PG8_SCHED __builtin_amdgcn_sched_barrier(0)
; template <class Desc, class Epi>
; __device__ __forceinline__ void gemm_phase(const int wv_, LAS unsigned char* lds, const Desc& d, const Epi& E) {
;     ...
;             PG8_LDA(At, 1, 1); PG8_STAGE(PG8_SB(1, 0), b3, voffB); PG8_STAGE(PG8_SB(1, 1), b3 + hstepB, voffB); PG8_STAGE(PG8_SA(1, 0), a3, sA0);
;             PG8_WAIT_V(8); PG8_WAIT_L(0); PG8_BAR; PG8_MMA(1, 0, At, B0); PG8_MMA(1, 1, At, B1); PG8_BAR; PG8_SCHED;
;         }
;         if (wr == 0) PG8_BAR;
	v_mov_b32_e32 v96, v221
	ds_read_b128 v[164:167], v231 offset:49152
	ds_read_b128 v[168:171], v231 offset:50176
	ds_read_b128 v[172:175], v231 offset:51200
	ds_read_b128 v[176:179], v231 offset:52224
	ds_read_b128 v[180:183], v231 offset:53248
	ds_read_b128 v[184:187], v231 offset:54272
	ds_read_b128 v[188:191], v231 offset:55296
	ds_read_b128 v[236:239], v231 offset:56320
	s_add_i32 s47, s47, s59
	v_lshl_add_u64 v[194:195], s[20:21], 0, v[96:97]
	v_lshl_add_u64 v[194:195], v[194:195], 0, s[30:31]
	s_mov_b32 m0, s47
	v_mov_b32_e32 v96, v224
	global_load_lds_dwordx4 v[194:195], off
	s_add_i32 m0, s47, 0x2000
	s_nop 0
	v_lshl_add_u64 v[194:195], s[20:21], 0, v[96:97]
	s_add_u32 s20, s20, 0x40080
	v_lshl_add_u64 v[194:195], v[194:195], 0, s[30:31]
	s_addc_u32 s21, s21, 0
	v_mov_b32_e32 v96, v221
	s_add_i32 s47, s49, s59
	global_load_lds_dwordx4 v[194:195], off
	s_mov_b32 m0, s47
	s_nop 0
	global_load_lds_dwordx4 v96, s[20:21]
	v_mov_b32_e32 v96, v224
	s_add_i32 m0, s47, 0x2000
	s_nop 0
	global_load_lds_dwordx4 v96, s[20:21]
	v_mov_b32_e32 v96, v219
	s_mov_b32 m0, s66
	v_lshl_add_u64 v[194:195], s[4:5], 0, v[96:97]
	v_lshl_add_u64 v[194:195], v[194:195], 0, s[30:31]
	v_mov_b32_e32 v96, v222
	global_load_lds_dwordx4 v[194:195], off
	s_mov_b32 m0, s67
	v_lshl_add_u64 v[194:195], s[4:5], 0, v[96:97]
	v_lshl_add_u64 v[194:195], v[194:195], 0, s[30:31]
	global_load_lds_dwordx4 v[194:195], off
	s_waitcnt vmcnt(8)
	s_waitcnt lgkmcnt(0)
	s_barrier
	s_setprio 1
	s_waitcnt lgkmcnt(0)
	v_mfma_f32_16x16x32_bf16 v[60:63], v[118:121], v[164:167], v[60:63]
	v_mfma_f32_16x16x32_bf16 v[56:59], v[130:133], v[164:167], v[56:59]
	v_mfma_f32_16x16x32_bf16 v[44:47], v[118:121], v[172:175], v[44:47]
	v_mfma_f32_16x16x32_bf16 v[40:43], v[130:133], v[172:175], v[40:43]
	v_mfma_f32_16x16x32_bf16 v[20:23], v[118:121], v[180:183], v[20:23]
	v_mfma_f32_16x16x32_bf16 v[16:19], v[130:133], v[180:183], v[16:19]
	v_mfma_f32_16x16x32_bf16 v[4:7], v[118:121], v[188:191], v[4:7]
	v_mfma_f32_16x16x32_bf16 v[0:3], v[130:133], v[188:191], v[0:3]
	v_mfma_f32_16x16x32_bf16 v[60:63], v[126:129], v[168:171], v[60:63]
	v_mfma_f32_16x16x32_bf16 v[56:59], v[134:137], v[168:171], v[56:59]
	v_mfma_f32_16x16x32_bf16 v[44:47], v[126:129], v[176:179], v[44:47]
	v_mfma_f32_16x16x32_bf16 v[40:43], v[134:137], v[176:179], v[40:43]
	v_mfma_f32_16x16x32_bf16 v[20:23], v[126:129], v[184:187], v[20:23]
	v_mfma_f32_16x16x32_bf16 v[16:19], v[134:137], v[184:187], v[16:19]
	v_mfma_f32_16x16x32_bf16 v[4:7], v[126:129], v[236:239], v[4:7]
	v_mfma_f32_16x16x32_bf16 v[0:3], v[134:137], v[236:239], v[0:3]
	s_setprio 0
	s_setprio 1
	v_mfma_f32_16x16x32_bf16 v[52:55], v[142:145], v[164:167], v[52:55]
	v_mfma_f32_16x16x32_bf16 v[48:51], v[154:157], v[164:167], v[48:51]
	v_mfma_f32_16x16x32_bf16 v[36:39], v[142:145], v[172:175], v[36:39]
	v_mfma_f32_16x16x32_bf16 v[32:35], v[154:157], v[172:175], v[32:35]
	v_mfma_f32_16x16x32_bf16 v[28:31], v[142:145], v[180:183], v[28:31]
	v_mfma_f32_16x16x32_bf16 v[24:27], v[154:157], v[180:183], v[24:27]
	v_mfma_f32_16x16x32_bf16 v[12:15], v[142:145], v[188:191], v[12:15]
	v_mfma_f32_16x16x32_bf16 v[8:11], v[154:157], v[188:191], v[8:11]
	v_mfma_f32_16x16x32_bf16 v[52:55], v[150:153], v[168:171], v[52:55]
	v_mfma_f32_16x16x32_bf16 v[48:51], v[158:161], v[168:171], v[48:51]
	v_mfma_f32_16x16x32_bf16 v[36:39], v[150:153], v[176:179], v[36:39]
	v_mfma_f32_16x16x32_bf16 v[32:35], v[158:161], v[176:179], v[32:35]
	v_mfma_f32_16x16x32_bf16 v[28:31], v[150:153], v[184:187], v[28:31]
	v_mfma_f32_16x16x32_bf16 v[24:27], v[158:161], v[184:187], v[24:27]
	v_mfma_f32_16x16x32_bf16 v[12:15], v[150:153], v[236:239], v[12:15]
	v_mfma_f32_16x16x32_bf16 v[8:11], v[158:161], v[236:239], v[8:11]
	s_setprio 0
	s_barrier
	s_add_i32 s29, s29, 2
	s_add_u32 s2, s2, 0x100
	s_addc_u32 s3, s3, 0
	s_add_u32 s1, s1, 0x100
	s_addc_u32 s26, s26, 0
	s_cmp_gt_u32 s29, 13
	s_cbranch_scc0 .LBB0_1075
	s_and_b64 vcc, exec, s[44:45]
	s_cbranch_vccz .LBB0_1078
	s_barrier

; #define PG8_AOFF(ord, U, O0, O1) do { _Pragma("unroll") for (int _i = 0; _i < 2; ++_i) { \
;         O0[_i] = d.rowbyte(U, (int)tix[(ord) * 256 + Rr[_i]]) + (unsigned)(Cc[_i] * 2); O1[_i] = d.rowbyte(U, (int)tix[(ord) * 256 + HALF + Rr[_i]]) + (unsigned)(Cc[_i] * 2); } } while (0)
; #define PG8_STAGE(bufoff, gbase, voff) do { _Pragma("unroll") for (int _i = 0; _i < 2; ++_i) \
;         __builtin_amdgcn_global_load_lds((const __attribute__((address_space(1))) unsigned*)((const __attribute__((address_space(1))) char*)(gbase) + (unsigned)lnd_v((int)(voff)[_i])), (LAS unsigned*)(lds + (bufoff) + ldsw + _i * 8192), 16, 0, 0); } while (0)
; #define PG8_BAR __builtin_amdgcn_s_barrier()
; template <class Desc, class Epi>
; __device__ __forceinline__ void gemm_phase(const int wv_, LAS unsigned char* lds, const Desc& d, const Epi& E) {
;     ...
;         const int inext = bid + (ui + 1) * nblk; const bool has_next = inext < d.nunits;
;         if (has_next) d.unit(inext, nxt);
;         if constexpr (Desc::GATHER) { if (has_next) PG8_AOFF(ui + 1, nxt, voffAn, voffAn1); else { voffAn[0] = voffA[0]; voffAn[1] = voffA[1]; voffAn1[0] = voffA1[0]; voffAn1[1] = voffA1[1]; } }
;         const char* nA = has_next ? (const char*)nxt.a : cA; const char* nB = has_next ? (const char*)nxt.b : cB;
;         for (int t = 0; t < nt; t += 2) {
;             const bool last = (t == nt - 2);
;             unsigned sA0[2], sA1[2];
;             if constexpr (Desc::GATHER) { sA0[0] = last ? voffAn[0] : voffA[0]; sA0[1] = last ? voffAn[1] : voffA[1]; sA1[0] = last ? voffAn1[0] : voffA1[0]; sA1[1] = last ? voffAn1[1] : voffA1[1]; }
;             else { sA0[0] = voffA[0]; sA0[1] = voffA[1]; sA1[0] = voffA1[0]; sA1[1] = voffA1[1]; }
;             const char* a1 = cA + (size_t)(t + 1) * kstep;
;             const char* a2 = last ? nA : cA + (size_t)(t + 2) * kstep; const char* b2 = last ? nB : cB + (size_t)(t + 2) * kstep;
;             const char* a3 = a2 + kstep; const char* b3 = b2 + kstep;
;             PG8_LDB(B0, 0, 0); PG8_LDB(B1, 0, 1); PG8_SCHED; PG8_LDA(At, 0, 0); PG8_STAGE(PG8_SA(1, 1), a1, voffA1);
;             PG8_WAIT_V(8); PG8_WAIT_L(0); PG8_BAR; PG8_MMA(0, 0, At, B0); PG8_MMA(0, 1, At, B1); PG8_BAR; PG8_SCHED;
;             PG8_LDA(At, 0, 1); PG8_STAGE(PG8_SB(0, 0), b2, voffB); PG8_STAGE(PG8_SB(0, 1), b2 + hstepB, voffB); PG8_STAGE(PG8_SA(0, 0), a2, sA0);
.LBB0_1161:
	s_add_u32 s4, s2, 0x80
	s_addc_u32 s5, s3, 0
	s_add_i32 s65, 0, 0x10000
	s_cmp_eq_u32 s45, 12
	s_cselect_b32 s5, s47, s5
	s_cselect_b32 s4, s46, s4
	v_add_u32_e32 v96, s65, v197
	s_cselect_b32 s21, s49, s29
	s_cselect_b32 s20, s48, s1
	s_add_i32 s68, 0, 0x14000
	ds_read_b128 v[130:133], v96
	ds_read_b128 v[134:137], v96 offset:1024
	ds_read_b128 v[138:141], v96 offset:2048
	ds_read_b128 v[142:145], v96 offset:3072
	v_add_u32_e32 v96, s68, v197
	ds_read_b128 v[146:149], v96
	ds_read_b128 v[150:153], v96 offset:1024
	ds_read_b128 v[154:157], v96 offset:2048
	ds_read_b128 v[158:161], v96 offset:3072
	v_mov_b32_e32 v96, v191
	ds_read_b128 v[164:167], v228
	ds_read_b128 v[168:171], v228 offset:1024
	ds_read_b128 v[172:175], v228 offset:2048
	ds_read_b128 v[176:179], v228 offset:3072
	ds_read_b128 v[180:183], v228 offset:4096
	ds_read_b128 v[184:187], v228 offset:5120
	ds_read_b128 v[236:239], v228 offset:6144
	ds_read_b128 v[240:243], v228 offset:7168
	s_add_i32 m0, s55, 0xc000
	s_nop 0
	global_load_lds_dwordx4 v96, s[2:3]
	v_mov_b32_e32 v96, v194
	s_add_i32 m0, s55, 0xe000
	s_nop 0
	global_load_lds_dwordx4 v96, s[2:3]
	s_waitcnt vmcnt(8)
	s_waitcnt lgkmcnt(0)
	s_barrier
	s_setprio 1
	s_waitcnt lgkmcnt(0)
	v_mfma_f32_16x16x32_bf16 v[126:129], v[130:133], v[164:167], v[126:129]
	v_mfma_f32_16x16x32_bf16 v[122:125], v[138:141], v[164:167], v[122:125]
	v_mfma_f32_16x16x32_bf16 v[114:117], v[130:133], v[172:175], v[114:117]
	v_mfma_f32_16x16x32_bf16 v[106:109], v[138:141], v[172:175], v[106:109]
	v_mfma_f32_16x16x32_bf16 v[98:101], v[130:133], v[180:183], v[98:101]
	v_mfma_f32_16x16x32_bf16 v[88:91], v[138:141], v[180:183], v[88:91]
	v_mfma_f32_16x16x32_bf16 v[80:83], v[130:133], v[236:239], v[80:83]
	v_mfma_f32_16x16x32_bf16 v[72:75], v[138:141], v[236:239], v[72:75]
	v_mfma_f32_16x16x32_bf16 v[126:129], v[134:137], v[168:171], v[126:129]
	v_mfma_f32_16x16x32_bf16 v[122:125], v[142:145], v[168:171], v[122:125]
	v_mfma_f32_16x16x32_bf16 v[114:117], v[134:137], v[176:179], v[114:117]
	v_mfma_f32_16x16x32_bf16 v[106:109], v[142:145], v[176:179], v[106:109]
	v_mfma_f32_16x16x32_bf16 v[98:101], v[134:137], v[184:187], v[98:101]
	v_mfma_f32_16x16x32_bf16 v[88:91], v[142:145], v[184:187], v[88:91]
	v_mfma_f32_16x16x32_bf16 v[80:83], v[134:137], v[240:243], v[80:83]
	v_mfma_f32_16x16x32_bf16 v[72:75], v[142:145], v[240:243], v[72:75]
	s_setprio 0
	s_setprio 1
	v_mfma_f32_16x16x32_bf16 v[118:121], v[146:149], v[164:167], v[118:121]
	v_mfma_f32_16x16x32_bf16 v[110:113], v[154:157], v[164:167], v[110:113]
	v_mfma_f32_16x16x32_bf16 v[102:105], v[146:149], v[172:175], v[102:105]
	v_mfma_f32_16x16x32_bf16 v[92:95], v[154:157], v[172:175], v[92:95]
	v_mfma_f32_16x16x32_bf16 v[84:87], v[146:149], v[180:183], v[84:87]
	v_mfma_f32_16x16x32_bf16 v[76:79], v[154:157], v[180:183], v[76:79]
	v_mfma_f32_16x16x32_bf16 v[68:71], v[146:149], v[236:239], v[68:71]
	v_mfma_f32_16x16x32_bf16 v[64:67], v[154:157], v[236:239], v[64:67]
	v_mfma_f32_16x16x32_bf16 v[118:121], v[150:153], v[168:171], v[118:121]
	v_mfma_f32_16x16x32_bf16 v[110:113], v[158:161], v[168:171], v[110:113]
	v_mfma_f32_16x16x32_bf16 v[102:105], v[150:153], v[176:179], v[102:105]
	v_mfma_f32_16x16x32_bf16 v[92:95], v[158:161], v[176:179], v[92:95]
	v_mfma_f32_16x16x32_bf16 v[84:87], v[150:153], v[184:187], v[84:87]
	v_mfma_f32_16x16x32_bf16 v[76:79], v[158:161], v[184:187], v[76:79]
	v_mfma_f32_16x16x32_bf16 v[68:71], v[150:153], v[240:243], v[68:71]
	v_mfma_f32_16x16x32_bf16 v[64:67], v[158:161], v[240:243], v[64:67]
	s_setprio 0
	s_barrier
	v_mov_b32_e32 v96, v192
	s_add_i32 s65, s65, s54
	ds_read_b128 v[164:167], v228 offset:16384
	ds_read_b128 v[168:171], v228 offset:17408
	ds_read_b128 v[172:175], v228 offset:18432
	ds_read_b128 v[176:179], v228 offset:19456
	ds_read_b128 v[180:183], v228 offset:20480
	ds_read_b128 v[184:187], v228 offset:21504
	ds_read_b128 v[236:239], v228 offset:22528
	ds_read_b128 v[240:243], v228 offset:23552
	s_mov_b32 m0, s65
	s_nop 0
	global_load_lds_dwordx4 v96, s[20:21]
	v_mov_b32_e32 v96, v195
	s_add_i32 m0, s65, 0x2000
	s_add_u32 s66, s20, 0x40000
	global_load_lds_dwordx4 v96, s[20:21]
	s_addc_u32 s67, s21, 0
	v_mov_b32_e32 v96, v192
	s_add_i32 s65, s68, s54
	s_mov_b32 m0, s65
	s_nop 0
	global_load_lds_dwordx4 v96, s[66:67]
	v_mov_b32_e32 v96, v195
	s_add_i32 m0, s65, 0x2000
	s_nop 0
	global_load_lds_dwordx4 v96, s[66:67]
	v_mov_b32_e32 v96, v190
	s_mov_b32 m0, s55
	s_nop 0
	global_load_lds_dwordx4 v96, s[4:5]
	v_mov_b32_e32 v96, v193
	s_mov_b32 m0, s56
	s_nop 0
	global_load_lds_dwordx4 v96, s[4:5]
	s_waitcnt vmcnt(8)
	s_waitcnt lgkmcnt(0)
	s_barrier
; #define PG8_STAGE(bufoff, gbase, voff) do { _Pragma("unroll") for (int _i = 0; _i < 2; ++_i) \
;         __builtin_amdgcn_global_load_lds((const __attribute__((address_space(1))) unsigned*)((const __attribute__((address_space(1))) char*)(gbase) + (unsigned)lnd_v((int)(voff)[_i])), (LAS unsigned*)(lds + (bufoff) + ldsw + _i * 8192), 16, 0, 0); } while (0)
; #define PG8_LDA(dst, b, h) do { _Pragma("unroll") for (int m = 0; m < 4; ++m) _Pragma("unroll") for (int k = 0; k < 2; ++k) dst[m][k] = *(const LAS bf16x8*)(lds + PG8_SA(b, h) + aoff + m * 2048 + k * 1024); } while (0)
; #define PG8_LDB(dst, b, h) do { _Pragma("unroll") for (int n = 0; n < 2; ++n) _Pragma("unroll") for (int k = 0; k < 2; ++k) dst[n][k] = *(const LAS bf16x8*)(lds + PG8_SB(b, h) + boff + n * 2048 + k * 1024); } while (0)
; #define PG8_MMA(ai, bj, At, Bt) do { __builtin_amdgcn_s_setprio(1); _Pragma("unroll") for (int m = 0; m < 4; ++m) _Pragma("unroll") for (int n = 0; n < 2; ++n) _Pragma("unroll") for (int k = 0; k < 2; ++k) \
;         acc[ai][bj][m][n] = __builtin_amdgcn_mfma_f32_16x16x32_bf16(Bt[n][k], At[m][k], acc[ai][bj][m][n], 0, 0, 0); __builtin_amdgcn_s_setprio(0); } while (0)
; #define PG8_WAIT_V(n) asm volatile("s_waitcnt vmcnt(" #n ")" ::: "memory")
; #define PG8_WAIT_L(n) asm volatile("s_waitcnt lgkmcnt(" #n ")" ::: "memory")
; #define PG8_BAR __builtin_amdgcn_s_barrier()
; #define PG8_SCHED __builtin_amdgcn_sched_barrier(0)
; template <class Desc, class Epi>
; __device__ __forceinline__ void gemm_phase(const int wv_, LAS unsigned char* lds, const Desc& d, const Epi& E) {
;     ...
;             PG8_WAIT_V(8); PG8_WAIT_L(0); PG8_BAR; PG8_MMA(1, 0, At, B0); PG8_MMA(1, 1, At, B1); PG8_BAR; PG8_SCHED;
;             PG8_LDB(B0, 1, 0); PG8_LDB(B1, 1, 1); PG8_SCHED; PG8_LDA(At, 1, 0); PG8_STAGE(PG8_SA(0, 1), a2, sA1);
;             PG8_WAIT_V(8); PG8_WAIT_L(0); PG8_BAR; PG8_MMA(0, 0, At, B0); PG8_MMA(0, 1, At, B1); PG8_BAR; PG8_SCHED;
	s_setprio 1
	s_waitcnt lgkmcnt(0)
	v_mfma_f32_16x16x32_bf16 v[60:63], v[130:133], v[164:167], v[60:63]
	v_mfma_f32_16x16x32_bf16 v[56:59], v[138:141], v[164:167], v[56:59]
	v_mfma_f32_16x16x32_bf16 v[40:43], v[130:133], v[172:175], v[40:43]
	v_mfma_f32_16x16x32_bf16 v[32:35], v[138:141], v[172:175], v[32:35]
	v_mfma_f32_16x16x32_bf16 v[16:19], v[130:133], v[180:183], v[16:19]
	v_mfma_f32_16x16x32_bf16 v[8:11], v[138:141], v[180:183], v[8:11]
	v_mfma_f32_16x16x32_bf16 v[4:7], v[130:133], v[236:239], v[4:7]
	v_mfma_f32_16x16x32_bf16 v[0:3], v[138:141], v[236:239], v[0:3]
	v_mfma_f32_16x16x32_bf16 v[60:63], v[134:137], v[168:171], v[60:63]
	v_mfma_f32_16x16x32_bf16 v[56:59], v[142:145], v[168:171], v[56:59]
	v_mfma_f32_16x16x32_bf16 v[40:43], v[134:137], v[176:179], v[40:43]
	v_mfma_f32_16x16x32_bf16 v[32:35], v[142:145], v[176:179], v[32:35]
	v_mfma_f32_16x16x32_bf16 v[16:19], v[134:137], v[184:187], v[16:19]
	v_mfma_f32_16x16x32_bf16 v[8:11], v[142:145], v[184:187], v[8:11]
	v_mfma_f32_16x16x32_bf16 v[4:7], v[134:137], v[240:243], v[4:7]
	v_mfma_f32_16x16x32_bf16 v[0:3], v[142:145], v[240:243], v[0:3]
	s_setprio 0
	s_setprio 1
	v_mfma_f32_16x16x32_bf16 v[44:47], v[146:149], v[164:167], v[44:47]
	v_mfma_f32_16x16x32_bf16 v[36:39], v[154:157], v[164:167], v[36:39]
	v_mfma_f32_16x16x32_bf16 v[20:23], v[146:149], v[172:175], v[20:23]
	v_mfma_f32_16x16x32_bf16 v[12:15], v[154:157], v[172:175], v[12:15]
	v_mfma_f32_16x16x32_bf16 v[52:55], v[146:149], v[180:183], v[52:55]
	v_mfma_f32_16x16x32_bf16 v[48:51], v[154:157], v[180:183], v[48:51]
	v_mfma_f32_16x16x32_bf16 v[28:31], v[146:149], v[236:239], v[28:31]
	v_mfma_f32_16x16x32_bf16 v[24:27], v[154:157], v[236:239], v[24:27]
	v_mfma_f32_16x16x32_bf16 v[44:47], v[150:153], v[168:171], v[44:47]
	v_mfma_f32_16x16x32_bf16 v[36:39], v[158:161], v[168:171], v[36:39]
	v_mfma_f32_16x16x32_bf16 v[20:23], v[150:153], v[176:179], v[20:23]
	v_mfma_f32_16x16x32_bf16 v[12:15], v[158:161], v[176:179], v[12:15]
	v_mfma_f32_16x16x32_bf16 v[52:55], v[150:153], v[184:187], v[52:55]
	v_mfma_f32_16x16x32_bf16 v[48:51], v[158:161], v[184:187], v[48:51]
	v_mfma_f32_16x16x32_bf16 v[28:31], v[150:153], v[240:243], v[28:31]
	v_mfma_f32_16x16x32_bf16 v[24:27], v[158:161], v[240:243], v[24:27]
	s_setprio 0
	s_barrier
	s_add_i32 s65, 0, 0x18000
	v_add_u32_e32 v96, s65, v197
	s_add_i32 s66, 0, 0x1c000
	ds_read_b128 v[130:133], v96
	ds_read_b128 v[134:137], v96 offset:1024
	ds_read_b128 v[138:141], v96 offset:2048
	ds_read_b128 v[142:145], v96 offset:3072
	v_add_u32_e32 v96, s66, v197
	ds_read_b128 v[146:149], v96
	ds_read_b128 v[150:153], v96 offset:1024
	ds_read_b128 v[154:157], v96 offset:2048
	ds_read_b128 v[158:161], v96 offset:3072
	v_mov_b32_e32 v96, v191
	s_mov_b32 m0, s57
	ds_read_b128 v[164:167], v228 offset:32768
	ds_read_b128 v[168:171], v228 offset:33792
	ds_read_b128 v[172:175], v228 offset:34816
	ds_read_b128 v[176:179], v228 offset:35840
	ds_read_b128 v[180:183], v228 offset:36864
	ds_read_b128 v[184:187], v228 offset:37888
	ds_read_b128 v[236:239], v228 offset:38912
	ds_read_b128 v[240:243], v228 offset:39936
	s_nop 0
	global_load_lds_dwordx4 v96, s[4:5]
	v_mov_b32_e32 v96, v194
	s_mov_b32 m0, s58
	s_nop 0
	global_load_lds_dwordx4 v96, s[4:5]
	s_waitcnt vmcnt(8)
	s_waitcnt lgkmcnt(0)
	s_barrier
	s_setprio 1
	s_waitcnt lgkmcnt(0)
	v_mfma_f32_16x16x32_bf16 v[126:129], v[130:133], v[164:167], v[126:129]
	v_mfma_f32_16x16x32_bf16 v[122:125], v[138:141], v[164:167], v[122:125]
	v_mfma_f32_16x16x32_bf16 v[114:117], v[130:133], v[172:175], v[114:117]
	v_mfma_f32_16x16x32_bf16 v[106:109], v[138:141], v[172:175], v[106:109]
	v_mfma_f32_16x16x32_bf16 v[98:101], v[130:133], v[180:183], v[98:101]
	v_mfma_f32_16x16x32_bf16 v[88:91], v[138:141], v[180:183], v[88:91]
	v_mfma_f32_16x16x32_bf16 v[80:83], v[130:133], v[236:239], v[80:83]
	v_mfma_f32_16x16x32_bf16 v[72:75], v[138:141], v[236:239], v[72:75]
	v_mfma_f32_16x16x32_bf16 v[126:129], v[134:137], v[168:171], v[126:129]
	v_mfma_f32_16x16x32_bf16 v[122:125], v[142:145], v[168:171], v[122:125]
	v_mfma_f32_16x16x32_bf16 v[114:117], v[134:137], v[176:179], v[114:117]
	v_mfma_f32_16x16x32_bf16 v[106:109], v[142:145], v[176:179], v[106:109]
	v_mfma_f32_16x16x32_bf16 v[98:101], v[134:137], v[184:187], v[98:101]
	v_mfma_f32_16x16x32_bf16 v[88:91], v[142:145], v[184:187], v[88:91]
	v_mfma_f32_16x16x32_bf16 v[80:83], v[134:137], v[240:243], v[80:83]
	v_mfma_f32_16x16x32_bf16 v[72:75], v[142:145], v[240:243], v[72:75]
	s_setprio 0
	s_setprio 1
	v_mfma_f32_16x16x32_bf16 v[118:121], v[146:149], v[164:167], v[118:121]
	v_mfma_f32_16x16x32_bf16 v[110:113], v[154:157], v[164:167], v[110:113]
	v_mfma_f32_16x16x32_bf16 v[102:105], v[146:149], v[172:175], v[102:105]
	v_mfma_f32_16x16x32_bf16 v[92:95], v[154:157], v[172:175], v[92:95]
	v_mfma_f32_16x16x32_bf16 v[84:87], v[146:149], v[180:183], v[84:87]
	v_mfma_f32_16x16x32_bf16 v[76:79], v[154:157], v[180:183], v[76:79]
	v_mfma_f32_16x16x32_bf16 v[68:71], v[146:149], v[236:239], v[68:71]
	v_mfma_f32_16x16x32_bf16 v[64:67], v[154:157], v[236:239], v[64:67]
	v_mfma_f32_16x16x32_bf16 v[118:121], v[150:153], v[168:171], v[118:121]
	v_mfma_f32_16x16x32_bf16 v[110:113], v[158:161], v[168:171], v[110:113]
	v_mfma_f32_16x16x32_bf16 v[102:105], v[150:153], v[176:179], v[102:105]
	v_mfma_f32_16x16x32_bf16 v[92:95], v[158:161], v[176:179], v[92:95]
	v_mfma_f32_16x16x32_bf16 v[84:87], v[150:153], v[184:187], v[84:87]
	v_mfma_f32_16x16x32_bf16 v[76:79], v[158:161], v[184:187], v[76:79]
	v_mfma_f32_16x16x32_bf16 v[68:71], v[150:153], v[240:243], v[68:71]
	v_mfma_f32_16x16x32_bf16 v[64:67], v[158:161], v[240:243], v[64:67]
	s_setprio 0
	s_barrier
; #define PG8_STAGE(bufoff, gbase, voff) do { _Pragma("unroll") for (int _i = 0; _i < 2; ++_i) \
;         __builtin_amdgcn_global_load_lds((const __attribute__((address_space(1))) unsigned*)((const __attribute__((address_space(1))) char*)(gbase) + (unsigned)lnd_v((int)(voff)[_i])), (LAS unsigned*)(lds + (bufoff) + ldsw + _i * 8192), 16, 0, 0); } while (0)
; #define PG8_LDA(dst, b, h) do { _Pragma("unroll") for (int m = 0; m < 4; ++m) _Pragma("unroll") for (int k = 0; k < 2; ++k) dst[m][k] = *(const LAS bf16x8*)(lds + PG8_SA(b, h) + aoff + m * 2048 + k * 1024); } while (0)
; #define PG8_MMA(ai, bj, At, Bt) do { __builtin_amdgcn_s_setprio(1); _Pragma("unroll") for (int m = 0; m < 4; ++m) _Pragma("unroll") for (int n = 0; n < 2; ++n) _Pragma("unroll") for (int k = 0; k < 2; ++k) \
;         acc[ai][bj][m][n] = __builtin_amdgcn_mfma_f32_16x16x32_bf16(Bt[n][k], At[m][k], acc[ai][bj][m][n], 0, 0, 0); __builtin_amdgcn_s_setprio(0); } while (0)
; #define PG8_WAIT_V(n) asm volatile("s_waitcnt vmcnt(" #n ")" ::: "memory")
; #define PG8_WAIT_L(n) asm volatile("s_waitcnt lgkmcnt(" #n ")" ::: "memory")
; #define PG8_BAR __builtin_amdgcn_s_barrier()
; #define PG8_SCHED __builtin_amdgcn_sched_barrier(0)
; template <class Desc, class Epi>
; __device__ __forceinline__ void gemm_phase(const int wv_, LAS unsigned char* lds, const Desc& d, const Epi& E) {
;     ...
;             PG8_LDA(At, 1, 1); PG8_STAGE(PG8_SB(1, 0), b3, voffB); PG8_STAGE(PG8_SB(1, 1), b3 + hstepB, voffB); PG8_STAGE(PG8_SA(1, 0), a3, sA0);
;             PG8_WAIT_V(8); PG8_WAIT_L(0); PG8_BAR; PG8_MMA(1, 0, At, B0); PG8_MMA(1, 1, At, B1); PG8_BAR; PG8_SCHED;
;         }
;         if (wr == 0) PG8_BAR;
	v_mov_b32_e32 v96, v192
	ds_read_b128 v[164:167], v228 offset:49152
	ds_read_b128 v[168:171], v228 offset:50176
	ds_read_b128 v[172:175], v228 offset:51200
	ds_read_b128 v[176:179], v228 offset:52224
	ds_read_b128 v[180:183], v228 offset:53248
	ds_read_b128 v[184:187], v228 offset:54272
	ds_read_b128 v[236:239], v228 offset:55296
	ds_read_b128 v[240:243], v228 offset:56320
	s_add_i32 s65, s65, s54
	v_lshl_add_u64 v[234:235], s[20:21], 0, v[96:97]
	v_lshl_add_u64 v[234:235], v[234:235], 0, s[30:31]
	s_mov_b32 m0, s65
	v_mov_b32_e32 v96, v195
	global_load_lds_dwordx4 v[234:235], off
	s_add_i32 m0, s65, 0x2000
	s_nop 0
	v_lshl_add_u64 v[234:235], s[20:21], 0, v[96:97]
	s_add_u32 s20, s20, 0x40080
	v_lshl_add_u64 v[234:235], v[234:235], 0, s[30:31]
	s_addc_u32 s21, s21, 0
	v_mov_b32_e32 v96, v192
	s_add_i32 s65, s66, s54
	global_load_lds_dwordx4 v[234:235], off
	s_mov_b32 m0, s65
	s_nop 0
	global_load_lds_dwordx4 v96, s[20:21]
	v_mov_b32_e32 v96, v195
	s_add_i32 m0, s65, 0x2000
	s_nop 0
	global_load_lds_dwordx4 v96, s[20:21]
	v_mov_b32_e32 v96, v190
	s_mov_b32 m0, s59
	v_lshl_add_u64 v[234:235], s[4:5], 0, v[96:97]
	v_lshl_add_u64 v[234:235], v[234:235], 0, s[30:31]
	v_mov_b32_e32 v96, v193
	global_load_lds_dwordx4 v[234:235], off
	s_mov_b32 m0, s60
	v_lshl_add_u64 v[234:235], s[4:5], 0, v[96:97]
	v_lshl_add_u64 v[234:235], v[234:235], 0, s[30:31]
	global_load_lds_dwordx4 v[234:235], off
	s_waitcnt vmcnt(8)
	s_waitcnt lgkmcnt(0)
	s_barrier
	s_setprio 1
	s_waitcnt lgkmcnt(0)
	v_mfma_f32_16x16x32_bf16 v[60:63], v[130:133], v[164:167], v[60:63]
	v_mfma_f32_16x16x32_bf16 v[56:59], v[138:141], v[164:167], v[56:59]
	v_mfma_f32_16x16x32_bf16 v[40:43], v[130:133], v[172:175], v[40:43]
	v_mfma_f32_16x16x32_bf16 v[32:35], v[138:141], v[172:175], v[32:35]
	v_mfma_f32_16x16x32_bf16 v[16:19], v[130:133], v[180:183], v[16:19]
	v_mfma_f32_16x16x32_bf16 v[8:11], v[138:141], v[180:183], v[8:11]
	v_mfma_f32_16x16x32_bf16 v[4:7], v[130:133], v[236:239], v[4:7]
	v_mfma_f32_16x16x32_bf16 v[0:3], v[138:141], v[236:239], v[0:3]
	v_mfma_f32_16x16x32_bf16 v[60:63], v[134:137], v[168:171], v[60:63]
	v_mfma_f32_16x16x32_bf16 v[56:59], v[142:145], v[168:171], v[56:59]
	v_mfma_f32_16x16x32_bf16 v[40:43], v[134:137], v[176:179], v[40:43]
	v_mfma_f32_16x16x32_bf16 v[32:35], v[142:145], v[176:179], v[32:35]
	v_mfma_f32_16x16x32_bf16 v[16:19], v[134:137], v[184:187], v[16:19]
	v_mfma_f32_16x16x32_bf16 v[8:11], v[142:145], v[184:187], v[8:11]
	v_mfma_f32_16x16x32_bf16 v[4:7], v[134:137], v[240:243], v[4:7]
	v_mfma_f32_16x16x32_bf16 v[0:3], v[142:145], v[240:243], v[0:3]
	s_setprio 0
	s_setprio 1
	v_mfma_f32_16x16x32_bf16 v[44:47], v[146:149], v[164:167], v[44:47]
	v_mfma_f32_16x16x32_bf16 v[36:39], v[154:157], v[164:167], v[36:39]
	v_mfma_f32_16x16x32_bf16 v[20:23], v[146:149], v[172:175], v[20:23]
	v_mfma_f32_16x16x32_bf16 v[12:15], v[154:157], v[172:175], v[12:15]
	v_mfma_f32_16x16x32_bf16 v[52:55], v[146:149], v[180:183], v[52:55]
	v_mfma_f32_16x16x32_bf16 v[48:51], v[154:157], v[180:183], v[48:51]
	v_mfma_f32_16x16x32_bf16 v[28:31], v[146:149], v[236:239], v[28:31]
	v_mfma_f32_16x16x32_bf16 v[24:27], v[154:157], v[236:239], v[24:27]
	v_mfma_f32_16x16x32_bf16 v[44:47], v[150:153], v[168:171], v[44:47]
	v_mfma_f32_16x16x32_bf16 v[36:39], v[158:161], v[168:171], v[36:39]
	v_mfma_f32_16x16x32_bf16 v[20:23], v[150:153], v[176:179], v[20:23]
	v_mfma_f32_16x16x32_bf16 v[12:15], v[158:161], v[176:179], v[12:15]
	v_mfma_f32_16x16x32_bf16 v[52:55], v[150:153], v[184:187], v[52:55]
	v_mfma_f32_16x16x32_bf16 v[48:51], v[158:161], v[184:187], v[48:51]
	v_mfma_f32_16x16x32_bf16 v[28:31], v[150:153], v[240:243], v[28:31]
	v_mfma_f32_16x16x32_bf16 v[24:27], v[158:161], v[240:243], v[24:27]
	s_setprio 0
	s_barrier
	s_add_i32 s45, s45, 2
	s_add_u32 s2, s2, 0x100
	s_addc_u32 s3, s3, 0
	s_add_u32 s1, s1, 0x100
	s_addc_u32 s29, s29, 0
	s_cmp_gt_u32 s45, 13
	s_cbranch_scc0 .LBB0_1161
	s_and_b64 vcc, exec, s[42:43]
	s_cbranch_vccz .LBB0_1164
	s_barrier

; #define PG8_AOFF(ord, U, O0, O1) do { _Pragma("unroll") for (int _i = 0; _i < 2; ++_i) { \
;         O0[_i] = d.rowbyte(U, (int)tix[(ord) * 256 + Rr[_i]]) + (unsigned)(Cc[_i] * 2); O1[_i] = d.rowbyte(U, (int)tix[(ord) * 256 + HALF + Rr[_i]]) + (unsigned)(Cc[_i] * 2); } } while (0)
; #define PG8_STAGE(bufoff, gbase, voff) do { _Pragma("unroll") for (int _i = 0; _i < 2; ++_i) \
;         __builtin_amdgcn_global_load_lds((const __attribute__((address_space(1))) unsigned*)((const __attribute__((address_space(1))) char*)(gbase) + (unsigned)lnd_v((int)(voff)[_i])), (LAS unsigned*)(lds + (bufoff) + ldsw + _i * 8192), 16, 0, 0); } while (0)
; #define PG8_BAR __builtin_amdgcn_s_barrier()
; template <class Desc, class Epi>
; __device__ __forceinline__ void gemm_phase(const int wv_, LAS unsigned char* lds, const Desc& d, const Epi& E) {
;     ...
;         const int inext = bid + (ui + 1) * nblk; const bool has_next = inext < d.nunits;
;         if (has_next) d.unit(inext, nxt);
;         if constexpr (Desc::GATHER) { if (has_next) PG8_AOFF(ui + 1, nxt, voffAn, voffAn1); else { voffAn[0] = voffA[0]; voffAn[1] = voffA[1]; voffAn1[0] = voffA1[0]; voffAn1[1] = voffA1[1]; } }
;         const char* nA = has_next ? (const char*)nxt.a : cA; const char* nB = has_next ? (const char*)nxt.b : cB;
;         for (int t = 0; t < nt; t += 2) {
;             const bool last = (t == nt - 2);
;             unsigned sA0[2], sA1[2];
;             if constexpr (Desc::GATHER) { sA0[0] = last ? voffAn[0] : voffA[0]; sA0[1] = last ? voffAn[1] : voffA[1]; sA1[0] = last ? voffAn1[0] : voffA1[0]; sA1[1] = last ? voffAn1[1] : voffA1[1]; }
;             else { sA0[0] = voffA[0]; sA0[1] = voffA[1]; sA1[0] = voffA1[0]; sA1[1] = voffA1[1]; }
;             const char* a1 = cA + (size_t)(t + 1) * kstep;
;             const char* a2 = last ? nA : cA + (size_t)(t + 2) * kstep; const char* b2 = last ? nB : cB + (size_t)(t + 2) * kstep;
;             const char* a3 = a2 + kstep; const char* b3 = b2 + kstep;
;             PG8_LDB(B0, 0, 0); PG8_LDB(B1, 0, 1); PG8_SCHED; PG8_LDA(At, 0, 0); PG8_STAGE(PG8_SA(1, 1), a1, voffA1);
;             PG8_WAIT_V(8); PG8_WAIT_L(0); PG8_BAR; PG8_MMA(0, 0, At, B0); PG8_MMA(0, 1, At, B1); PG8_BAR; PG8_SCHED;
;             PG8_LDA(At, 0, 1); PG8_STAGE(PG8_SB(0, 0), b2, voffB); PG8_STAGE(PG8_SB(0, 1), b2 + hstepB, voffB); PG8_STAGE(PG8_SA(0, 0), a2, sA0);
.LBB0_1262:
	s_add_u32 s4, s2, 0x80
	s_addc_u32 s5, s3, 0
	s_add_i32 s62, 0, 0x10000
	s_cmp_eq_u32 s61, 12
	s_cselect_b32 s5, s45, s5
	s_cselect_b32 s4, s44, s4
	v_add_u32_e32 v96, s62, v213
	s_cselect_b32 s21, s47, s43
	s_cselect_b32 s20, s46, s29
	s_add_i32 s64, 0, 0x14000
	ds_read_b128 v[130:133], v96
	ds_read_b128 v[134:137], v96 offset:1024
	ds_read_b128 v[138:141], v96 offset:2048
	ds_read_b128 v[142:145], v96 offset:3072
	v_add_u32_e32 v96, s64, v213
	ds_read_b128 v[146:149], v96
	ds_read_b128 v[150:153], v96 offset:1024
	ds_read_b128 v[154:157], v96 offset:2048
	ds_read_b128 v[158:161], v96 offset:3072
	v_mov_b32_e32 v96, v207
	ds_read_b128 v[164:167], v221
	ds_read_b128 v[168:171], v221 offset:1024
	ds_read_b128 v[172:175], v221 offset:2048
	ds_read_b128 v[176:179], v221 offset:3072
	ds_read_b128 v[180:183], v221 offset:4096
	ds_read_b128 v[184:187], v221 offset:5120
	ds_read_b128 v[188:191], v221 offset:6144
	ds_read_b128 v[224:227], v221 offset:7168
	s_add_i32 m0, s53, 0xc000
	s_nop 0
	global_load_lds_dwordx4 v96, s[2:3]
	v_mov_b32_e32 v96, v210
	s_add_i32 m0, s53, 0xe000
	s_nop 0
	global_load_lds_dwordx4 v96, s[2:3]
	s_waitcnt vmcnt(8)
	s_waitcnt lgkmcnt(0)
	s_barrier
	s_setprio 1
	s_waitcnt lgkmcnt(0)
	v_mfma_f32_16x16x32_bf16 v[126:129], v[130:133], v[164:167], v[126:129]
	v_mfma_f32_16x16x32_bf16 v[122:125], v[138:141], v[164:167], v[122:125]
	v_mfma_f32_16x16x32_bf16 v[110:113], v[130:133], v[172:175], v[110:113]
	v_mfma_f32_16x16x32_bf16 v[106:109], v[138:141], v[172:175], v[106:109]
	v_mfma_f32_16x16x32_bf16 v[92:95], v[130:133], v[180:183], v[92:95]
	v_mfma_f32_16x16x32_bf16 v[88:91], v[138:141], v[180:183], v[88:91]
	v_mfma_f32_16x16x32_bf16 v[76:79], v[130:133], v[188:191], v[76:79]
	v_mfma_f32_16x16x32_bf16 v[72:75], v[138:141], v[188:191], v[72:75]
	v_mfma_f32_16x16x32_bf16 v[126:129], v[134:137], v[168:171], v[126:129]
	v_mfma_f32_16x16x32_bf16 v[122:125], v[142:145], v[168:171], v[122:125]
	v_mfma_f32_16x16x32_bf16 v[110:113], v[134:137], v[176:179], v[110:113]
	v_mfma_f32_16x16x32_bf16 v[106:109], v[142:145], v[176:179], v[106:109]
	v_mfma_f32_16x16x32_bf16 v[92:95], v[134:137], v[184:187], v[92:95]
	v_mfma_f32_16x16x32_bf16 v[88:91], v[142:145], v[184:187], v[88:91]
	v_mfma_f32_16x16x32_bf16 v[76:79], v[134:137], v[224:227], v[76:79]
	v_mfma_f32_16x16x32_bf16 v[72:75], v[142:145], v[224:227], v[72:75]
	s_setprio 0
	s_setprio 1
	v_mfma_f32_16x16x32_bf16 v[118:121], v[146:149], v[164:167], v[118:121]
	v_mfma_f32_16x16x32_bf16 v[114:117], v[154:157], v[164:167], v[114:117]
	v_mfma_f32_16x16x32_bf16 v[102:105], v[146:149], v[172:175], v[102:105]
	v_mfma_f32_16x16x32_bf16 v[98:101], v[154:157], v[172:175], v[98:101]
	v_mfma_f32_16x16x32_bf16 v[84:87], v[146:149], v[180:183], v[84:87]
	v_mfma_f32_16x16x32_bf16 v[80:83], v[154:157], v[180:183], v[80:83]
	v_mfma_f32_16x16x32_bf16 v[68:71], v[146:149], v[188:191], v[68:71]
	v_mfma_f32_16x16x32_bf16 v[64:67], v[154:157], v[188:191], v[64:67]
	v_mfma_f32_16x16x32_bf16 v[118:121], v[150:153], v[168:171], v[118:121]
	v_mfma_f32_16x16x32_bf16 v[114:117], v[158:161], v[168:171], v[114:117]
	v_mfma_f32_16x16x32_bf16 v[102:105], v[150:153], v[176:179], v[102:105]
	v_mfma_f32_16x16x32_bf16 v[98:101], v[158:161], v[176:179], v[98:101]
	v_mfma_f32_16x16x32_bf16 v[84:87], v[150:153], v[184:187], v[84:87]
	v_mfma_f32_16x16x32_bf16 v[80:83], v[158:161], v[184:187], v[80:83]
	v_mfma_f32_16x16x32_bf16 v[68:71], v[150:153], v[224:227], v[68:71]
	v_mfma_f32_16x16x32_bf16 v[64:67], v[158:161], v[224:227], v[64:67]
	s_setprio 0
	s_barrier
	v_mov_b32_e32 v96, v208
	s_add_i32 s62, s62, s52
	ds_read_b128 v[164:167], v221 offset:16384
	ds_read_b128 v[168:171], v221 offset:17408
	ds_read_b128 v[172:175], v221 offset:18432
	ds_read_b128 v[176:179], v221 offset:19456
	ds_read_b128 v[180:183], v221 offset:20480
	ds_read_b128 v[184:187], v221 offset:21504
	ds_read_b128 v[188:191], v221 offset:22528
	ds_read_b128 v[224:227], v221 offset:23552
	s_mov_b32 m0, s62
	s_nop 0
	global_load_lds_dwordx4 v96, s[20:21]
	v_mov_b32_e32 v96, v211
	s_add_i32 m0, s62, 0x2000
	s_add_u32 s62, s20, 0x40000
	global_load_lds_dwordx4 v96, s[20:21]
	s_addc_u32 s63, s21, 0
	v_mov_b32_e32 v96, v208
	s_add_i32 s64, s64, s52
	s_mov_b32 m0, s64
	s_nop 0
	global_load_lds_dwordx4 v96, s[62:63]
	v_mov_b32_e32 v96, v211
	s_add_i32 m0, s64, 0x2000
	s_nop 0
	global_load_lds_dwordx4 v96, s[62:63]
	v_mov_b32_e32 v96, v206
	s_mov_b32 m0, s53
	s_nop 0
	global_load_lds_dwordx4 v96, s[4:5]
	v_mov_b32_e32 v96, v209
	s_mov_b32 m0, s54
	s_nop 0
	global_load_lds_dwordx4 v96, s[4:5]
	s_waitcnt vmcnt(8)
	s_waitcnt lgkmcnt(0)
	s_barrier
; #define PG8_STAGE(bufoff, gbase, voff) do { _Pragma("unroll") for (int _i = 0; _i < 2; ++_i) \
;         __builtin_amdgcn_global_load_lds((const __attribute__((address_space(1))) unsigned*)((const __attribute__((address_space(1))) char*)(gbase) + (unsigned)lnd_v((int)(voff)[_i])), (LAS unsigned*)(lds + (bufoff) + ldsw + _i * 8192), 16, 0, 0); } while (0)
; #define PG8_LDA(dst, b, h) do { _Pragma("unroll") for (int m = 0; m < 4; ++m) _Pragma("unroll") for (int k = 0; k < 2; ++k) dst[m][k] = *(const LAS bf16x8*)(lds + PG8_SA(b, h) + aoff + m * 2048 + k * 1024); } while (0)
; #define PG8_LDB(dst, b, h) do { _Pragma("unroll") for (int n = 0; n < 2; ++n) _Pragma("unroll") for (int k = 0; k < 2; ++k) dst[n][k] = *(const LAS bf16x8*)(lds + PG8_SB(b, h) + boff + n * 2048 + k * 1024); } while (0)
; #define PG8_MMA(ai, bj, At, Bt) do { __builtin_amdgcn_s_setprio(1); _Pragma("unroll") for (int m = 0; m < 4; ++m) _Pragma("unroll") for (int n = 0; n < 2; ++n) _Pragma("unroll") for (int k = 0; k < 2; ++k) \
;         acc[ai][bj][m][n] = __builtin_amdgcn_mfma_f32_16x16x32_bf16(Bt[n][k], At[m][k], acc[ai][bj][m][n], 0, 0, 0); __builtin_amdgcn_s_setprio(0); } while (0)
; #define PG8_WAIT_V(n) asm volatile("s_waitcnt vmcnt(" #n ")" ::: "memory")
; #define PG8_WAIT_L(n) asm volatile("s_waitcnt lgkmcnt(" #n ")" ::: "memory")
; #define PG8_BAR __builtin_amdgcn_s_barrier()
; #define PG8_SCHED __builtin_amdgcn_sched_barrier(0)
; template <class Desc, class Epi>
; __device__ __forceinline__ void gemm_phase(const int wv_, LAS unsigned char* lds, const Desc& d, const Epi& E) {
;     ...
;             PG8_WAIT_V(8); PG8_WAIT_L(0); PG8_BAR; PG8_MMA(1, 0, At, B0); PG8_MMA(1, 1, At, B1); PG8_BAR; PG8_SCHED;
;             PG8_LDB(B0, 1, 0); PG8_LDB(B1, 1, 1); PG8_SCHED; PG8_LDA(At, 1, 0); PG8_STAGE(PG8_SA(0, 1), a2, sA1);
;             PG8_WAIT_V(8); PG8_WAIT_L(0); PG8_BAR; PG8_MMA(0, 0, At, B0); PG8_MMA(0, 1, At, B1); PG8_BAR; PG8_SCHED;
	s_setprio 1
	s_waitcnt lgkmcnt(0)
	v_mfma_f32_16x16x32_bf16 v[60:63], v[130:133], v[164:167], v[60:63]
	v_mfma_f32_16x16x32_bf16 v[56:59], v[138:141], v[164:167], v[56:59]
	v_mfma_f32_16x16x32_bf16 v[44:47], v[130:133], v[172:175], v[44:47]
	v_mfma_f32_16x16x32_bf16 v[40:43], v[138:141], v[172:175], v[40:43]
	v_mfma_f32_16x16x32_bf16 v[24:27], v[130:133], v[180:183], v[24:27]
	v_mfma_f32_16x16x32_bf16 v[16:19], v[138:141], v[180:183], v[16:19]
	v_mfma_f32_16x16x32_bf16 v[4:7], v[130:133], v[188:191], v[4:7]
	v_mfma_f32_16x16x32_bf16 v[0:3], v[138:141], v[188:191], v[0:3]
	v_mfma_f32_16x16x32_bf16 v[60:63], v[134:137], v[168:171], v[60:63]
	v_mfma_f32_16x16x32_bf16 v[56:59], v[142:145], v[168:171], v[56:59]
	v_mfma_f32_16x16x32_bf16 v[44:47], v[134:137], v[176:179], v[44:47]
	v_mfma_f32_16x16x32_bf16 v[40:43], v[142:145], v[176:179], v[40:43]
	v_mfma_f32_16x16x32_bf16 v[24:27], v[134:137], v[184:187], v[24:27]
	v_mfma_f32_16x16x32_bf16 v[16:19], v[142:145], v[184:187], v[16:19]
	v_mfma_f32_16x16x32_bf16 v[4:7], v[134:137], v[224:227], v[4:7]
	v_mfma_f32_16x16x32_bf16 v[0:3], v[142:145], v[224:227], v[0:3]
	s_setprio 0
	s_setprio 1
	v_mfma_f32_16x16x32_bf16 v[52:55], v[146:149], v[164:167], v[52:55]
	v_mfma_f32_16x16x32_bf16 v[48:51], v[154:157], v[164:167], v[48:51]
	v_mfma_f32_16x16x32_bf16 v[28:31], v[146:149], v[172:175], v[28:31]
	v_mfma_f32_16x16x32_bf16 v[20:23], v[154:157], v[172:175], v[20:23]
	v_mfma_f32_16x16x32_bf16 v[36:39], v[146:149], v[180:183], v[36:39]
	v_mfma_f32_16x16x32_bf16 v[32:35], v[154:157], v[180:183], v[32:35]
	v_mfma_f32_16x16x32_bf16 v[12:15], v[146:149], v[188:191], v[12:15]
	v_mfma_f32_16x16x32_bf16 v[8:11], v[154:157], v[188:191], v[8:11]
	v_mfma_f32_16x16x32_bf16 v[52:55], v[150:153], v[168:171], v[52:55]
	v_mfma_f32_16x16x32_bf16 v[48:51], v[158:161], v[168:171], v[48:51]
	v_mfma_f32_16x16x32_bf16 v[28:31], v[150:153], v[176:179], v[28:31]
	v_mfma_f32_16x16x32_bf16 v[20:23], v[158:161], v[176:179], v[20:23]
	v_mfma_f32_16x16x32_bf16 v[36:39], v[150:153], v[184:187], v[36:39]
	v_mfma_f32_16x16x32_bf16 v[32:35], v[158:161], v[184:187], v[32:35]
	v_mfma_f32_16x16x32_bf16 v[12:15], v[150:153], v[224:227], v[12:15]
	v_mfma_f32_16x16x32_bf16 v[8:11], v[158:161], v[224:227], v[8:11]
	s_setprio 0
	s_barrier
	s_add_i32 s62, 0, 0x18000
	v_add_u32_e32 v96, s62, v213
	s_add_i32 s63, 0, 0x1c000
	ds_read_b128 v[130:133], v96
	ds_read_b128 v[134:137], v96 offset:1024
	ds_read_b128 v[138:141], v96 offset:2048
	ds_read_b128 v[142:145], v96 offset:3072
	v_add_u32_e32 v96, s63, v213
	ds_read_b128 v[146:149], v96
	ds_read_b128 v[150:153], v96 offset:1024
	ds_read_b128 v[154:157], v96 offset:2048
	ds_read_b128 v[158:161], v96 offset:3072
	v_mov_b32_e32 v96, v207
	s_mov_b32 m0, s55
	ds_read_b128 v[164:167], v221 offset:32768
	ds_read_b128 v[168:171], v221 offset:33792
	ds_read_b128 v[172:175], v221 offset:34816
	ds_read_b128 v[176:179], v221 offset:35840
	ds_read_b128 v[180:183], v221 offset:36864
	ds_read_b128 v[184:187], v221 offset:37888
	ds_read_b128 v[188:191], v221 offset:38912
	ds_read_b128 v[224:227], v221 offset:39936
	s_nop 0
	global_load_lds_dwordx4 v96, s[4:5]
	v_mov_b32_e32 v96, v210
	s_mov_b32 m0, s56
	s_nop 0
	global_load_lds_dwordx4 v96, s[4:5]
	s_waitcnt vmcnt(8)
	s_waitcnt lgkmcnt(0)
	s_barrier
	s_setprio 1
	s_waitcnt lgkmcnt(0)
	v_mfma_f32_16x16x32_bf16 v[126:129], v[130:133], v[164:167], v[126:129]
	v_mfma_f32_16x16x32_bf16 v[122:125], v[138:141], v[164:167], v[122:125]
	v_mfma_f32_16x16x32_bf16 v[110:113], v[130:133], v[172:175], v[110:113]
	v_mfma_f32_16x16x32_bf16 v[106:109], v[138:141], v[172:175], v[106:109]
	v_mfma_f32_16x16x32_bf16 v[92:95], v[130:133], v[180:183], v[92:95]
	v_mfma_f32_16x16x32_bf16 v[88:91], v[138:141], v[180:183], v[88:91]
	v_mfma_f32_16x16x32_bf16 v[76:79], v[130:133], v[188:191], v[76:79]
	v_mfma_f32_16x16x32_bf16 v[72:75], v[138:141], v[188:191], v[72:75]
	v_mfma_f32_16x16x32_bf16 v[126:129], v[134:137], v[168:171], v[126:129]
	v_mfma_f32_16x16x32_bf16 v[122:125], v[142:145], v[168:171], v[122:125]
	v_mfma_f32_16x16x32_bf16 v[110:113], v[134:137], v[176:179], v[110:113]
	v_mfma_f32_16x16x32_bf16 v[106:109], v[142:145], v[176:179], v[106:109]
	v_mfma_f32_16x16x32_bf16 v[92:95], v[134:137], v[184:187], v[92:95]
	v_mfma_f32_16x16x32_bf16 v[88:91], v[142:145], v[184:187], v[88:91]
	v_mfma_f32_16x16x32_bf16 v[76:79], v[134:137], v[224:227], v[76:79]
	v_mfma_f32_16x16x32_bf16 v[72:75], v[142:145], v[224:227], v[72:75]
	s_setprio 0
	s_setprio 1
	v_mfma_f32_16x16x32_bf16 v[118:121], v[146:149], v[164:167], v[118:121]
	v_mfma_f32_16x16x32_bf16 v[114:117], v[154:157], v[164:167], v[114:117]
	v_mfma_f32_16x16x32_bf16 v[102:105], v[146:149], v[172:175], v[102:105]
	v_mfma_f32_16x16x32_bf16 v[98:101], v[154:157], v[172:175], v[98:101]
	v_mfma_f32_16x16x32_bf16 v[84:87], v[146:149], v[180:183], v[84:87]
	v_mfma_f32_16x16x32_bf16 v[80:83], v[154:157], v[180:183], v[80:83]
	v_mfma_f32_16x16x32_bf16 v[68:71], v[146:149], v[188:191], v[68:71]
	v_mfma_f32_16x16x32_bf16 v[64:67], v[154:157], v[188:191], v[64:67]
	v_mfma_f32_16x16x32_bf16 v[118:121], v[150:153], v[168:171], v[118:121]
	v_mfma_f32_16x16x32_bf16 v[114:117], v[158:161], v[168:171], v[114:117]
	v_mfma_f32_16x16x32_bf16 v[102:105], v[150:153], v[176:179], v[102:105]
	v_mfma_f32_16x16x32_bf16 v[98:101], v[158:161], v[176:179], v[98:101]
	v_mfma_f32_16x16x32_bf16 v[84:87], v[150:153], v[184:187], v[84:87]
	v_mfma_f32_16x16x32_bf16 v[80:83], v[158:161], v[184:187], v[80:83]
	v_mfma_f32_16x16x32_bf16 v[68:71], v[150:153], v[224:227], v[68:71]
	v_mfma_f32_16x16x32_bf16 v[64:67], v[158:161], v[224:227], v[64:67]
	s_setprio 0
	s_barrier
; #define PG8_STAGE(bufoff, gbase, voff) do { _Pragma("unroll") for (int _i = 0; _i < 2; ++_i) \
;         __builtin_amdgcn_global_load_lds((const __attribute__((address_space(1))) unsigned*)((const __attribute__((address_space(1))) char*)(gbase) + (unsigned)lnd_v((int)(voff)[_i])), (LAS unsigned*)(lds + (bufoff) + ldsw + _i * 8192), 16, 0, 0); } while (0)
; #define PG8_LDA(dst, b, h) do { _Pragma("unroll") for (int m = 0; m < 4; ++m) _Pragma("unroll") for (int k = 0; k < 2; ++k) dst[m][k] = *(const LAS bf16x8*)(lds + PG8_SA(b, h) + aoff + m * 2048 + k * 1024); } while (0)
; #define PG8_MMA(ai, bj, At, Bt) do { __builtin_amdgcn_s_setprio(1); _Pragma("unroll") for (int m = 0; m < 4; ++m) _Pragma("unroll") for (int n = 0; n < 2; ++n) _Pragma("unroll") for (int k = 0; k < 2; ++k) \
;         acc[ai][bj][m][n] = __builtin_amdgcn_mfma_f32_16x16x32_bf16(Bt[n][k], At[m][k], acc[ai][bj][m][n], 0, 0, 0); __builtin_amdgcn_s_setprio(0); } while (0)
; #define PG8_WAIT_V(n) asm volatile("s_waitcnt vmcnt(" #n ")" ::: "memory")
; #define PG8_WAIT_L(n) asm volatile("s_waitcnt lgkmcnt(" #n ")" ::: "memory")
; #define PG8_BAR __builtin_amdgcn_s_barrier()
; #define PG8_SCHED __builtin_amdgcn_sched_barrier(0)
; template <class Desc, class Epi>
; __device__ __forceinline__ void gemm_phase(const int wv_, LAS unsigned char* lds, const Desc& d, const Epi& E) {
;     ...
;             PG8_LDA(At, 1, 1); PG8_STAGE(PG8_SB(1, 0), b3, voffB); PG8_STAGE(PG8_SB(1, 1), b3 + hstepB, voffB); PG8_STAGE(PG8_SA(1, 0), a3, sA0);
;             PG8_WAIT_V(8); PG8_WAIT_L(0); PG8_BAR; PG8_MMA(1, 0, At, B0); PG8_MMA(1, 1, At, B1); PG8_BAR; PG8_SCHED;
;         }
;         if (wr == 0) PG8_BAR;
	v_mov_b32_e32 v96, v208
	ds_read_b128 v[164:167], v221 offset:49152
	ds_read_b128 v[168:171], v221 offset:50176
	ds_read_b128 v[172:175], v221 offset:51200
	ds_read_b128 v[176:179], v221 offset:52224
	ds_read_b128 v[180:183], v221 offset:53248
	ds_read_b128 v[184:187], v221 offset:54272
	ds_read_b128 v[188:191], v221 offset:55296
	ds_read_b128 v[224:227], v221 offset:56320
	s_add_i32 s62, s62, s52
	v_lshl_add_u64 v[194:195], s[20:21], 0, v[96:97]
	v_lshl_add_u64 v[194:195], v[194:195], 0, s[30:31]
	s_mov_b32 m0, s62
	v_mov_b32_e32 v96, v211
	global_load_lds_dwordx4 v[194:195], off
	s_add_i32 m0, s62, 0x2000
	s_nop 0
	v_lshl_add_u64 v[194:195], s[20:21], 0, v[96:97]
	s_add_u32 s20, s20, 0x40080
	v_lshl_add_u64 v[194:195], v[194:195], 0, s[30:31]
	s_addc_u32 s21, s21, 0
	v_mov_b32_e32 v96, v208
	s_add_i32 s62, s63, s52
	global_load_lds_dwordx4 v[194:195], off
	s_mov_b32 m0, s62
	s_nop 0
	global_load_lds_dwordx4 v96, s[20:21]
	v_mov_b32_e32 v96, v211
	s_add_i32 m0, s62, 0x2000
	s_nop 0
	global_load_lds_dwordx4 v96, s[20:21]
	v_mov_b32_e32 v96, v206
	s_mov_b32 m0, s57
	v_lshl_add_u64 v[194:195], s[4:5], 0, v[96:97]
	v_lshl_add_u64 v[194:195], v[194:195], 0, s[30:31]
	v_mov_b32_e32 v96, v209
	global_load_lds_dwordx4 v[194:195], off
	s_mov_b32 m0, s58
	v_lshl_add_u64 v[194:195], s[4:5], 0, v[96:97]
	v_lshl_add_u64 v[194:195], v[194:195], 0, s[30:31]
	global_load_lds_dwordx4 v[194:195], off
	s_waitcnt vmcnt(8)
	s_waitcnt lgkmcnt(0)
	s_barrier
	s_setprio 1
	s_waitcnt lgkmcnt(0)
	v_mfma_f32_16x16x32_bf16 v[60:63], v[130:133], v[164:167], v[60:63]
	v_mfma_f32_16x16x32_bf16 v[56:59], v[138:141], v[164:167], v[56:59]
	v_mfma_f32_16x16x32_bf16 v[44:47], v[130:133], v[172:175], v[44:47]
	v_mfma_f32_16x16x32_bf16 v[40:43], v[138:141], v[172:175], v[40:43]
	v_mfma_f32_16x16x32_bf16 v[24:27], v[130:133], v[180:183], v[24:27]
	v_mfma_f32_16x16x32_bf16 v[16:19], v[138:141], v[180:183], v[16:19]
	v_mfma_f32_16x16x32_bf16 v[4:7], v[130:133], v[188:191], v[4:7]
	v_mfma_f32_16x16x32_bf16 v[0:3], v[138:141], v[188:191], v[0:3]
	v_mfma_f32_16x16x32_bf16 v[60:63], v[134:137], v[168:171], v[60:63]
	v_mfma_f32_16x16x32_bf16 v[56:59], v[142:145], v[168:171], v[56:59]
	v_mfma_f32_16x16x32_bf16 v[44:47], v[134:137], v[176:179], v[44:47]
	v_mfma_f32_16x16x32_bf16 v[40:43], v[142:145], v[176:179], v[40:43]
	v_mfma_f32_16x16x32_bf16 v[24:27], v[134:137], v[184:187], v[24:27]
	v_mfma_f32_16x16x32_bf16 v[16:19], v[142:145], v[184:187], v[16:19]
	v_mfma_f32_16x16x32_bf16 v[4:7], v[134:137], v[224:227], v[4:7]
	v_mfma_f32_16x16x32_bf16 v[0:3], v[142:145], v[224:227], v[0:3]
	s_setprio 0
	s_setprio 1
	v_mfma_f32_16x16x32_bf16 v[52:55], v[146:149], v[164:167], v[52:55]
	v_mfma_f32_16x16x32_bf16 v[48:51], v[154:157], v[164:167], v[48:51]
	v_mfma_f32_16x16x32_bf16 v[28:31], v[146:149], v[172:175], v[28:31]
	v_mfma_f32_16x16x32_bf16 v[20:23], v[154:157], v[172:175], v[20:23]
	v_mfma_f32_16x16x32_bf16 v[36:39], v[146:149], v[180:183], v[36:39]
	v_mfma_f32_16x16x32_bf16 v[32:35], v[154:157], v[180:183], v[32:35]
	v_mfma_f32_16x16x32_bf16 v[12:15], v[146:149], v[188:191], v[12:15]
	v_mfma_f32_16x16x32_bf16 v[8:11], v[154:157], v[188:191], v[8:11]
	v_mfma_f32_16x16x32_bf16 v[52:55], v[150:153], v[168:171], v[52:55]
	v_mfma_f32_16x16x32_bf16 v[48:51], v[158:161], v[168:171], v[48:51]
	v_mfma_f32_16x16x32_bf16 v[28:31], v[150:153], v[176:179], v[28:31]
	v_mfma_f32_16x16x32_bf16 v[20:23], v[158:161], v[176:179], v[20:23]
	v_mfma_f32_16x16x32_bf16 v[36:39], v[150:153], v[184:187], v[36:39]
	v_mfma_f32_16x16x32_bf16 v[32:35], v[158:161], v[184:187], v[32:35]
	v_mfma_f32_16x16x32_bf16 v[12:15], v[150:153], v[224:227], v[12:15]
	v_mfma_f32_16x16x32_bf16 v[8:11], v[158:161], v[224:227], v[8:11]
	s_setprio 0
	s_barrier
	s_add_i32 s61, s61, 2
	s_add_u32 s2, s2, 0x100
	s_addc_u32 s3, s3, 0
	s_add_u32 s29, s29, 0x100
	s_addc_u32 s43, s43, 0
	s_cmp_gt_u32 s61, 13
	s_cbranch_scc0 .LBB0_1262
	s_and_b64 vcc, exec, s[40:41]
	s_cbranch_vccz .LBB0_1265
	s_barrier

; #define PG8_STAGE(bufoff, gbase, voff) do { _Pragma("unroll") for (int _i = 0; _i < 2; ++_i) \
;         __builtin_amdgcn_global_load_lds((const __attribute__((address_space(1))) unsigned*)((const __attribute__((address_space(1))) char*)(gbase) + (unsigned)lnd_v((int)(voff)[_i])), (LAS unsigned*)(lds + (bufoff) + ldsw + _i * 8192), 16, 0, 0); } while (0)
; #define PG8_LDA(dst, b, h) do { _Pragma("unroll") for (int m = 0; m < 4; ++m) _Pragma("unroll") for (int k = 0; k < 2; ++k) dst[m][k] = *(const LAS bf16x8*)(lds + PG8_SA(b, h) + aoff + m * 2048 + k * 1024); } while (0)
; #define PG8_LDB(dst, b, h) do { _Pragma("unroll") for (int n = 0; n < 2; ++n) _Pragma("unroll") for (int k = 0; k < 2; ++k) dst[n][k] = *(const LAS bf16x8*)(lds + PG8_SB(b, h) + boff + n * 2048 + k * 1024); } while (0)
; #define PG8_MMA(ai, bj, At, Bt) do { __builtin_amdgcn_s_setprio(1); _Pragma("unroll") for (int m = 0; m < 4; ++m) _Pragma("unroll") for (int n = 0; n < 2; ++n) _Pragma("unroll") for (int k = 0; k < 2; ++k) \
;         acc[ai][bj][m][n] = __builtin_amdgcn_mfma_f32_16x16x32_bf16(Bt[n][k], At[m][k], acc[ai][bj][m][n], 0, 0, 0); __builtin_amdgcn_s_setprio(0); } while (0)
; template <class Desc, class Epi>
; __device__ __forceinline__ void gemm_phase(const int wv_, LAS unsigned char* lds, const Desc& d, const Epi& E) {
;     ...
;             if constexpr (Desc::GATHER) { sA0[0] = last ? voffAn[0] : voffA[0]; sA0[1] = last ? voffAn[1] : voffA[1]; sA1[0] = last ? voffAn1[0] : voffA1[0]; sA1[1] = last ? voffAn1[1] : voffA1[1]; }
;             else { sA0[0] = voffA[0]; sA0[1] = voffA[1]; sA1[0] = voffA1[0]; sA1[1] = voffA1[1]; }
;             const char* a1 = cA + (size_t)(t + 1) * kstep;
;             const char* a2 = last ? nA : cA + (size_t)(t + 2) * kstep; const char* b2 = last ? nB : cB + (size_t)(t + 2) * kstep;
;             const char* a3 = a2 + kstep; const char* b3 = b2 + kstep;
;             PG8_LDB(B0, 0, 0); PG8_LDB(B1, 0, 1); PG8_SCHED; PG8_LDA(At, 0, 0); PG8_STAGE(PG8_SA(1, 1), a1, voffA1);
;             PG8_WAIT_V(8); PG8_WAIT_L(0); PG8_BAR; PG8_MMA(0, 0, At, B0); PG8_MMA(0, 1, At, B1); PG8_BAR; PG8_SCHED;
;             PG8_LDA(At, 0, 1); PG8_STAGE(PG8_SB(0, 0), b2, voffB); PG8_STAGE(PG8_SB(0, 1), b2 + hstepB, voffB); PG8_STAGE(PG8_SA(0, 0), a2, sA0);
;             PG8_WAIT_V(8); PG8_WAIT_L(0); PG8_BAR; PG8_MMA(1, 0, At, B0); PG8_MMA(1, 1, At, B1); PG8_BAR; PG8_SCHED;
.LBB0_1481:
	s_add_u32 s52, s50, s22
	s_addc_u32 s53, s51, 0
	s_add_u32 s23, s52, 0x100
	s_addc_u32 s24, s53, 0
	s_and_b64 s[4:5], s[20:21], exec
	s_cselect_b32 s4, s42, s23
	s_cselect_b32 s5, s43, s24
	s_add_u32 s22, s48, s22
	s_addc_u32 s23, s49, 0
	s_add_u32 s22, s22, 0x100
	s_addc_u32 s23, s23, 0
	s_add_i32 s77, 0, 0x10000
	s_and_b64 s[20:21], s[20:21], exec
	s_cselect_b32 s21, s45, s23
	s_cselect_b32 s20, s44, s22
	s_add_i32 s23, 0, 0x14000
	v_add_u32_e32 v96, s77, v139
	s_add_i32 s79, s77, s59
	ds_read_b128 v[150:153], v96
	ds_read_b128 v[154:157], v96 offset:1024
	ds_read_b128 v[158:161], v96 offset:2048
	ds_read_b128 v[162:165], v96 offset:3072
	v_add_u32_e32 v96, s23, v139
	s_add_i32 m0, s60, 0xc000
	s_add_i32 s80, s60, 0xe000
	s_add_i32 s75, s79, 0x2000
	ds_read_b128 v[166:169], v96
	ds_read_b128 v[170:173], v96 offset:1024
	ds_read_b128 v[174:177], v96 offset:2048
	ds_read_b128 v[178:181], v96 offset:3072
	s_add_u32 s24, s20, 0x40000
	s_addc_u32 s25, s21, 0
	s_add_i32 s73, 0, 0x18000
	s_add_i32 s76, s23, s59
	s_add_i32 s71, s73, s59
	s_add_i32 s74, s76, 0x2000
	s_add_i32 s72, 0, 0x1c000
	s_add_i32 s29, s71, 0x2000
	s_add_u32 s22, s20, 0x40080
	s_addc_u32 s23, s21, 0
	s_add_i32 s78, s72, s59
	s_add_i32 s77, s78, 0x2000
	v_mov_b32_e32 v96, v133
	ds_read_b128 v[184:187], v149
	ds_read_b128 v[188:191], v149 offset:1024
	ds_read_b128 v[192:195], v149 offset:2048
	ds_read_b128 v[196:199], v149 offset:3072
	ds_read_b128 v[200:203], v149 offset:4096
	ds_read_b128 v[204:207], v149 offset:5120
	ds_read_b128 v[208:211], v149 offset:6144
	ds_read_b128 v[212:215], v149 offset:7168
	s_nop 0
	v_lshl_add_u64 v[130:131], s[52:53], 0, v[96:97]
	v_lshl_add_u64 v[130:131], v[130:131], 0, s[30:31]
	v_mov_b32_e32 v96, v136
	global_load_lds_dwordx4 v[130:131], off
	s_mov_b32 m0, s80
	v_lshl_add_u64 v[130:131], s[52:53], 0, v[96:97]
	v_lshl_add_u64 v[130:131], v[130:131], 0, s[30:31]
	global_load_lds_dwordx4 v[130:131], off
	s_waitcnt vmcnt(8)
	s_waitcnt lgkmcnt(0)
	s_barrier
	s_setprio 1
	s_waitcnt lgkmcnt(0)
	v_mfma_f32_16x16x32_bf16 v[126:129], v[150:153], v[184:187], v[126:129]
	v_mfma_f32_16x16x32_bf16 v[122:125], v[158:161], v[184:187], v[122:125]
	v_mfma_f32_16x16x32_bf16 v[110:113], v[150:153], v[192:195], v[110:113]
	v_mfma_f32_16x16x32_bf16 v[106:109], v[158:161], v[192:195], v[106:109]
	v_mfma_f32_16x16x32_bf16 v[92:95], v[150:153], v[200:203], v[92:95]
	v_mfma_f32_16x16x32_bf16 v[88:91], v[158:161], v[200:203], v[88:91]
	v_mfma_f32_16x16x32_bf16 v[76:79], v[150:153], v[208:211], v[76:79]
	v_mfma_f32_16x16x32_bf16 v[72:75], v[158:161], v[208:211], v[72:75]
	v_mfma_f32_16x16x32_bf16 v[126:129], v[154:157], v[188:191], v[126:129]
	v_mfma_f32_16x16x32_bf16 v[122:125], v[162:165], v[188:191], v[122:125]
	v_mfma_f32_16x16x32_bf16 v[110:113], v[154:157], v[196:199], v[110:113]
	v_mfma_f32_16x16x32_bf16 v[106:109], v[162:165], v[196:199], v[106:109]
	v_mfma_f32_16x16x32_bf16 v[92:95], v[154:157], v[204:207], v[92:95]
	v_mfma_f32_16x16x32_bf16 v[88:91], v[162:165], v[204:207], v[88:91]
	v_mfma_f32_16x16x32_bf16 v[76:79], v[154:157], v[212:215], v[76:79]
	v_mfma_f32_16x16x32_bf16 v[72:75], v[162:165], v[212:215], v[72:75]
	s_setprio 0
	s_setprio 1
	v_mfma_f32_16x16x32_bf16 v[118:121], v[166:169], v[184:187], v[118:121]
	v_mfma_f32_16x16x32_bf16 v[114:117], v[174:177], v[184:187], v[114:117]
	v_mfma_f32_16x16x32_bf16 v[102:105], v[166:169], v[192:195], v[102:105]
	v_mfma_f32_16x16x32_bf16 v[98:101], v[174:177], v[192:195], v[98:101]
	v_mfma_f32_16x16x32_bf16 v[84:87], v[166:169], v[200:203], v[84:87]
	v_mfma_f32_16x16x32_bf16 v[80:83], v[174:177], v[200:203], v[80:83]
	v_mfma_f32_16x16x32_bf16 v[68:71], v[166:169], v[208:211], v[68:71]
	v_mfma_f32_16x16x32_bf16 v[64:67], v[174:177], v[208:211], v[64:67]
	v_mfma_f32_16x16x32_bf16 v[118:121], v[170:173], v[188:191], v[118:121]
	v_mfma_f32_16x16x32_bf16 v[114:117], v[178:181], v[188:191], v[114:117]
	v_mfma_f32_16x16x32_bf16 v[102:105], v[170:173], v[196:199], v[102:105]
	v_mfma_f32_16x16x32_bf16 v[98:101], v[178:181], v[196:199], v[98:101]
	v_mfma_f32_16x16x32_bf16 v[84:87], v[170:173], v[204:207], v[84:87]
	v_mfma_f32_16x16x32_bf16 v[80:83], v[178:181], v[204:207], v[80:83]
	v_mfma_f32_16x16x32_bf16 v[68:71], v[170:173], v[212:215], v[68:71]
	v_mfma_f32_16x16x32_bf16 v[64:67], v[178:181], v[212:215], v[64:67]
	s_setprio 0
	s_barrier
	v_mov_b32_e32 v96, v134
	s_mov_b32 m0, s79
	ds_read_b128 v[184:187], v149 offset:16384
	ds_read_b128 v[188:191], v149 offset:17408
	ds_read_b128 v[192:195], v149 offset:18432
	ds_read_b128 v[196:199], v149 offset:19456
	ds_read_b128 v[200:203], v149 offset:20480
	ds_read_b128 v[204:207], v149 offset:21504
	ds_read_b128 v[208:211], v149 offset:22528
	ds_read_b128 v[212:215], v149 offset:23552
	s_nop 0
	global_load_lds_dwordx4 v96, s[20:21]
	v_mov_b32_e32 v96, v137
	s_mov_b32 m0, s75
	s_nop 0
	global_load_lds_dwordx4 v96, s[20:21]
	v_mov_b32_e32 v96, v134
	s_mov_b32 m0, s76
	s_nop 0
	global_load_lds_dwordx4 v96, s[24:25]
	v_mov_b32_e32 v96, v137
	s_mov_b32 m0, s74
	s_nop 0
	global_load_lds_dwordx4 v96, s[24:25]
	v_mov_b32_e32 v96, v132
	s_mov_b32 m0, s60
	s_nop 0
	global_load_lds_dwordx4 v96, s[4:5]
	v_mov_b32_e32 v96, v135
	s_mov_b32 m0, s61
	s_nop 0
	global_load_lds_dwordx4 v96, s[4:5]
	s_waitcnt vmcnt(8)
	s_waitcnt lgkmcnt(0)
	s_barrier
; #define PG8_STAGE(bufoff, gbase, voff) do { _Pragma("unroll") for (int _i = 0; _i < 2; ++_i) \
;         __builtin_amdgcn_global_load_lds((const __attribute__((address_space(1))) unsigned*)((const __attribute__((address_space(1))) char*)(gbase) + (unsigned)lnd_v((int)(voff)[_i])), (LAS unsigned*)(lds + (bufoff) + ldsw + _i * 8192), 16, 0, 0); } while (0)
; #define PG8_LDA(dst, b, h) do { _Pragma("unroll") for (int m = 0; m < 4; ++m) _Pragma("unroll") for (int k = 0; k < 2; ++k) dst[m][k] = *(const LAS bf16x8*)(lds + PG8_SA(b, h) + aoff + m * 2048 + k * 1024); } while (0)
; #define PG8_LDB(dst, b, h) do { _Pragma("unroll") for (int n = 0; n < 2; ++n) _Pragma("unroll") for (int k = 0; k < 2; ++k) dst[n][k] = *(const LAS bf16x8*)(lds + PG8_SB(b, h) + boff + n * 2048 + k * 1024); } while (0)
; #define PG8_MMA(ai, bj, At, Bt) do { __builtin_amdgcn_s_setprio(1); _Pragma("unroll") for (int m = 0; m < 4; ++m) _Pragma("unroll") for (int n = 0; n < 2; ++n) _Pragma("unroll") for (int k = 0; k < 2; ++k) \
;         acc[ai][bj][m][n] = __builtin_amdgcn_mfma_f32_16x16x32_bf16(Bt[n][k], At[m][k], acc[ai][bj][m][n], 0, 0, 0); __builtin_amdgcn_s_setprio(0); } while (0)
; #define PG8_WAIT_V(n) asm volatile("s_waitcnt vmcnt(" #n ")" ::: "memory")
; #define PG8_WAIT_L(n) asm volatile("s_waitcnt lgkmcnt(" #n ")" ::: "memory")
; #define PG8_BAR __builtin_amdgcn_s_barrier()
; #define PG8_SCHED __builtin_amdgcn_sched_barrier(0)
; template <class Desc, class Epi>
; __device__ __forceinline__ void gemm_phase(const int wv_, LAS unsigned char* lds, const Desc& d, const Epi& E) {
;     ...
;             PG8_WAIT_V(8); PG8_WAIT_L(0); PG8_BAR; PG8_MMA(1, 0, At, B0); PG8_MMA(1, 1, At, B1); PG8_BAR; PG8_SCHED;
;             PG8_LDB(B0, 1, 0); PG8_LDB(B1, 1, 1); PG8_SCHED; PG8_LDA(At, 1, 0); PG8_STAGE(PG8_SA(0, 1), a2, sA1);
;             PG8_WAIT_V(8); PG8_WAIT_L(0); PG8_BAR; PG8_MMA(0, 0, At, B0); PG8_MMA(0, 1, At, B1); PG8_BAR; PG8_SCHED;
	s_setprio 1
	s_waitcnt lgkmcnt(0)
	v_mfma_f32_16x16x32_bf16 v[60:63], v[150:153], v[184:187], v[60:63]
	v_mfma_f32_16x16x32_bf16 v[56:59], v[158:161], v[184:187], v[56:59]
	v_mfma_f32_16x16x32_bf16 v[44:47], v[150:153], v[192:195], v[44:47]
	v_mfma_f32_16x16x32_bf16 v[32:35], v[158:161], v[192:195], v[32:35]
	v_mfma_f32_16x16x32_bf16 v[16:19], v[150:153], v[200:203], v[16:19]
	v_mfma_f32_16x16x32_bf16 v[8:11], v[158:161], v[200:203], v[8:11]
	v_mfma_f32_16x16x32_bf16 v[4:7], v[150:153], v[208:211], v[4:7]
	v_mfma_f32_16x16x32_bf16 v[0:3], v[158:161], v[208:211], v[0:3]
	v_mfma_f32_16x16x32_bf16 v[60:63], v[154:157], v[188:191], v[60:63]
	v_mfma_f32_16x16x32_bf16 v[56:59], v[162:165], v[188:191], v[56:59]
	v_mfma_f32_16x16x32_bf16 v[44:47], v[154:157], v[196:199], v[44:47]
	v_mfma_f32_16x16x32_bf16 v[32:35], v[162:165], v[196:199], v[32:35]
	v_mfma_f32_16x16x32_bf16 v[16:19], v[154:157], v[204:207], v[16:19]
	v_mfma_f32_16x16x32_bf16 v[8:11], v[162:165], v[204:207], v[8:11]
	v_mfma_f32_16x16x32_bf16 v[4:7], v[154:157], v[212:215], v[4:7]
	v_mfma_f32_16x16x32_bf16 v[0:3], v[162:165], v[212:215], v[0:3]
	s_setprio 0
	s_setprio 1
	v_mfma_f32_16x16x32_bf16 v[52:55], v[166:169], v[184:187], v[52:55]
	v_mfma_f32_16x16x32_bf16 v[48:51], v[174:177], v[184:187], v[48:51]
	v_mfma_f32_16x16x32_bf16 v[28:31], v[166:169], v[192:195], v[28:31]
	v_mfma_f32_16x16x32_bf16 v[12:15], v[174:177], v[192:195], v[12:15]
	v_mfma_f32_16x16x32_bf16 v[36:39], v[166:169], v[200:203], v[36:39]
	v_mfma_f32_16x16x32_bf16 v[40:43], v[174:177], v[200:203], v[40:43]
	v_mfma_f32_16x16x32_bf16 v[20:23], v[166:169], v[208:211], v[20:23]
	v_mfma_f32_16x16x32_bf16 v[24:27], v[174:177], v[208:211], v[24:27]
	v_mfma_f32_16x16x32_bf16 v[52:55], v[170:173], v[188:191], v[52:55]
	v_mfma_f32_16x16x32_bf16 v[48:51], v[178:181], v[188:191], v[48:51]
	v_mfma_f32_16x16x32_bf16 v[28:31], v[170:173], v[196:199], v[28:31]
	v_mfma_f32_16x16x32_bf16 v[12:15], v[178:181], v[196:199], v[12:15]
	v_mfma_f32_16x16x32_bf16 v[36:39], v[170:173], v[204:207], v[36:39]
	v_mfma_f32_16x16x32_bf16 v[40:43], v[178:181], v[204:207], v[40:43]
	v_mfma_f32_16x16x32_bf16 v[20:23], v[170:173], v[212:215], v[20:23]
	v_mfma_f32_16x16x32_bf16 v[24:27], v[178:181], v[212:215], v[24:27]
	s_setprio 0
	s_barrier
	v_add_u32_e32 v96, s73, v139
	ds_read_b128 v[150:153], v96
	ds_read_b128 v[154:157], v96 offset:1024
	ds_read_b128 v[158:161], v96 offset:2048
	ds_read_b128 v[162:165], v96 offset:3072
	v_add_u32_e32 v96, s72, v139
	ds_read_b128 v[166:169], v96
	ds_read_b128 v[170:173], v96 offset:1024
	ds_read_b128 v[174:177], v96 offset:2048
	ds_read_b128 v[178:181], v96 offset:3072
	v_mov_b32_e32 v96, v133
	s_mov_b32 m0, s62
	ds_read_b128 v[184:187], v149 offset:32768
	ds_read_b128 v[188:191], v149 offset:33792
	ds_read_b128 v[192:195], v149 offset:34816
	ds_read_b128 v[196:199], v149 offset:35840
	ds_read_b128 v[200:203], v149 offset:36864
	ds_read_b128 v[204:207], v149 offset:37888
	ds_read_b128 v[208:211], v149 offset:38912
	ds_read_b128 v[212:215], v149 offset:39936
	s_nop 0
	global_load_lds_dwordx4 v96, s[4:5]
	v_mov_b32_e32 v96, v136
	s_mov_b32 m0, s63
	s_nop 0
	global_load_lds_dwordx4 v96, s[4:5]
	s_waitcnt vmcnt(8)
	s_waitcnt lgkmcnt(0)
	s_barrier
	s_setprio 1
	s_waitcnt lgkmcnt(0)
	v_mfma_f32_16x16x32_bf16 v[126:129], v[150:153], v[184:187], v[126:129]
	v_mfma_f32_16x16x32_bf16 v[122:125], v[158:161], v[184:187], v[122:125]
	v_mfma_f32_16x16x32_bf16 v[110:113], v[150:153], v[192:195], v[110:113]
	v_mfma_f32_16x16x32_bf16 v[106:109], v[158:161], v[192:195], v[106:109]
	v_mfma_f32_16x16x32_bf16 v[92:95], v[150:153], v[200:203], v[92:95]
	v_mfma_f32_16x16x32_bf16 v[88:91], v[158:161], v[200:203], v[88:91]
	v_mfma_f32_16x16x32_bf16 v[76:79], v[150:153], v[208:211], v[76:79]
	v_mfma_f32_16x16x32_bf16 v[72:75], v[158:161], v[208:211], v[72:75]
	v_mfma_f32_16x16x32_bf16 v[126:129], v[154:157], v[188:191], v[126:129]
	v_mfma_f32_16x16x32_bf16 v[122:125], v[162:165], v[188:191], v[122:125]
	v_mfma_f32_16x16x32_bf16 v[110:113], v[154:157], v[196:199], v[110:113]
	v_mfma_f32_16x16x32_bf16 v[106:109], v[162:165], v[196:199], v[106:109]
	v_mfma_f32_16x16x32_bf16 v[92:95], v[154:157], v[204:207], v[92:95]
	v_mfma_f32_16x16x32_bf16 v[88:91], v[162:165], v[204:207], v[88:91]
	v_mfma_f32_16x16x32_bf16 v[76:79], v[154:157], v[212:215], v[76:79]
	v_mfma_f32_16x16x32_bf16 v[72:75], v[162:165], v[212:215], v[72:75]
	s_setprio 0
	s_setprio 1
	v_mfma_f32_16x16x32_bf16 v[118:121], v[166:169], v[184:187], v[118:121]
	v_mfma_f32_16x16x32_bf16 v[114:117], v[174:177], v[184:187], v[114:117]
	v_mfma_f32_16x16x32_bf16 v[102:105], v[166:169], v[192:195], v[102:105]
	v_mfma_f32_16x16x32_bf16 v[98:101], v[174:177], v[192:195], v[98:101]
	v_mfma_f32_16x16x32_bf16 v[84:87], v[166:169], v[200:203], v[84:87]
	v_mfma_f32_16x16x32_bf16 v[80:83], v[174:177], v[200:203], v[80:83]
	v_mfma_f32_16x16x32_bf16 v[68:71], v[166:169], v[208:211], v[68:71]
	v_mfma_f32_16x16x32_bf16 v[64:67], v[174:177], v[208:211], v[64:67]
	v_mfma_f32_16x16x32_bf16 v[118:121], v[170:173], v[188:191], v[118:121]
	v_mfma_f32_16x16x32_bf16 v[114:117], v[178:181], v[188:191], v[114:117]
	v_mfma_f32_16x16x32_bf16 v[102:105], v[170:173], v[196:199], v[102:105]
	v_mfma_f32_16x16x32_bf16 v[98:101], v[178:181], v[196:199], v[98:101]
	v_mfma_f32_16x16x32_bf16 v[84:87], v[170:173], v[204:207], v[84:87]
	v_mfma_f32_16x16x32_bf16 v[80:83], v[178:181], v[204:207], v[80:83]
	v_mfma_f32_16x16x32_bf16 v[68:71], v[170:173], v[212:215], v[68:71]
	v_mfma_f32_16x16x32_bf16 v[64:67], v[178:181], v[212:215], v[64:67]
	s_setprio 0
	s_barrier
; #define PG8_STAGE(bufoff, gbase, voff) do { _Pragma("unroll") for (int _i = 0; _i < 2; ++_i) \
;         __builtin_amdgcn_global_load_lds((const __attribute__((address_space(1))) unsigned*)((const __attribute__((address_space(1))) char*)(gbase) + (unsigned)lnd_v((int)(voff)[_i])), (LAS unsigned*)(lds + (bufoff) + ldsw + _i * 8192), 16, 0, 0); } while (0)
; #define PG8_LDA(dst, b, h) do { _Pragma("unroll") for (int m = 0; m < 4; ++m) _Pragma("unroll") for (int k = 0; k < 2; ++k) dst[m][k] = *(const LAS bf16x8*)(lds + PG8_SA(b, h) + aoff + m * 2048 + k * 1024); } while (0)
; #define PG8_MMA(ai, bj, At, Bt) do { __builtin_amdgcn_s_setprio(1); _Pragma("unroll") for (int m = 0; m < 4; ++m) _Pragma("unroll") for (int n = 0; n < 2; ++n) _Pragma("unroll") for (int k = 0; k < 2; ++k) \
;         acc[ai][bj][m][n] = __builtin_amdgcn_mfma_f32_16x16x32_bf16(Bt[n][k], At[m][k], acc[ai][bj][m][n], 0, 0, 0); __builtin_amdgcn_s_setprio(0); } while (0)
; #define PG8_WAIT_V(n) asm volatile("s_waitcnt vmcnt(" #n ")" ::: "memory")
; #define PG8_WAIT_L(n) asm volatile("s_waitcnt lgkmcnt(" #n ")" ::: "memory")
; #define PG8_BAR __builtin_amdgcn_s_barrier()
; #define PG8_SCHED __builtin_amdgcn_sched_barrier(0)
; template <class Desc, class Epi>
; __device__ __forceinline__ void gemm_phase(const int wv_, LAS unsigned char* lds, const Desc& d, const Epi& E) {
;     ...
;             PG8_LDA(At, 1, 1); PG8_STAGE(PG8_SB(1, 0), b3, voffB); PG8_STAGE(PG8_SB(1, 1), b3 + hstepB, voffB); PG8_STAGE(PG8_SA(1, 0), a3, sA0);
;             PG8_WAIT_V(8); PG8_WAIT_L(0); PG8_BAR; PG8_MMA(1, 0, At, B0); PG8_MMA(1, 1, At, B1); PG8_BAR; PG8_SCHED;
;         }
;         if (wr == 0) PG8_BAR;
	v_mov_b32_e32 v96, v134
	ds_read_b128 v[184:187], v149 offset:49152
	ds_read_b128 v[188:191], v149 offset:50176
	ds_read_b128 v[192:195], v149 offset:51200
	ds_read_b128 v[196:199], v149 offset:52224
	ds_read_b128 v[200:203], v149 offset:53248
	ds_read_b128 v[204:207], v149 offset:54272
	ds_read_b128 v[208:211], v149 offset:55296
	ds_read_b128 v[212:215], v149 offset:56320
	s_mov_b32 m0, s71
	v_lshl_add_u64 v[130:131], s[20:21], 0, v[96:97]
	v_lshl_add_u64 v[130:131], v[130:131], 0, s[30:31]
	v_mov_b32_e32 v96, v137
	global_load_lds_dwordx4 v[130:131], off
	s_mov_b32 m0, s29
	v_lshl_add_u64 v[130:131], s[20:21], 0, v[96:97]
	v_lshl_add_u64 v[130:131], v[130:131], 0, s[30:31]
	v_mov_b32_e32 v96, v134
	global_load_lds_dwordx4 v[130:131], off
	s_mov_b32 m0, s78
	s_nop 0
	global_load_lds_dwordx4 v96, s[22:23]
	v_mov_b32_e32 v96, v137
	s_mov_b32 m0, s77
	s_nop 0
	global_load_lds_dwordx4 v96, s[22:23]
	v_mov_b32_e32 v96, v132
	s_mov_b32 m0, s65
	v_lshl_add_u64 v[130:131], s[4:5], 0, v[96:97]
	v_lshl_add_u64 v[130:131], v[130:131], 0, s[30:31]
	v_mov_b32_e32 v96, v135
	global_load_lds_dwordx4 v[130:131], off
	s_mov_b32 m0, s66
	v_lshl_add_u64 v[130:131], s[4:5], 0, v[96:97]
	v_lshl_add_u64 v[130:131], v[130:131], 0, s[30:31]
	global_load_lds_dwordx4 v[130:131], off
	s_waitcnt vmcnt(8)
	s_waitcnt lgkmcnt(0)
	s_barrier
	s_setprio 1
	s_waitcnt lgkmcnt(0)
	v_mfma_f32_16x16x32_bf16 v[60:63], v[150:153], v[184:187], v[60:63]
	v_mfma_f32_16x16x32_bf16 v[56:59], v[158:161], v[184:187], v[56:59]
	v_mfma_f32_16x16x32_bf16 v[44:47], v[150:153], v[192:195], v[44:47]
	v_mfma_f32_16x16x32_bf16 v[32:35], v[158:161], v[192:195], v[32:35]
	v_mfma_f32_16x16x32_bf16 v[16:19], v[150:153], v[200:203], v[16:19]
	v_mfma_f32_16x16x32_bf16 v[8:11], v[158:161], v[200:203], v[8:11]
	v_mfma_f32_16x16x32_bf16 v[4:7], v[150:153], v[208:211], v[4:7]
	v_mfma_f32_16x16x32_bf16 v[0:3], v[158:161], v[208:211], v[0:3]
	v_mfma_f32_16x16x32_bf16 v[60:63], v[154:157], v[188:191], v[60:63]
	v_mfma_f32_16x16x32_bf16 v[56:59], v[162:165], v[188:191], v[56:59]
	v_mfma_f32_16x16x32_bf16 v[44:47], v[154:157], v[196:199], v[44:47]
	v_mfma_f32_16x16x32_bf16 v[32:35], v[162:165], v[196:199], v[32:35]
	v_mfma_f32_16x16x32_bf16 v[16:19], v[154:157], v[204:207], v[16:19]
	v_mfma_f32_16x16x32_bf16 v[8:11], v[162:165], v[204:207], v[8:11]
	v_mfma_f32_16x16x32_bf16 v[4:7], v[154:157], v[212:215], v[4:7]
	v_mfma_f32_16x16x32_bf16 v[0:3], v[162:165], v[212:215], v[0:3]
	s_setprio 0
	s_setprio 1
	v_mfma_f32_16x16x32_bf16 v[52:55], v[166:169], v[184:187], v[52:55]
	v_mfma_f32_16x16x32_bf16 v[48:51], v[174:177], v[184:187], v[48:51]
	v_mfma_f32_16x16x32_bf16 v[28:31], v[166:169], v[192:195], v[28:31]
	v_mfma_f32_16x16x32_bf16 v[12:15], v[174:177], v[192:195], v[12:15]
	v_mfma_f32_16x16x32_bf16 v[36:39], v[166:169], v[200:203], v[36:39]
	v_mfma_f32_16x16x32_bf16 v[40:43], v[174:177], v[200:203], v[40:43]
	v_mfma_f32_16x16x32_bf16 v[20:23], v[166:169], v[208:211], v[20:23]
	v_mfma_f32_16x16x32_bf16 v[24:27], v[174:177], v[208:211], v[24:27]
	v_mfma_f32_16x16x32_bf16 v[52:55], v[170:173], v[188:191], v[52:55]
	v_mfma_f32_16x16x32_bf16 v[48:51], v[178:181], v[188:191], v[48:51]
	v_mfma_f32_16x16x32_bf16 v[28:31], v[170:173], v[196:199], v[28:31]
	v_mfma_f32_16x16x32_bf16 v[12:15], v[178:181], v[196:199], v[12:15]
	v_mfma_f32_16x16x32_bf16 v[36:39], v[170:173], v[204:207], v[36:39]
	v_mfma_f32_16x16x32_bf16 v[40:43], v[178:181], v[204:207], v[40:43]
	v_mfma_f32_16x16x32_bf16 v[20:23], v[170:173], v[212:215], v[20:23]
	v_mfma_f32_16x16x32_bf16 v[24:27], v[178:181], v[212:215], v[24:27]
	s_setprio 0
	s_barrier
	s_movk_i32 s22, 0x100
	s_andn2_b64 vcc, exec, s[2:3]
	s_mov_b64 s[20:21], -1
	s_mov_b64 s[2:3], 0
	s_cbranch_vccz .LBB0_1481
	s_and_b64 vcc, exec, s[40:41]
	s_cbranch_vccz .LBB0_1484
	s_barrier

; #define PG8_STAGE(bufoff, gbase, voff) do { _Pragma("unroll") for (int _i = 0; _i < 2; ++_i) \
;         __builtin_amdgcn_global_load_lds((const __attribute__((address_space(1))) unsigned*)((const __attribute__((address_space(1))) char*)(gbase) + (unsigned)lnd_v((int)(voff)[_i])), (LAS unsigned*)(lds + (bufoff) + ldsw + _i * 8192), 16, 0, 0); } while (0)
; #define PG8_LDA(dst, b, h) do { _Pragma("unroll") for (int m = 0; m < 4; ++m) _Pragma("unroll") for (int k = 0; k < 2; ++k) dst[m][k] = *(const LAS bf16x8*)(lds + PG8_SA(b, h) + aoff + m * 2048 + k * 1024); } while (0)
; #define PG8_LDB(dst, b, h) do { _Pragma("unroll") for (int n = 0; n < 2; ++n) _Pragma("unroll") for (int k = 0; k < 2; ++k) dst[n][k] = *(const LAS bf16x8*)(lds + PG8_SB(b, h) + boff + n * 2048 + k * 1024); } while (0)
; #define PG8_MMA(ai, bj, At, Bt) do { __builtin_amdgcn_s_setprio(1); _Pragma("unroll") for (int m = 0; m < 4; ++m) _Pragma("unroll") for (int n = 0; n < 2; ++n) _Pragma("unroll") for (int k = 0; k < 2; ++k) \
;         acc[ai][bj][m][n] = __builtin_amdgcn_mfma_f32_16x16x32_bf16(Bt[n][k], At[m][k], acc[ai][bj][m][n], 0, 0, 0); __builtin_amdgcn_s_setprio(0); } while (0)
; template <class Desc, class Epi>
; __device__ __forceinline__ void gemm_phase(const int wv_, LAS unsigned char* lds, const Desc& d, const Epi& E) {
;     ...
;             if constexpr (Desc::GATHER) { sA0[0] = last ? voffAn[0] : voffA[0]; sA0[1] = last ? voffAn[1] : voffA[1]; sA1[0] = last ? voffAn1[0] : voffA1[0]; sA1[1] = last ? voffAn1[1] : voffA1[1]; }
;             else { sA0[0] = voffA[0]; sA0[1] = voffA[1]; sA1[0] = voffA1[0]; sA1[1] = voffA1[1]; }
;             const char* a1 = cA + (size_t)(t + 1) * kstep;
;             const char* a2 = last ? nA : cA + (size_t)(t + 2) * kstep; const char* b2 = last ? nB : cB + (size_t)(t + 2) * kstep;
;             const char* a3 = a2 + kstep; const char* b3 = b2 + kstep;
;             PG8_LDB(B0, 0, 0); PG8_LDB(B1, 0, 1); PG8_SCHED; PG8_LDA(At, 0, 0); PG8_STAGE(PG8_SA(1, 1), a1, voffA1);
;             PG8_WAIT_V(8); PG8_WAIT_L(0); PG8_BAR; PG8_MMA(0, 0, At, B0); PG8_MMA(0, 1, At, B1); PG8_BAR; PG8_SCHED;
;             PG8_LDA(At, 0, 1); PG8_STAGE(PG8_SB(0, 0), b2, voffB); PG8_STAGE(PG8_SB(0, 1), b2 + hstepB, voffB); PG8_STAGE(PG8_SA(0, 0), a2, sA0);
;             PG8_WAIT_V(8); PG8_WAIT_L(0); PG8_BAR; PG8_MMA(1, 0, At, B0); PG8_MMA(1, 1, At, B1); PG8_BAR; PG8_SCHED;
.LBB0_1565:
	s_add_u32 s4, s2, 0x100
	s_addc_u32 s5, s3, 0
	s_add_u32 s22, s29, s2
	s_addc_u32 s23, s59, s3
	s_cmp_eq_u32 s75, 12
	s_cselect_b64 vcc, -1, 0
	s_and_b64 s[20:21], vcc, exec
	s_cselect_b32 s20, 0, s4
	s_cselect_b32 s21, 0, s5
	s_cselect_b32 s22, s54, s22
	s_cselect_b32 s23, s55, s23
	s_add_u32 s20, s42, s20
	s_addc_u32 s21, s43, s21
	s_add_i32 s76, 0, 0x10000
	v_add_u32_e32 v135, s76, v143
	s_add_i32 s77, 0, 0x14000
	ds_read_b128 v[160:163], v135
	ds_read_b128 v[164:167], v135 offset:1024
	ds_read_b128 v[168:171], v135 offset:2048
	ds_read_b128 v[172:175], v135 offset:3072
	v_add_u32_e32 v135, s77, v143
	ds_read_b128 v[176:179], v135
	ds_read_b128 v[180:183], v135 offset:1024
	ds_read_b128 v[184:187], v135 offset:2048
	ds_read_b128 v[188:191], v135 offset:3072
	v_cndmask_b32_e32 v134, v157, v153, vcc
	v_cndmask_b32_e32 v132, v159, v154, vcc
	v_cndmask_b32_e32 v96, v131, v155, vcc
	v_cndmask_b32_e32 v133, v158, v156, vcc
	s_add_i32 m0, s64, 0xc000
	v_mov_b32_e32 v135, v131
	s_add_u32 s2, s40, s2
	ds_read_b128 v[194:197], v152
	ds_read_b128 v[198:201], v152 offset:1024
	ds_read_b128 v[202:205], v152 offset:2048
	ds_read_b128 v[206:209], v152 offset:3072
	ds_read_b128 v[210:213], v152 offset:4096
	ds_read_b128 v[222:225], v152 offset:5120
	ds_read_b128 v[230:233], v152 offset:6144
	ds_read_b128 v[234:237], v152 offset:7168
	s_addc_u32 s3, s41, s3
	global_load_lds_dwordx4 v135, s[2:3]
	v_mov_b32_e32 v135, v158
	s_add_i32 m0, s64, 0xe000
	s_nop 0
	global_load_lds_dwordx4 v135, s[2:3]
	s_waitcnt vmcnt(8)
	s_waitcnt lgkmcnt(0)
	s_barrier
	s_setprio 1
	s_waitcnt lgkmcnt(0)
	v_mfma_f32_16x16x32_bf16 v[122:125], v[160:163], v[194:197], v[122:125]
	v_mfma_f32_16x16x32_bf16 v[114:117], v[168:171], v[194:197], v[114:117]
	v_mfma_f32_16x16x32_bf16 v[106:109], v[160:163], v[202:205], v[106:109]
	v_mfma_f32_16x16x32_bf16 v[98:101], v[168:171], v[202:205], v[98:101]
	v_mfma_f32_16x16x32_bf16 v[88:91], v[160:163], v[210:213], v[88:91]
	v_mfma_f32_16x16x32_bf16 v[80:83], v[168:171], v[210:213], v[80:83]
	v_mfma_f32_16x16x32_bf16 v[72:75], v[160:163], v[230:233], v[72:75]
	v_mfma_f32_16x16x32_bf16 v[64:67], v[168:171], v[230:233], v[64:67]
	v_mfma_f32_16x16x32_bf16 v[122:125], v[164:167], v[198:201], v[122:125]
	v_mfma_f32_16x16x32_bf16 v[114:117], v[172:175], v[198:201], v[114:117]
	v_mfma_f32_16x16x32_bf16 v[106:109], v[164:167], v[206:209], v[106:109]
	v_mfma_f32_16x16x32_bf16 v[98:101], v[172:175], v[206:209], v[98:101]
	v_mfma_f32_16x16x32_bf16 v[88:91], v[164:167], v[222:225], v[88:91]
	v_mfma_f32_16x16x32_bf16 v[80:83], v[172:175], v[222:225], v[80:83]
	v_mfma_f32_16x16x32_bf16 v[72:75], v[164:167], v[234:237], v[72:75]
	v_mfma_f32_16x16x32_bf16 v[64:67], v[172:175], v[234:237], v[64:67]
	s_setprio 0
	s_setprio 1
	v_mfma_f32_16x16x32_bf16 v[126:129], v[176:179], v[194:197], v[126:129]
	v_mfma_f32_16x16x32_bf16 v[118:121], v[184:187], v[194:197], v[118:121]
	v_mfma_f32_16x16x32_bf16 v[110:113], v[176:179], v[202:205], v[110:113]
	v_mfma_f32_16x16x32_bf16 v[102:105], v[184:187], v[202:205], v[102:105]
	v_mfma_f32_16x16x32_bf16 v[92:95], v[176:179], v[210:213], v[92:95]
	v_mfma_f32_16x16x32_bf16 v[84:87], v[184:187], v[210:213], v[84:87]
	v_mfma_f32_16x16x32_bf16 v[76:79], v[176:179], v[230:233], v[76:79]
	v_mfma_f32_16x16x32_bf16 v[68:71], v[184:187], v[230:233], v[68:71]
	v_mfma_f32_16x16x32_bf16 v[126:129], v[180:183], v[198:201], v[126:129]
	v_mfma_f32_16x16x32_bf16 v[118:121], v[188:191], v[198:201], v[118:121]
	v_mfma_f32_16x16x32_bf16 v[110:113], v[180:183], v[206:209], v[110:113]
	v_mfma_f32_16x16x32_bf16 v[102:105], v[188:191], v[206:209], v[102:105]
	v_mfma_f32_16x16x32_bf16 v[92:95], v[180:183], v[222:225], v[92:95]
	v_mfma_f32_16x16x32_bf16 v[84:87], v[188:191], v[222:225], v[84:87]
	v_mfma_f32_16x16x32_bf16 v[76:79], v[180:183], v[234:237], v[76:79]
	v_mfma_f32_16x16x32_bf16 v[68:71], v[188:191], v[234:237], v[68:71]
	s_setprio 0
	s_barrier
	v_mov_b32_e32 v135, v138
	s_add_i32 s2, s76, s63
	ds_read_b128 v[194:197], v152 offset:16384
	ds_read_b128 v[198:201], v152 offset:17408
	ds_read_b128 v[202:205], v152 offset:18432
	ds_read_b128 v[206:209], v152 offset:19456
	ds_read_b128 v[210:213], v152 offset:20480
	ds_read_b128 v[222:225], v152 offset:21504
	ds_read_b128 v[230:233], v152 offset:22528
	ds_read_b128 v[234:237], v152 offset:23552
	s_mov_b32 m0, s2
	s_nop 0
	global_load_lds_dwordx4 v135, s[22:23]
	v_mov_b32_e32 v135, v141
	s_add_i32 m0, s2, 0x2000
	s_add_u32 s2, s22, 0x40000
	global_load_lds_dwordx4 v135, s[22:23]
	s_addc_u32 s3, s23, 0
	v_mov_b32_e32 v135, v138
	s_add_i32 s76, s77, s63
	s_mov_b32 m0, s76
	s_nop 0
	global_load_lds_dwordx4 v135, s[2:3]
	v_mov_b32_e32 v135, v141
	s_add_i32 m0, s76, 0x2000
	s_nop 0
	global_load_lds_dwordx4 v135, s[2:3]
	v_mov_b32_e32 v135, v134
	s_mov_b32 m0, s64
	s_nop 0
	global_load_lds_dwordx4 v135, s[20:21]
	v_mov_b32_e32 v135, v132
	s_mov_b32 m0, s65
	s_nop 0
	global_load_lds_dwordx4 v135, s[20:21]
	s_waitcnt vmcnt(8)
	s_waitcnt lgkmcnt(0)
	s_barrier
; #define PG8_STAGE(bufoff, gbase, voff) do { _Pragma("unroll") for (int _i = 0; _i < 2; ++_i) \
;         __builtin_amdgcn_global_load_lds((const __attribute__((address_space(1))) unsigned*)((const __attribute__((address_space(1))) char*)(gbase) + (unsigned)lnd_v((int)(voff)[_i])), (LAS unsigned*)(lds + (bufoff) + ldsw + _i * 8192), 16, 0, 0); } while (0)
; #define PG8_LDA(dst, b, h) do { _Pragma("unroll") for (int m = 0; m < 4; ++m) _Pragma("unroll") for (int k = 0; k < 2; ++k) dst[m][k] = *(const LAS bf16x8*)(lds + PG8_SA(b, h) + aoff + m * 2048 + k * 1024); } while (0)
; #define PG8_LDB(dst, b, h) do { _Pragma("unroll") for (int n = 0; n < 2; ++n) _Pragma("unroll") for (int k = 0; k < 2; ++k) dst[n][k] = *(const LAS bf16x8*)(lds + PG8_SB(b, h) + boff + n * 2048 + k * 1024); } while (0)
; #define PG8_MMA(ai, bj, At, Bt) do { __builtin_amdgcn_s_setprio(1); _Pragma("unroll") for (int m = 0; m < 4; ++m) _Pragma("unroll") for (int n = 0; n < 2; ++n) _Pragma("unroll") for (int k = 0; k < 2; ++k) \
;         acc[ai][bj][m][n] = __builtin_amdgcn_mfma_f32_16x16x32_bf16(Bt[n][k], At[m][k], acc[ai][bj][m][n], 0, 0, 0); __builtin_amdgcn_s_setprio(0); } while (0)
; #define PG8_WAIT_V(n) asm volatile("s_waitcnt vmcnt(" #n ")" ::: "memory")
; #define PG8_WAIT_L(n) asm volatile("s_waitcnt lgkmcnt(" #n ")" ::: "memory")
; #define PG8_BAR __builtin_amdgcn_s_barrier()
; #define PG8_SCHED __builtin_amdgcn_sched_barrier(0)
; template <class Desc, class Epi>
; __device__ __forceinline__ void gemm_phase(const int wv_, LAS unsigned char* lds, const Desc& d, const Epi& E) {
;     ...
;             PG8_WAIT_V(8); PG8_WAIT_L(0); PG8_BAR; PG8_MMA(1, 0, At, B0); PG8_MMA(1, 1, At, B1); PG8_BAR; PG8_SCHED;
;             PG8_LDB(B0, 1, 0); PG8_LDB(B1, 1, 1); PG8_SCHED; PG8_LDA(At, 1, 0); PG8_STAGE(PG8_SA(0, 1), a2, sA1);
;             PG8_WAIT_V(8); PG8_WAIT_L(0); PG8_BAR; PG8_MMA(0, 0, At, B0); PG8_MMA(0, 1, At, B1); PG8_BAR; PG8_SCHED;
	s_setprio 1
	s_waitcnt lgkmcnt(0)
	v_mfma_f32_16x16x32_bf16 v[56:59], v[160:163], v[194:197], v[56:59]
	v_mfma_f32_16x16x32_bf16 v[48:51], v[168:171], v[194:197], v[48:51]
	v_mfma_f32_16x16x32_bf16 v[40:43], v[160:163], v[202:205], v[40:43]
	v_mfma_f32_16x16x32_bf16 v[32:35], v[168:171], v[202:205], v[32:35]
	v_mfma_f32_16x16x32_bf16 v[24:27], v[160:163], v[210:213], v[24:27]
	v_mfma_f32_16x16x32_bf16 v[16:19], v[168:171], v[210:213], v[16:19]
	v_mfma_f32_16x16x32_bf16 v[8:11], v[160:163], v[230:233], v[8:11]
	v_mfma_f32_16x16x32_bf16 v[4:7], v[168:171], v[230:233], v[4:7]
	v_mfma_f32_16x16x32_bf16 v[56:59], v[164:167], v[198:201], v[56:59]
	v_mfma_f32_16x16x32_bf16 v[48:51], v[172:175], v[198:201], v[48:51]
	v_mfma_f32_16x16x32_bf16 v[40:43], v[164:167], v[206:209], v[40:43]
	v_mfma_f32_16x16x32_bf16 v[32:35], v[172:175], v[206:209], v[32:35]
	v_mfma_f32_16x16x32_bf16 v[24:27], v[164:167], v[222:225], v[24:27]
	v_mfma_f32_16x16x32_bf16 v[16:19], v[172:175], v[222:225], v[16:19]
	v_mfma_f32_16x16x32_bf16 v[8:11], v[164:167], v[234:237], v[8:11]
	v_mfma_f32_16x16x32_bf16 v[4:7], v[172:175], v[234:237], v[4:7]
	s_setprio 0
	s_setprio 1
	v_mfma_f32_16x16x32_bf16 v[60:63], v[176:179], v[194:197], v[60:63]
	v_mfma_f32_16x16x32_bf16 v[52:55], v[184:187], v[194:197], v[52:55]
	v_mfma_f32_16x16x32_bf16 v[44:47], v[176:179], v[202:205], v[44:47]
	v_mfma_f32_16x16x32_bf16 v[36:39], v[184:187], v[202:205], v[36:39]
	v_mfma_f32_16x16x32_bf16 v[28:31], v[176:179], v[210:213], v[28:31]
	v_mfma_f32_16x16x32_bf16 v[20:23], v[184:187], v[210:213], v[20:23]
	v_mfma_f32_16x16x32_bf16 v[12:15], v[176:179], v[230:233], v[12:15]
	v_mfma_f32_16x16x32_bf16 v[0:3], v[184:187], v[230:233], v[0:3]
	v_mfma_f32_16x16x32_bf16 v[60:63], v[180:183], v[198:201], v[60:63]
	v_mfma_f32_16x16x32_bf16 v[52:55], v[188:191], v[198:201], v[52:55]
	v_mfma_f32_16x16x32_bf16 v[44:47], v[180:183], v[206:209], v[44:47]
	v_mfma_f32_16x16x32_bf16 v[36:39], v[188:191], v[206:209], v[36:39]
	v_mfma_f32_16x16x32_bf16 v[28:31], v[180:183], v[222:225], v[28:31]
	v_mfma_f32_16x16x32_bf16 v[20:23], v[188:191], v[222:225], v[20:23]
	v_mfma_f32_16x16x32_bf16 v[12:15], v[180:183], v[234:237], v[12:15]
	v_mfma_f32_16x16x32_bf16 v[0:3], v[188:191], v[234:237], v[0:3]
	s_setprio 0
	s_barrier
	s_add_i32 s2, 0, 0x18000
	v_add_u32_e32 v135, s2, v143
	s_add_i32 s76, 0, 0x1c000
	ds_read_b128 v[160:163], v135
	ds_read_b128 v[164:167], v135 offset:1024
	ds_read_b128 v[168:171], v135 offset:2048
	ds_read_b128 v[172:175], v135 offset:3072
	v_add_u32_e32 v135, s76, v143
	ds_read_b128 v[176:179], v135
	ds_read_b128 v[180:183], v135 offset:1024
	ds_read_b128 v[184:187], v135 offset:2048
	ds_read_b128 v[188:191], v135 offset:3072
	s_mov_b32 m0, s68
	ds_read_b128 v[194:197], v152 offset:32768
	ds_read_b128 v[198:201], v152 offset:33792
	ds_read_b128 v[202:205], v152 offset:34816
	ds_read_b128 v[206:209], v152 offset:35840
	ds_read_b128 v[210:213], v152 offset:36864
	ds_read_b128 v[222:225], v152 offset:37888
	ds_read_b128 v[230:233], v152 offset:38912
	ds_read_b128 v[234:237], v152 offset:39936
	s_nop 0
	global_load_lds_dwordx4 v96, s[20:21]
	s_mov_b32 m0, s69
	s_nop 0
	global_load_lds_dwordx4 v133, s[20:21]
	s_waitcnt vmcnt(8)
	s_waitcnt lgkmcnt(0)
	s_barrier
	s_setprio 1
	s_waitcnt lgkmcnt(0)
	v_mfma_f32_16x16x32_bf16 v[122:125], v[160:163], v[194:197], v[122:125]
	v_mfma_f32_16x16x32_bf16 v[114:117], v[168:171], v[194:197], v[114:117]
	v_mfma_f32_16x16x32_bf16 v[106:109], v[160:163], v[202:205], v[106:109]
	v_mfma_f32_16x16x32_bf16 v[98:101], v[168:171], v[202:205], v[98:101]
	v_mfma_f32_16x16x32_bf16 v[88:91], v[160:163], v[210:213], v[88:91]
	v_mfma_f32_16x16x32_bf16 v[80:83], v[168:171], v[210:213], v[80:83]
	v_mfma_f32_16x16x32_bf16 v[72:75], v[160:163], v[230:233], v[72:75]
	v_mfma_f32_16x16x32_bf16 v[64:67], v[168:171], v[230:233], v[64:67]
	v_mfma_f32_16x16x32_bf16 v[122:125], v[164:167], v[198:201], v[122:125]
	v_mfma_f32_16x16x32_bf16 v[114:117], v[172:175], v[198:201], v[114:117]
	v_mfma_f32_16x16x32_bf16 v[106:109], v[164:167], v[206:209], v[106:109]
	v_mfma_f32_16x16x32_bf16 v[98:101], v[172:175], v[206:209], v[98:101]
	v_mfma_f32_16x16x32_bf16 v[88:91], v[164:167], v[222:225], v[88:91]
	v_mfma_f32_16x16x32_bf16 v[80:83], v[172:175], v[222:225], v[80:83]
	v_mfma_f32_16x16x32_bf16 v[72:75], v[164:167], v[234:237], v[72:75]
	v_mfma_f32_16x16x32_bf16 v[64:67], v[172:175], v[234:237], v[64:67]
	s_setprio 0
	s_setprio 1
	v_mfma_f32_16x16x32_bf16 v[126:129], v[176:179], v[194:197], v[126:129]
	v_mfma_f32_16x16x32_bf16 v[118:121], v[184:187], v[194:197], v[118:121]
	v_mfma_f32_16x16x32_bf16 v[110:113], v[176:179], v[202:205], v[110:113]
	v_mfma_f32_16x16x32_bf16 v[102:105], v[184:187], v[202:205], v[102:105]
	v_mfma_f32_16x16x32_bf16 v[92:95], v[176:179], v[210:213], v[92:95]
	v_mfma_f32_16x16x32_bf16 v[84:87], v[184:187], v[210:213], v[84:87]
	v_mfma_f32_16x16x32_bf16 v[76:79], v[176:179], v[230:233], v[76:79]
	v_mfma_f32_16x16x32_bf16 v[68:71], v[184:187], v[230:233], v[68:71]
	v_mfma_f32_16x16x32_bf16 v[126:129], v[180:183], v[198:201], v[126:129]
	v_mfma_f32_16x16x32_bf16 v[118:121], v[188:191], v[198:201], v[118:121]
	v_mfma_f32_16x16x32_bf16 v[110:113], v[180:183], v[206:209], v[110:113]
	v_mfma_f32_16x16x32_bf16 v[102:105], v[188:191], v[206:209], v[102:105]
	v_mfma_f32_16x16x32_bf16 v[92:95], v[180:183], v[222:225], v[92:95]
	v_mfma_f32_16x16x32_bf16 v[84:87], v[188:191], v[222:225], v[84:87]
	v_mfma_f32_16x16x32_bf16 v[76:79], v[180:183], v[234:237], v[76:79]
	v_mfma_f32_16x16x32_bf16 v[68:71], v[188:191], v[234:237], v[68:71]
	s_setprio 0
	s_barrier
; #define PG8_STAGE(bufoff, gbase, voff) do { _Pragma("unroll") for (int _i = 0; _i < 2; ++_i) \
;         __builtin_amdgcn_global_load_lds((const __attribute__((address_space(1))) unsigned*)((const __attribute__((address_space(1))) char*)(gbase) + (unsigned)lnd_v((int)(voff)[_i])), (LAS unsigned*)(lds + (bufoff) + ldsw + _i * 8192), 16, 0, 0); } while (0)
; #define PG8_LDA(dst, b, h) do { _Pragma("unroll") for (int m = 0; m < 4; ++m) _Pragma("unroll") for (int k = 0; k < 2; ++k) dst[m][k] = *(const LAS bf16x8*)(lds + PG8_SA(b, h) + aoff + m * 2048 + k * 1024); } while (0)
; #define PG8_MMA(ai, bj, At, Bt) do { __builtin_amdgcn_s_setprio(1); _Pragma("unroll") for (int m = 0; m < 4; ++m) _Pragma("unroll") for (int n = 0; n < 2; ++n) _Pragma("unroll") for (int k = 0; k < 2; ++k) \
;         acc[ai][bj][m][n] = __builtin_amdgcn_mfma_f32_16x16x32_bf16(Bt[n][k], At[m][k], acc[ai][bj][m][n], 0, 0, 0); __builtin_amdgcn_s_setprio(0); } while (0)
; #define PG8_WAIT_V(n) asm volatile("s_waitcnt vmcnt(" #n ")" ::: "memory")
; #define PG8_WAIT_L(n) asm volatile("s_waitcnt lgkmcnt(" #n ")" ::: "memory")
; #define PG8_BAR __builtin_amdgcn_s_barrier()
; #define PG8_SCHED __builtin_amdgcn_sched_barrier(0)
; template <class Desc, class Epi>
; __device__ __forceinline__ void gemm_phase(const int wv_, LAS unsigned char* lds, const Desc& d, const Epi& E) {
;     ...
;             PG8_LDA(At, 1, 1); PG8_STAGE(PG8_SB(1, 0), b3, voffB); PG8_STAGE(PG8_SB(1, 1), b3 + hstepB, voffB); PG8_STAGE(PG8_SA(1, 0), a3, sA0);
;             PG8_WAIT_V(8); PG8_WAIT_L(0); PG8_BAR; PG8_MMA(1, 0, At, B0); PG8_MMA(1, 1, At, B1); PG8_BAR; PG8_SCHED;
;         }
;         if (wr == 0) PG8_BAR;
	v_mov_b32_e32 v96, v138
	ds_read_b128 v[194:197], v152 offset:49152
	ds_read_b128 v[198:201], v152 offset:50176
	ds_read_b128 v[202:205], v152 offset:51200
	ds_read_b128 v[206:209], v152 offset:52224
	ds_read_b128 v[210:213], v152 offset:53248
	ds_read_b128 v[222:225], v152 offset:54272
	ds_read_b128 v[230:233], v152 offset:55296
	ds_read_b128 v[234:237], v152 offset:56320
	s_add_i32 s2, s2, s63
	v_lshl_add_u64 v[228:229], s[22:23], 0, v[96:97]
	v_lshl_add_u64 v[228:229], v[228:229], 0, s[30:31]
	s_mov_b32 m0, s2
	v_mov_b32_e32 v96, v141
	global_load_lds_dwordx4 v[228:229], off
	s_add_i32 m0, s2, 0x2000
	s_add_u32 s2, s22, 0x40080
	v_lshl_add_u64 v[228:229], s[22:23], 0, v[96:97]
	v_lshl_add_u64 v[228:229], v[228:229], 0, s[30:31]
	s_addc_u32 s3, s23, 0
	v_mov_b32_e32 v96, v138
	s_add_i32 s22, s76, s63
	global_load_lds_dwordx4 v[228:229], off
	s_mov_b32 m0, s22
	v_mov_b32_e32 v135, v97
	global_load_lds_dwordx4 v96, s[2:3]
	v_mov_b32_e32 v96, v141
	s_add_i32 m0, s22, 0x2000
	v_mov_b32_e32 v133, v97
	global_load_lds_dwordx4 v96, s[2:3]
	s_mov_b32 m0, s70
	v_lshl_add_u64 v[134:135], s[20:21], 0, v[134:135]
	v_lshl_add_u64 v[134:135], v[134:135], 0, s[30:31]
	global_load_lds_dwordx4 v[134:135], off
	s_mov_b32 m0, s71
	v_lshl_add_u64 v[132:133], s[20:21], 0, v[132:133]
	v_lshl_add_u64 v[132:133], v[132:133], 0, s[30:31]
	global_load_lds_dwordx4 v[132:133], off
	s_waitcnt vmcnt(8)
	s_waitcnt lgkmcnt(0)
	s_barrier
	s_setprio 1
	s_waitcnt lgkmcnt(0)
	v_mfma_f32_16x16x32_bf16 v[56:59], v[160:163], v[194:197], v[56:59]
	v_mfma_f32_16x16x32_bf16 v[48:51], v[168:171], v[194:197], v[48:51]
	v_mfma_f32_16x16x32_bf16 v[40:43], v[160:163], v[202:205], v[40:43]
	v_mfma_f32_16x16x32_bf16 v[32:35], v[168:171], v[202:205], v[32:35]
	v_mfma_f32_16x16x32_bf16 v[24:27], v[160:163], v[210:213], v[24:27]
	v_mfma_f32_16x16x32_bf16 v[16:19], v[168:171], v[210:213], v[16:19]
	v_mfma_f32_16x16x32_bf16 v[8:11], v[160:163], v[230:233], v[8:11]
	v_mfma_f32_16x16x32_bf16 v[4:7], v[168:171], v[230:233], v[4:7]
	v_mfma_f32_16x16x32_bf16 v[56:59], v[164:167], v[198:201], v[56:59]
	v_mfma_f32_16x16x32_bf16 v[48:51], v[172:175], v[198:201], v[48:51]
	v_mfma_f32_16x16x32_bf16 v[40:43], v[164:167], v[206:209], v[40:43]
	v_mfma_f32_16x16x32_bf16 v[32:35], v[172:175], v[206:209], v[32:35]
	v_mfma_f32_16x16x32_bf16 v[24:27], v[164:167], v[222:225], v[24:27]
	v_mfma_f32_16x16x32_bf16 v[16:19], v[172:175], v[222:225], v[16:19]
	v_mfma_f32_16x16x32_bf16 v[8:11], v[164:167], v[234:237], v[8:11]
	v_mfma_f32_16x16x32_bf16 v[4:7], v[172:175], v[234:237], v[4:7]
	s_setprio 0
	s_setprio 1
	v_mfma_f32_16x16x32_bf16 v[60:63], v[176:179], v[194:197], v[60:63]
	v_mfma_f32_16x16x32_bf16 v[52:55], v[184:187], v[194:197], v[52:55]
	v_mfma_f32_16x16x32_bf16 v[44:47], v[176:179], v[202:205], v[44:47]
	v_mfma_f32_16x16x32_bf16 v[36:39], v[184:187], v[202:205], v[36:39]
	v_mfma_f32_16x16x32_bf16 v[28:31], v[176:179], v[210:213], v[28:31]
	v_mfma_f32_16x16x32_bf16 v[20:23], v[184:187], v[210:213], v[20:23]
	v_mfma_f32_16x16x32_bf16 v[12:15], v[176:179], v[230:233], v[12:15]
	v_mfma_f32_16x16x32_bf16 v[0:3], v[184:187], v[230:233], v[0:3]
	v_mfma_f32_16x16x32_bf16 v[60:63], v[180:183], v[198:201], v[60:63]
	v_mfma_f32_16x16x32_bf16 v[52:55], v[188:191], v[198:201], v[52:55]
	v_mfma_f32_16x16x32_bf16 v[44:47], v[180:183], v[206:209], v[44:47]
	v_mfma_f32_16x16x32_bf16 v[36:39], v[188:191], v[206:209], v[36:39]
	v_mfma_f32_16x16x32_bf16 v[28:31], v[180:183], v[222:225], v[28:31]
	v_mfma_f32_16x16x32_bf16 v[20:23], v[188:191], v[222:225], v[20:23]
	v_mfma_f32_16x16x32_bf16 v[12:15], v[180:183], v[234:237], v[12:15]
	v_mfma_f32_16x16x32_bf16 v[0:3], v[188:191], v[234:237], v[0:3]
	s_setprio 0
	s_barrier
	s_add_i32 s75, s75, 2
	s_cmp_gt_u32 s75, 13
	s_mov_b64 s[2:3], s[4:5]
	s_cbranch_scc0 .LBB0_1565
	s_and_b64 vcc, exec, s[52:53]
	s_cbranch_vccz .LBB0_1568
	s_barrier

; #define PG8_STAGE(bufoff, gbase, voff) do { _Pragma("unroll") for (int _i = 0; _i < 2; ++_i) \
;         __builtin_amdgcn_global_load_lds((const __attribute__((address_space(1))) unsigned*)((const __attribute__((address_space(1))) char*)(gbase) + (unsigned)lnd_v((int)(voff)[_i])), (LAS unsigned*)(lds + (bufoff) + ldsw + _i * 8192), 16, 0, 0); } while (0)
; #define PG8_LDA(dst, b, h) do { _Pragma("unroll") for (int m = 0; m < 4; ++m) _Pragma("unroll") for (int k = 0; k < 2; ++k) dst[m][k] = *(const LAS bf16x8*)(lds + PG8_SA(b, h) + aoff + m * 2048 + k * 1024); } while (0)
; #define PG8_LDB(dst, b, h) do { _Pragma("unroll") for (int n = 0; n < 2; ++n) _Pragma("unroll") for (int k = 0; k < 2; ++k) dst[n][k] = *(const LAS bf16x8*)(lds + PG8_SB(b, h) + boff + n * 2048 + k * 1024); } while (0)
; #define PG8_MMA(ai, bj, At, Bt) do { __builtin_amdgcn_s_setprio(1); _Pragma("unroll") for (int m = 0; m < 4; ++m) _Pragma("unroll") for (int n = 0; n < 2; ++n) _Pragma("unroll") for (int k = 0; k < 2; ++k) \
;         acc[ai][bj][m][n] = __builtin_amdgcn_mfma_f32_16x16x32_bf16(Bt[n][k], At[m][k], acc[ai][bj][m][n], 0, 0, 0); __builtin_amdgcn_s_setprio(0); } while (0)
; template <class Desc, class Epi>
; __device__ __forceinline__ void gemm_phase(const int wv_, LAS unsigned char* lds, const Desc& d, const Epi& E) {
;     ...
;             if constexpr (Desc::GATHER) { sA0[0] = last ? voffAn[0] : voffA[0]; sA0[1] = last ? voffAn[1] : voffA[1]; sA1[0] = last ? voffAn1[0] : voffA1[0]; sA1[1] = last ? voffAn1[1] : voffA1[1]; }
;             else { sA0[0] = voffA[0]; sA0[1] = voffA[1]; sA1[0] = voffA1[0]; sA1[1] = voffA1[1]; }
;             const char* a1 = cA + (size_t)(t + 1) * kstep;
;             const char* a2 = last ? nA : cA + (size_t)(t + 2) * kstep; const char* b2 = last ? nB : cB + (size_t)(t + 2) * kstep;
;             const char* a3 = a2 + kstep; const char* b3 = b2 + kstep;
;             PG8_LDB(B0, 0, 0); PG8_LDB(B1, 0, 1); PG8_SCHED; PG8_LDA(At, 0, 0); PG8_STAGE(PG8_SA(1, 1), a1, voffA1);
;             PG8_WAIT_V(8); PG8_WAIT_L(0); PG8_BAR; PG8_MMA(0, 0, At, B0); PG8_MMA(0, 1, At, B1); PG8_BAR; PG8_SCHED;
;             PG8_LDA(At, 0, 1); PG8_STAGE(PG8_SB(0, 0), b2, voffB); PG8_STAGE(PG8_SB(0, 1), b2 + hstepB, voffB); PG8_STAGE(PG8_SA(0, 0), a2, sA0);
;             PG8_WAIT_V(8); PG8_WAIT_L(0); PG8_BAR; PG8_MMA(1, 0, At, B0); PG8_MMA(1, 1, At, B1); PG8_BAR; PG8_SCHED;
.LBB0_1861:
	s_add_u32 s4, s2, 0x100
	s_addc_u32 s5, s3, 0
	s_add_u32 s22, s29, s2
	s_addc_u32 s23, s51, s3
	s_cmp_eq_u32 s66, 12
	s_cselect_b64 vcc, -1, 0
	s_and_b64 s[20:21], vcc, exec
	s_cselect_b32 s20, 0, s4
	s_cselect_b32 s21, 0, s5
	s_cselect_b32 s22, s46, s22
	s_cselect_b32 s23, s47, s23
	s_add_u32 s20, s42, s20
	s_addc_u32 s21, s43, s21
	s_add_i32 s67, 0, 0x10000
	v_add_u32_e32 v135, s67, v143
	s_add_i32 s68, 0, 0x14000
	ds_read_b128 v[160:163], v135
	ds_read_b128 v[164:167], v135 offset:1024
	ds_read_b128 v[168:171], v135 offset:2048
	ds_read_b128 v[172:175], v135 offset:3072
	v_add_u32_e32 v135, s68, v143
	ds_read_b128 v[176:179], v135
	ds_read_b128 v[180:183], v135 offset:1024
	ds_read_b128 v[184:187], v135 offset:2048
	ds_read_b128 v[188:191], v135 offset:3072
	v_cndmask_b32_e32 v134, v157, v153, vcc
	v_cndmask_b32_e32 v132, v159, v154, vcc
	v_cndmask_b32_e32 v96, v131, v155, vcc
	v_cndmask_b32_e32 v133, v158, v156, vcc
	s_add_i32 m0, s57, 0xc000
	v_mov_b32_e32 v135, v131
	s_add_u32 s2, s38, s2
	ds_read_b128 v[194:197], v152
	ds_read_b128 v[198:201], v152 offset:1024
	ds_read_b128 v[202:205], v152 offset:2048
	ds_read_b128 v[206:209], v152 offset:3072
	ds_read_b128 v[210:213], v152 offset:4096
	ds_read_b128 v[222:225], v152 offset:5120
	ds_read_b128 v[230:233], v152 offset:6144
	ds_read_b128 v[234:237], v152 offset:7168
	s_addc_u32 s3, s39, s3
	global_load_lds_dwordx4 v135, s[2:3]
	v_mov_b32_e32 v135, v158
	s_add_i32 m0, s57, 0xe000
	s_nop 0
	global_load_lds_dwordx4 v135, s[2:3]
	s_waitcnt vmcnt(8)
	s_waitcnt lgkmcnt(0)
	s_barrier
	s_setprio 1
	s_waitcnt lgkmcnt(0)
	v_mfma_f32_16x16x32_bf16 v[122:125], v[160:163], v[194:197], v[122:125]
	v_mfma_f32_16x16x32_bf16 v[114:117], v[168:171], v[194:197], v[114:117]
	v_mfma_f32_16x16x32_bf16 v[106:109], v[160:163], v[202:205], v[106:109]
	v_mfma_f32_16x16x32_bf16 v[98:101], v[168:171], v[202:205], v[98:101]
	v_mfma_f32_16x16x32_bf16 v[88:91], v[160:163], v[210:213], v[88:91]
	v_mfma_f32_16x16x32_bf16 v[80:83], v[168:171], v[210:213], v[80:83]
	v_mfma_f32_16x16x32_bf16 v[72:75], v[160:163], v[230:233], v[72:75]
	v_mfma_f32_16x16x32_bf16 v[64:67], v[168:171], v[230:233], v[64:67]
	v_mfma_f32_16x16x32_bf16 v[122:125], v[164:167], v[198:201], v[122:125]
	v_mfma_f32_16x16x32_bf16 v[114:117], v[172:175], v[198:201], v[114:117]
	v_mfma_f32_16x16x32_bf16 v[106:109], v[164:167], v[206:209], v[106:109]
	v_mfma_f32_16x16x32_bf16 v[98:101], v[172:175], v[206:209], v[98:101]
	v_mfma_f32_16x16x32_bf16 v[88:91], v[164:167], v[222:225], v[88:91]
	v_mfma_f32_16x16x32_bf16 v[80:83], v[172:175], v[222:225], v[80:83]
	v_mfma_f32_16x16x32_bf16 v[72:75], v[164:167], v[234:237], v[72:75]
	v_mfma_f32_16x16x32_bf16 v[64:67], v[172:175], v[234:237], v[64:67]
	s_setprio 0
	s_setprio 1
	v_mfma_f32_16x16x32_bf16 v[126:129], v[176:179], v[194:197], v[126:129]
	v_mfma_f32_16x16x32_bf16 v[118:121], v[184:187], v[194:197], v[118:121]
	v_mfma_f32_16x16x32_bf16 v[110:113], v[176:179], v[202:205], v[110:113]
	v_mfma_f32_16x16x32_bf16 v[102:105], v[184:187], v[202:205], v[102:105]
	v_mfma_f32_16x16x32_bf16 v[92:95], v[176:179], v[210:213], v[92:95]
	v_mfma_f32_16x16x32_bf16 v[84:87], v[184:187], v[210:213], v[84:87]
	v_mfma_f32_16x16x32_bf16 v[76:79], v[176:179], v[230:233], v[76:79]
	v_mfma_f32_16x16x32_bf16 v[68:71], v[184:187], v[230:233], v[68:71]
	v_mfma_f32_16x16x32_bf16 v[126:129], v[180:183], v[198:201], v[126:129]
	v_mfma_f32_16x16x32_bf16 v[118:121], v[188:191], v[198:201], v[118:121]
	v_mfma_f32_16x16x32_bf16 v[110:113], v[180:183], v[206:209], v[110:113]
	v_mfma_f32_16x16x32_bf16 v[102:105], v[188:191], v[206:209], v[102:105]
	v_mfma_f32_16x16x32_bf16 v[92:95], v[180:183], v[222:225], v[92:95]
	v_mfma_f32_16x16x32_bf16 v[84:87], v[188:191], v[222:225], v[84:87]
	v_mfma_f32_16x16x32_bf16 v[76:79], v[180:183], v[234:237], v[76:79]
	v_mfma_f32_16x16x32_bf16 v[68:71], v[188:191], v[234:237], v[68:71]
	s_setprio 0
	s_barrier
	v_mov_b32_e32 v135, v138
	s_add_i32 s2, s67, s56
	ds_read_b128 v[194:197], v152 offset:16384
	ds_read_b128 v[198:201], v152 offset:17408
	ds_read_b128 v[202:205], v152 offset:18432
	ds_read_b128 v[206:209], v152 offset:19456
	ds_read_b128 v[210:213], v152 offset:20480
	ds_read_b128 v[222:225], v152 offset:21504
	ds_read_b128 v[230:233], v152 offset:22528
	ds_read_b128 v[234:237], v152 offset:23552
	s_mov_b32 m0, s2
	s_nop 0
	global_load_lds_dwordx4 v135, s[22:23]
	v_mov_b32_e32 v135, v141
	s_add_i32 m0, s2, 0x2000
	s_add_u32 s2, s22, 0x40000
	global_load_lds_dwordx4 v135, s[22:23]
	s_addc_u32 s3, s23, 0
	v_mov_b32_e32 v135, v138
	s_add_i32 s67, s68, s56
	s_mov_b32 m0, s67
	s_nop 0
	global_load_lds_dwordx4 v135, s[2:3]
	v_mov_b32_e32 v135, v141
	s_add_i32 m0, s67, 0x2000
	s_nop 0
	global_load_lds_dwordx4 v135, s[2:3]
	v_mov_b32_e32 v135, v134
	s_mov_b32 m0, s57
	s_nop 0
	global_load_lds_dwordx4 v135, s[20:21]
	v_mov_b32_e32 v135, v132
	s_mov_b32 m0, s58
	s_nop 0
	global_load_lds_dwordx4 v135, s[20:21]
	s_waitcnt vmcnt(8)
	s_waitcnt lgkmcnt(0)
	s_barrier
; #define PG8_STAGE(bufoff, gbase, voff) do { _Pragma("unroll") for (int _i = 0; _i < 2; ++_i) \
;         __builtin_amdgcn_global_load_lds((const __attribute__((address_space(1))) unsigned*)((const __attribute__((address_space(1))) char*)(gbase) + (unsigned)lnd_v((int)(voff)[_i])), (LAS unsigned*)(lds + (bufoff) + ldsw + _i * 8192), 16, 0, 0); } while (0)
; #define PG8_LDA(dst, b, h) do { _Pragma("unroll") for (int m = 0; m < 4; ++m) _Pragma("unroll") for (int k = 0; k < 2; ++k) dst[m][k] = *(const LAS bf16x8*)(lds + PG8_SA(b, h) + aoff + m * 2048 + k * 1024); } while (0)
; #define PG8_LDB(dst, b, h) do { _Pragma("unroll") for (int n = 0; n < 2; ++n) _Pragma("unroll") for (int k = 0; k < 2; ++k) dst[n][k] = *(const LAS bf16x8*)(lds + PG8_SB(b, h) + boff + n * 2048 + k * 1024); } while (0)
; #define PG8_MMA(ai, bj, At, Bt) do { __builtin_amdgcn_s_setprio(1); _Pragma("unroll") for (int m = 0; m < 4; ++m) _Pragma("unroll") for (int n = 0; n < 2; ++n) _Pragma("unroll") for (int k = 0; k < 2; ++k) \
;         acc[ai][bj][m][n] = __builtin_amdgcn_mfma_f32_16x16x32_bf16(Bt[n][k], At[m][k], acc[ai][bj][m][n], 0, 0, 0); __builtin_amdgcn_s_setprio(0); } while (0)
; #define PG8_WAIT_V(n) asm volatile("s_waitcnt vmcnt(" #n ")" ::: "memory")
; #define PG8_WAIT_L(n) asm volatile("s_waitcnt lgkmcnt(" #n ")" ::: "memory")
; #define PG8_BAR __builtin_amdgcn_s_barrier()
; #define PG8_SCHED __builtin_amdgcn_sched_barrier(0)
; template <class Desc, class Epi>
; __device__ __forceinline__ void gemm_phase(const int wv_, LAS unsigned char* lds, const Desc& d, const Epi& E) {
;     ...
;             PG8_WAIT_V(8); PG8_WAIT_L(0); PG8_BAR; PG8_MMA(1, 0, At, B0); PG8_MMA(1, 1, At, B1); PG8_BAR; PG8_SCHED;
;             PG8_LDB(B0, 1, 0); PG8_LDB(B1, 1, 1); PG8_SCHED; PG8_LDA(At, 1, 0); PG8_STAGE(PG8_SA(0, 1), a2, sA1);
;             PG8_WAIT_V(8); PG8_WAIT_L(0); PG8_BAR; PG8_MMA(0, 0, At, B0); PG8_MMA(0, 1, At, B1); PG8_BAR; PG8_SCHED;
	s_setprio 1
	s_waitcnt lgkmcnt(0)
	v_mfma_f32_16x16x32_bf16 v[56:59], v[160:163], v[194:197], v[56:59]
	v_mfma_f32_16x16x32_bf16 v[48:51], v[168:171], v[194:197], v[48:51]
	v_mfma_f32_16x16x32_bf16 v[40:43], v[160:163], v[202:205], v[40:43]
	v_mfma_f32_16x16x32_bf16 v[32:35], v[168:171], v[202:205], v[32:35]
	v_mfma_f32_16x16x32_bf16 v[24:27], v[160:163], v[210:213], v[24:27]
	v_mfma_f32_16x16x32_bf16 v[16:19], v[168:171], v[210:213], v[16:19]
	v_mfma_f32_16x16x32_bf16 v[8:11], v[160:163], v[230:233], v[8:11]
	v_mfma_f32_16x16x32_bf16 v[4:7], v[168:171], v[230:233], v[4:7]
	v_mfma_f32_16x16x32_bf16 v[56:59], v[164:167], v[198:201], v[56:59]
	v_mfma_f32_16x16x32_bf16 v[48:51], v[172:175], v[198:201], v[48:51]
	v_mfma_f32_16x16x32_bf16 v[40:43], v[164:167], v[206:209], v[40:43]
	v_mfma_f32_16x16x32_bf16 v[32:35], v[172:175], v[206:209], v[32:35]
	v_mfma_f32_16x16x32_bf16 v[24:27], v[164:167], v[222:225], v[24:27]
	v_mfma_f32_16x16x32_bf16 v[16:19], v[172:175], v[222:225], v[16:19]
	v_mfma_f32_16x16x32_bf16 v[8:11], v[164:167], v[234:237], v[8:11]
	v_mfma_f32_16x16x32_bf16 v[4:7], v[172:175], v[234:237], v[4:7]
	s_setprio 0
	s_setprio 1
	v_mfma_f32_16x16x32_bf16 v[60:63], v[176:179], v[194:197], v[60:63]
	v_mfma_f32_16x16x32_bf16 v[52:55], v[184:187], v[194:197], v[52:55]
	v_mfma_f32_16x16x32_bf16 v[44:47], v[176:179], v[202:205], v[44:47]
	v_mfma_f32_16x16x32_bf16 v[36:39], v[184:187], v[202:205], v[36:39]
	v_mfma_f32_16x16x32_bf16 v[28:31], v[176:179], v[210:213], v[28:31]
	v_mfma_f32_16x16x32_bf16 v[20:23], v[184:187], v[210:213], v[20:23]
	v_mfma_f32_16x16x32_bf16 v[12:15], v[176:179], v[230:233], v[12:15]
	v_mfma_f32_16x16x32_bf16 v[0:3], v[184:187], v[230:233], v[0:3]
	v_mfma_f32_16x16x32_bf16 v[60:63], v[180:183], v[198:201], v[60:63]
	v_mfma_f32_16x16x32_bf16 v[52:55], v[188:191], v[198:201], v[52:55]
	v_mfma_f32_16x16x32_bf16 v[44:47], v[180:183], v[206:209], v[44:47]
	v_mfma_f32_16x16x32_bf16 v[36:39], v[188:191], v[206:209], v[36:39]
	v_mfma_f32_16x16x32_bf16 v[28:31], v[180:183], v[222:225], v[28:31]
	v_mfma_f32_16x16x32_bf16 v[20:23], v[188:191], v[222:225], v[20:23]
	v_mfma_f32_16x16x32_bf16 v[12:15], v[180:183], v[234:237], v[12:15]
	v_mfma_f32_16x16x32_bf16 v[0:3], v[188:191], v[234:237], v[0:3]
	s_setprio 0
	s_barrier
	s_add_i32 s2, 0, 0x18000
	v_add_u32_e32 v135, s2, v143
	s_add_i32 s67, 0, 0x1c000
	ds_read_b128 v[160:163], v135
	ds_read_b128 v[164:167], v135 offset:1024
	ds_read_b128 v[168:171], v135 offset:2048
	ds_read_b128 v[172:175], v135 offset:3072
	v_add_u32_e32 v135, s67, v143
	ds_read_b128 v[176:179], v135
	ds_read_b128 v[180:183], v135 offset:1024
	ds_read_b128 v[184:187], v135 offset:2048
	ds_read_b128 v[188:191], v135 offset:3072
	s_mov_b32 m0, s59
	ds_read_b128 v[194:197], v152 offset:32768
	ds_read_b128 v[198:201], v152 offset:33792
	ds_read_b128 v[202:205], v152 offset:34816
	ds_read_b128 v[206:209], v152 offset:35840
	ds_read_b128 v[210:213], v152 offset:36864
	ds_read_b128 v[222:225], v152 offset:37888
	ds_read_b128 v[230:233], v152 offset:38912
	ds_read_b128 v[234:237], v152 offset:39936
	s_nop 0
	global_load_lds_dwordx4 v96, s[20:21]
	s_mov_b32 m0, s60
	s_nop 0
	global_load_lds_dwordx4 v133, s[20:21]
	s_waitcnt vmcnt(8)
	s_waitcnt lgkmcnt(0)
	s_barrier
	s_setprio 1
	s_waitcnt lgkmcnt(0)
	v_mfma_f32_16x16x32_bf16 v[122:125], v[160:163], v[194:197], v[122:125]
	v_mfma_f32_16x16x32_bf16 v[114:117], v[168:171], v[194:197], v[114:117]
	v_mfma_f32_16x16x32_bf16 v[106:109], v[160:163], v[202:205], v[106:109]
	v_mfma_f32_16x16x32_bf16 v[98:101], v[168:171], v[202:205], v[98:101]
	v_mfma_f32_16x16x32_bf16 v[88:91], v[160:163], v[210:213], v[88:91]
	v_mfma_f32_16x16x32_bf16 v[80:83], v[168:171], v[210:213], v[80:83]
	v_mfma_f32_16x16x32_bf16 v[72:75], v[160:163], v[230:233], v[72:75]
	v_mfma_f32_16x16x32_bf16 v[64:67], v[168:171], v[230:233], v[64:67]
	v_mfma_f32_16x16x32_bf16 v[122:125], v[164:167], v[198:201], v[122:125]
	v_mfma_f32_16x16x32_bf16 v[114:117], v[172:175], v[198:201], v[114:117]
	v_mfma_f32_16x16x32_bf16 v[106:109], v[164:167], v[206:209], v[106:109]
	v_mfma_f32_16x16x32_bf16 v[98:101], v[172:175], v[206:209], v[98:101]
	v_mfma_f32_16x16x32_bf16 v[88:91], v[164:167], v[222:225], v[88:91]
	v_mfma_f32_16x16x32_bf16 v[80:83], v[172:175], v[222:225], v[80:83]
	v_mfma_f32_16x16x32_bf16 v[72:75], v[164:167], v[234:237], v[72:75]
	v_mfma_f32_16x16x32_bf16 v[64:67], v[172:175], v[234:237], v[64:67]
	s_setprio 0
	s_setprio 1
	v_mfma_f32_16x16x32_bf16 v[126:129], v[176:179], v[194:197], v[126:129]
	v_mfma_f32_16x16x32_bf16 v[118:121], v[184:187], v[194:197], v[118:121]
	v_mfma_f32_16x16x32_bf16 v[110:113], v[176:179], v[202:205], v[110:113]
	v_mfma_f32_16x16x32_bf16 v[102:105], v[184:187], v[202:205], v[102:105]
	v_mfma_f32_16x16x32_bf16 v[92:95], v[176:179], v[210:213], v[92:95]
	v_mfma_f32_16x16x32_bf16 v[84:87], v[184:187], v[210:213], v[84:87]
	v_mfma_f32_16x16x32_bf16 v[76:79], v[176:179], v[230:233], v[76:79]
	v_mfma_f32_16x16x32_bf16 v[68:71], v[184:187], v[230:233], v[68:71]
	v_mfma_f32_16x16x32_bf16 v[126:129], v[180:183], v[198:201], v[126:129]
	v_mfma_f32_16x16x32_bf16 v[118:121], v[188:191], v[198:201], v[118:121]
	v_mfma_f32_16x16x32_bf16 v[110:113], v[180:183], v[206:209], v[110:113]
	v_mfma_f32_16x16x32_bf16 v[102:105], v[188:191], v[206:209], v[102:105]
	v_mfma_f32_16x16x32_bf16 v[92:95], v[180:183], v[222:225], v[92:95]
	v_mfma_f32_16x16x32_bf16 v[84:87], v[188:191], v[222:225], v[84:87]
	v_mfma_f32_16x16x32_bf16 v[76:79], v[180:183], v[234:237], v[76:79]
	v_mfma_f32_16x16x32_bf16 v[68:71], v[188:191], v[234:237], v[68:71]
	s_setprio 0
	s_barrier
; #define PG8_STAGE(bufoff, gbase, voff) do { _Pragma("unroll") for (int _i = 0; _i < 2; ++_i) \
;         __builtin_amdgcn_global_load_lds((const __attribute__((address_space(1))) unsigned*)((const __attribute__((address_space(1))) char*)(gbase) + (unsigned)lnd_v((int)(voff)[_i])), (LAS unsigned*)(lds + (bufoff) + ldsw + _i * 8192), 16, 0, 0); } while (0)
; #define PG8_LDA(dst, b, h) do { _Pragma("unroll") for (int m = 0; m < 4; ++m) _Pragma("unroll") for (int k = 0; k < 2; ++k) dst[m][k] = *(const LAS bf16x8*)(lds + PG8_SA(b, h) + aoff + m * 2048 + k * 1024); } while (0)
; #define PG8_MMA(ai, bj, At, Bt) do { __builtin_amdgcn_s_setprio(1); _Pragma("unroll") for (int m = 0; m < 4; ++m) _Pragma("unroll") for (int n = 0; n < 2; ++n) _Pragma("unroll") for (int k = 0; k < 2; ++k) \
;         acc[ai][bj][m][n] = __builtin_amdgcn_mfma_f32_16x16x32_bf16(Bt[n][k], At[m][k], acc[ai][bj][m][n], 0, 0, 0); __builtin_amdgcn_s_setprio(0); } while (0)
; #define PG8_WAIT_V(n) asm volatile("s_waitcnt vmcnt(" #n ")" ::: "memory")
; #define PG8_WAIT_L(n) asm volatile("s_waitcnt lgkmcnt(" #n ")" ::: "memory")
; #define PG8_BAR __builtin_amdgcn_s_barrier()
; #define PG8_SCHED __builtin_amdgcn_sched_barrier(0)
; template <class Desc, class Epi>
; __device__ __forceinline__ void gemm_phase(const int wv_, LAS unsigned char* lds, const Desc& d, const Epi& E) {
;     ...
;             PG8_LDA(At, 1, 1); PG8_STAGE(PG8_SB(1, 0), b3, voffB); PG8_STAGE(PG8_SB(1, 1), b3 + hstepB, voffB); PG8_STAGE(PG8_SA(1, 0), a3, sA0);
;             PG8_WAIT_V(8); PG8_WAIT_L(0); PG8_BAR; PG8_MMA(1, 0, At, B0); PG8_MMA(1, 1, At, B1); PG8_BAR; PG8_SCHED;
;         }
;         if (wr == 0) PG8_BAR;
	v_mov_b32_e32 v96, v138
	ds_read_b128 v[194:197], v152 offset:49152
	ds_read_b128 v[198:201], v152 offset:50176
	ds_read_b128 v[202:205], v152 offset:51200
	ds_read_b128 v[206:209], v152 offset:52224
	ds_read_b128 v[210:213], v152 offset:53248
	ds_read_b128 v[222:225], v152 offset:54272
	ds_read_b128 v[230:233], v152 offset:55296
	ds_read_b128 v[234:237], v152 offset:56320
	s_add_i32 s2, s2, s56
	v_lshl_add_u64 v[228:229], s[22:23], 0, v[96:97]
	v_lshl_add_u64 v[228:229], v[228:229], 0, s[30:31]
	s_mov_b32 m0, s2
	v_mov_b32_e32 v96, v141
	global_load_lds_dwordx4 v[228:229], off
	s_add_i32 m0, s2, 0x2000
	s_add_u32 s2, s22, 0x40080
	v_lshl_add_u64 v[228:229], s[22:23], 0, v[96:97]
	v_lshl_add_u64 v[228:229], v[228:229], 0, s[30:31]
	s_addc_u32 s3, s23, 0
	v_mov_b32_e32 v96, v138
	s_add_i32 s22, s67, s56
	global_load_lds_dwordx4 v[228:229], off
	s_mov_b32 m0, s22
	v_mov_b32_e32 v135, v97
	global_load_lds_dwordx4 v96, s[2:3]
	v_mov_b32_e32 v96, v141
	s_add_i32 m0, s22, 0x2000
	v_mov_b32_e32 v133, v97
	global_load_lds_dwordx4 v96, s[2:3]
	s_mov_b32 m0, s61
	v_lshl_add_u64 v[134:135], s[20:21], 0, v[134:135]
	v_lshl_add_u64 v[134:135], v[134:135], 0, s[30:31]
	global_load_lds_dwordx4 v[134:135], off
	s_mov_b32 m0, s62
	v_lshl_add_u64 v[132:133], s[20:21], 0, v[132:133]
	v_lshl_add_u64 v[132:133], v[132:133], 0, s[30:31]
	global_load_lds_dwordx4 v[132:133], off
	s_waitcnt vmcnt(8)
	s_waitcnt lgkmcnt(0)
	s_barrier
	s_setprio 1
	s_waitcnt lgkmcnt(0)
	v_mfma_f32_16x16x32_bf16 v[56:59], v[160:163], v[194:197], v[56:59]
	v_mfma_f32_16x16x32_bf16 v[48:51], v[168:171], v[194:197], v[48:51]
	v_mfma_f32_16x16x32_bf16 v[40:43], v[160:163], v[202:205], v[40:43]
	v_mfma_f32_16x16x32_bf16 v[32:35], v[168:171], v[202:205], v[32:35]
	v_mfma_f32_16x16x32_bf16 v[24:27], v[160:163], v[210:213], v[24:27]
	v_mfma_f32_16x16x32_bf16 v[16:19], v[168:171], v[210:213], v[16:19]
	v_mfma_f32_16x16x32_bf16 v[8:11], v[160:163], v[230:233], v[8:11]
	v_mfma_f32_16x16x32_bf16 v[4:7], v[168:171], v[230:233], v[4:7]
	v_mfma_f32_16x16x32_bf16 v[56:59], v[164:167], v[198:201], v[56:59]
	v_mfma_f32_16x16x32_bf16 v[48:51], v[172:175], v[198:201], v[48:51]
	v_mfma_f32_16x16x32_bf16 v[40:43], v[164:167], v[206:209], v[40:43]
	v_mfma_f32_16x16x32_bf16 v[32:35], v[172:175], v[206:209], v[32:35]
	v_mfma_f32_16x16x32_bf16 v[24:27], v[164:167], v[222:225], v[24:27]
	v_mfma_f32_16x16x32_bf16 v[16:19], v[172:175], v[222:225], v[16:19]
	v_mfma_f32_16x16x32_bf16 v[8:11], v[164:167], v[234:237], v[8:11]
	v_mfma_f32_16x16x32_bf16 v[4:7], v[172:175], v[234:237], v[4:7]
	s_setprio 0
	s_setprio 1
	v_mfma_f32_16x16x32_bf16 v[60:63], v[176:179], v[194:197], v[60:63]
	v_mfma_f32_16x16x32_bf16 v[52:55], v[184:187], v[194:197], v[52:55]
	v_mfma_f32_16x16x32_bf16 v[44:47], v[176:179], v[202:205], v[44:47]
	v_mfma_f32_16x16x32_bf16 v[36:39], v[184:187], v[202:205], v[36:39]
	v_mfma_f32_16x16x32_bf16 v[28:31], v[176:179], v[210:213], v[28:31]
	v_mfma_f32_16x16x32_bf16 v[20:23], v[184:187], v[210:213], v[20:23]
	v_mfma_f32_16x16x32_bf16 v[12:15], v[176:179], v[230:233], v[12:15]
	v_mfma_f32_16x16x32_bf16 v[0:3], v[184:187], v[230:233], v[0:3]
	v_mfma_f32_16x16x32_bf16 v[60:63], v[180:183], v[198:201], v[60:63]
	v_mfma_f32_16x16x32_bf16 v[52:55], v[188:191], v[198:201], v[52:55]
	v_mfma_f32_16x16x32_bf16 v[44:47], v[180:183], v[206:209], v[44:47]
	v_mfma_f32_16x16x32_bf16 v[36:39], v[188:191], v[206:209], v[36:39]
	v_mfma_f32_16x16x32_bf16 v[28:31], v[180:183], v[222:225], v[28:31]
	v_mfma_f32_16x16x32_bf16 v[20:23], v[188:191], v[222:225], v[20:23]
	v_mfma_f32_16x16x32_bf16 v[12:15], v[180:183], v[234:237], v[12:15]
	v_mfma_f32_16x16x32_bf16 v[0:3], v[188:191], v[234:237], v[0:3]
	s_setprio 0
	s_barrier
	s_add_i32 s66, s66, 2
	s_cmp_gt_u32 s66, 13
	s_mov_b64 s[2:3], s[4:5]
	s_cbranch_scc0 .LBB0_1861
	s_and_b64 vcc, exec, s[40:41]
	s_cbranch_vccz .LBB0_1864
	s_barrier

; #define PG8_STAGE(bufoff, gbase, voff) do { _Pragma("unroll") for (int _i = 0; _i < 2; ++_i) \
;         __builtin_amdgcn_global_load_lds((const __attribute__((address_space(1))) unsigned*)((const __attribute__((address_space(1))) char*)(gbase) + (unsigned)lnd_v((int)(voff)[_i])), (LAS unsigned*)(lds + (bufoff) + ldsw + _i * 8192), 16, 0, 0); } while (0)
; #define PG8_LDA(dst, b, h) do { _Pragma("unroll") for (int m = 0; m < 4; ++m) _Pragma("unroll") for (int k = 0; k < 2; ++k) dst[m][k] = *(const LAS bf16x8*)(lds + PG8_SA(b, h) + aoff + m * 2048 + k * 1024); } while (0)
; #define PG8_LDB(dst, b, h) do { _Pragma("unroll") for (int n = 0; n < 2; ++n) _Pragma("unroll") for (int k = 0; k < 2; ++k) dst[n][k] = *(const LAS bf16x8*)(lds + PG8_SB(b, h) + boff + n * 2048 + k * 1024); } while (0)
; #define PG8_MMA(ai, bj, At, Bt) do { __builtin_amdgcn_s_setprio(1); _Pragma("unroll") for (int m = 0; m < 4; ++m) _Pragma("unroll") for (int n = 0; n < 2; ++n) _Pragma("unroll") for (int k = 0; k < 2; ++k) \
;         acc[ai][bj][m][n] = __builtin_amdgcn_mfma_f32_16x16x32_bf16(Bt[n][k], At[m][k], acc[ai][bj][m][n], 0, 0, 0); __builtin_amdgcn_s_setprio(0); } while (0)
; template <class Desc, class Epi>
; __device__ __forceinline__ void gemm_phase(const int wv_, LAS unsigned char* lds, const Desc& d, const Epi& E) {
;     ...
;             if constexpr (Desc::GATHER) { sA0[0] = last ? voffAn[0] : voffA[0]; sA0[1] = last ? voffAn[1] : voffA[1]; sA1[0] = last ? voffAn1[0] : voffA1[0]; sA1[1] = last ? voffAn1[1] : voffA1[1]; }
;             else { sA0[0] = voffA[0]; sA0[1] = voffA[1]; sA1[0] = voffA1[0]; sA1[1] = voffA1[1]; }
;             const char* a1 = cA + (size_t)(t + 1) * kstep;
;             const char* a2 = last ? nA : cA + (size_t)(t + 2) * kstep; const char* b2 = last ? nB : cB + (size_t)(t + 2) * kstep;
;             const char* a3 = a2 + kstep; const char* b3 = b2 + kstep;
;             PG8_LDB(B0, 0, 0); PG8_LDB(B1, 0, 1); PG8_SCHED; PG8_LDA(At, 0, 0); PG8_STAGE(PG8_SA(1, 1), a1, voffA1);
;             PG8_WAIT_V(8); PG8_WAIT_L(0); PG8_BAR; PG8_MMA(0, 0, At, B0); PG8_MMA(0, 1, At, B1); PG8_BAR; PG8_SCHED;
;             PG8_LDA(At, 0, 1); PG8_STAGE(PG8_SB(0, 0), b2, voffB); PG8_STAGE(PG8_SB(0, 1), b2 + hstepB, voffB); PG8_STAGE(PG8_SA(0, 0), a2, sA0);
;             PG8_WAIT_V(8); PG8_WAIT_L(0); PG8_BAR; PG8_MMA(1, 0, At, B0); PG8_MMA(1, 1, At, B1); PG8_BAR; PG8_SCHED;
.LBB0_1942:
	s_add_u32 s4, s2, 0x80
	s_addc_u32 s5, s3, 0
	s_add_i32 s63, 0, 0x10000
	s_cmp_eq_u32 s62, 28
	s_cselect_b32 s5, s47, s5
	s_cselect_b32 s4, s46, s4
	v_add_u32_e32 v96, s63, v139
	s_cselect_b32 s21, s45, s43
	s_cselect_b32 s20, s44, s29
	s_add_i32 s66, 0, 0x14000
	ds_read_b128 v[150:153], v96
	ds_read_b128 v[154:157], v96 offset:1024
	ds_read_b128 v[158:161], v96 offset:2048
	ds_read_b128 v[162:165], v96 offset:3072
	v_add_u32_e32 v96, s66, v139
	ds_read_b128 v[166:169], v96
	ds_read_b128 v[170:173], v96 offset:1024
	ds_read_b128 v[174:177], v96 offset:2048
	ds_read_b128 v[178:181], v96 offset:3072
	v_mov_b32_e32 v96, v133
	ds_read_b128 v[184:187], v149
	ds_read_b128 v[188:191], v149 offset:1024
	ds_read_b128 v[192:195], v149 offset:2048
	ds_read_b128 v[196:199], v149 offset:3072
	ds_read_b128 v[200:203], v149 offset:4096
	ds_read_b128 v[204:207], v149 offset:5120
	ds_read_b128 v[208:211], v149 offset:6144
	ds_read_b128 v[212:215], v149 offset:7168
	s_add_i32 m0, s53, 0xc000
	s_nop 0
	global_load_lds_dwordx4 v96, s[2:3]
	v_mov_b32_e32 v96, v136
	s_add_i32 m0, s53, 0xe000
	s_nop 0
	global_load_lds_dwordx4 v96, s[2:3]
	s_waitcnt vmcnt(8)
	s_waitcnt lgkmcnt(0)
	s_barrier
	s_setprio 1
	s_waitcnt lgkmcnt(0)
	v_mfma_f32_16x16x32_bf16 v[126:129], v[150:153], v[184:187], v[126:129]
	v_mfma_f32_16x16x32_bf16 v[122:125], v[158:161], v[184:187], v[122:125]
	v_mfma_f32_16x16x32_bf16 v[110:113], v[150:153], v[192:195], v[110:113]
	v_mfma_f32_16x16x32_bf16 v[106:109], v[158:161], v[192:195], v[106:109]
	v_mfma_f32_16x16x32_bf16 v[92:95], v[150:153], v[200:203], v[92:95]
	v_mfma_f32_16x16x32_bf16 v[88:91], v[158:161], v[200:203], v[88:91]
	v_mfma_f32_16x16x32_bf16 v[76:79], v[150:153], v[208:211], v[76:79]
	v_mfma_f32_16x16x32_bf16 v[72:75], v[158:161], v[208:211], v[72:75]
	v_mfma_f32_16x16x32_bf16 v[126:129], v[154:157], v[188:191], v[126:129]
	v_mfma_f32_16x16x32_bf16 v[122:125], v[162:165], v[188:191], v[122:125]
	v_mfma_f32_16x16x32_bf16 v[110:113], v[154:157], v[196:199], v[110:113]
	v_mfma_f32_16x16x32_bf16 v[106:109], v[162:165], v[196:199], v[106:109]
	v_mfma_f32_16x16x32_bf16 v[92:95], v[154:157], v[204:207], v[92:95]
	v_mfma_f32_16x16x32_bf16 v[88:91], v[162:165], v[204:207], v[88:91]
	v_mfma_f32_16x16x32_bf16 v[76:79], v[154:157], v[212:215], v[76:79]
	v_mfma_f32_16x16x32_bf16 v[72:75], v[162:165], v[212:215], v[72:75]
	s_setprio 0
	s_setprio 1
	v_mfma_f32_16x16x32_bf16 v[118:121], v[166:169], v[184:187], v[118:121]
	v_mfma_f32_16x16x32_bf16 v[114:117], v[174:177], v[184:187], v[114:117]
	v_mfma_f32_16x16x32_bf16 v[102:105], v[166:169], v[192:195], v[102:105]
	v_mfma_f32_16x16x32_bf16 v[98:101], v[174:177], v[192:195], v[98:101]
	v_mfma_f32_16x16x32_bf16 v[84:87], v[166:169], v[200:203], v[84:87]
	v_mfma_f32_16x16x32_bf16 v[80:83], v[174:177], v[200:203], v[80:83]
	v_mfma_f32_16x16x32_bf16 v[68:71], v[166:169], v[208:211], v[68:71]
	v_mfma_f32_16x16x32_bf16 v[64:67], v[174:177], v[208:211], v[64:67]
	v_mfma_f32_16x16x32_bf16 v[118:121], v[170:173], v[188:191], v[118:121]
	v_mfma_f32_16x16x32_bf16 v[114:117], v[178:181], v[188:191], v[114:117]
	v_mfma_f32_16x16x32_bf16 v[102:105], v[170:173], v[196:199], v[102:105]
	v_mfma_f32_16x16x32_bf16 v[98:101], v[178:181], v[196:199], v[98:101]
	v_mfma_f32_16x16x32_bf16 v[84:87], v[170:173], v[204:207], v[84:87]
	v_mfma_f32_16x16x32_bf16 v[80:83], v[178:181], v[204:207], v[80:83]
	v_mfma_f32_16x16x32_bf16 v[68:71], v[170:173], v[212:215], v[68:71]
	v_mfma_f32_16x16x32_bf16 v[64:67], v[178:181], v[212:215], v[64:67]
	s_setprio 0
	s_barrier
	v_mov_b32_e32 v96, v134
	s_add_i32 s63, s63, s52
	ds_read_b128 v[184:187], v149 offset:16384
	ds_read_b128 v[188:191], v149 offset:17408
	ds_read_b128 v[192:195], v149 offset:18432
	ds_read_b128 v[196:199], v149 offset:19456
	ds_read_b128 v[200:203], v149 offset:20480
	ds_read_b128 v[204:207], v149 offset:21504
	ds_read_b128 v[208:211], v149 offset:22528
	ds_read_b128 v[212:215], v149 offset:23552
	s_mov_b32 m0, s63
	s_nop 0
	global_load_lds_dwordx4 v96, s[20:21]
	v_mov_b32_e32 v96, v137
	s_add_i32 m0, s63, 0x2000
	s_add_u32 s64, s20, 0x80000
	global_load_lds_dwordx4 v96, s[20:21]
	s_addc_u32 s65, s21, 0
	v_mov_b32_e32 v96, v134
	s_add_i32 s63, s66, s52
	s_mov_b32 m0, s63
	s_nop 0
	global_load_lds_dwordx4 v96, s[64:65]
	v_mov_b32_e32 v96, v137
	s_add_i32 m0, s63, 0x2000
	s_nop 0
	global_load_lds_dwordx4 v96, s[64:65]
	v_mov_b32_e32 v96, v132
	s_mov_b32 m0, s53
	s_nop 0
	global_load_lds_dwordx4 v96, s[4:5]
	v_mov_b32_e32 v96, v135
	s_mov_b32 m0, s54
	s_nop 0
	global_load_lds_dwordx4 v96, s[4:5]
	s_waitcnt vmcnt(8)
	s_waitcnt lgkmcnt(0)
	s_barrier
; #define PG8_STAGE(bufoff, gbase, voff) do { _Pragma("unroll") for (int _i = 0; _i < 2; ++_i) \
;         __builtin_amdgcn_global_load_lds((const __attribute__((address_space(1))) unsigned*)((const __attribute__((address_space(1))) char*)(gbase) + (unsigned)lnd_v((int)(voff)[_i])), (LAS unsigned*)(lds + (bufoff) + ldsw + _i * 8192), 16, 0, 0); } while (0)
; #define PG8_LDA(dst, b, h) do { _Pragma("unroll") for (int m = 0; m < 4; ++m) _Pragma("unroll") for (int k = 0; k < 2; ++k) dst[m][k] = *(const LAS bf16x8*)(lds + PG8_SA(b, h) + aoff + m * 2048 + k * 1024); } while (0)
; #define PG8_LDB(dst, b, h) do { _Pragma("unroll") for (int n = 0; n < 2; ++n) _Pragma("unroll") for (int k = 0; k < 2; ++k) dst[n][k] = *(const LAS bf16x8*)(lds + PG8_SB(b, h) + boff + n * 2048 + k * 1024); } while (0)
; #define PG8_MMA(ai, bj, At, Bt) do { __builtin_amdgcn_s_setprio(1); _Pragma("unroll") for (int m = 0; m < 4; ++m) _Pragma("unroll") for (int n = 0; n < 2; ++n) _Pragma("unroll") for (int k = 0; k < 2; ++k) \
;         acc[ai][bj][m][n] = __builtin_amdgcn_mfma_f32_16x16x32_bf16(Bt[n][k], At[m][k], acc[ai][bj][m][n], 0, 0, 0); __builtin_amdgcn_s_setprio(0); } while (0)
; #define PG8_WAIT_V(n) asm volatile("s_waitcnt vmcnt(" #n ")" ::: "memory")
; #define PG8_WAIT_L(n) asm volatile("s_waitcnt lgkmcnt(" #n ")" ::: "memory")
; #define PG8_BAR __builtin_amdgcn_s_barrier()
; #define PG8_SCHED __builtin_amdgcn_sched_barrier(0)
; template <class Desc, class Epi>
; __device__ __forceinline__ void gemm_phase(const int wv_, LAS unsigned char* lds, const Desc& d, const Epi& E) {
;     ...
;             PG8_WAIT_V(8); PG8_WAIT_L(0); PG8_BAR; PG8_MMA(1, 0, At, B0); PG8_MMA(1, 1, At, B1); PG8_BAR; PG8_SCHED;
;             PG8_LDB(B0, 1, 0); PG8_LDB(B1, 1, 1); PG8_SCHED; PG8_LDA(At, 1, 0); PG8_STAGE(PG8_SA(0, 1), a2, sA1);
;             PG8_WAIT_V(8); PG8_WAIT_L(0); PG8_BAR; PG8_MMA(0, 0, At, B0); PG8_MMA(0, 1, At, B1); PG8_BAR; PG8_SCHED;
	s_setprio 1
	s_waitcnt lgkmcnt(0)
	v_mfma_f32_16x16x32_bf16 v[60:63], v[150:153], v[184:187], v[60:63]
	v_mfma_f32_16x16x32_bf16 v[56:59], v[158:161], v[184:187], v[56:59]
	v_mfma_f32_16x16x32_bf16 v[44:47], v[150:153], v[192:195], v[44:47]
	v_mfma_f32_16x16x32_bf16 v[32:35], v[158:161], v[192:195], v[32:35]
	v_mfma_f32_16x16x32_bf16 v[16:19], v[150:153], v[200:203], v[16:19]
	v_mfma_f32_16x16x32_bf16 v[8:11], v[158:161], v[200:203], v[8:11]
	v_mfma_f32_16x16x32_bf16 v[4:7], v[150:153], v[208:211], v[4:7]
	v_mfma_f32_16x16x32_bf16 v[0:3], v[158:161], v[208:211], v[0:3]
	v_mfma_f32_16x16x32_bf16 v[60:63], v[154:157], v[188:191], v[60:63]
	v_mfma_f32_16x16x32_bf16 v[56:59], v[162:165], v[188:191], v[56:59]
	v_mfma_f32_16x16x32_bf16 v[44:47], v[154:157], v[196:199], v[44:47]
	v_mfma_f32_16x16x32_bf16 v[32:35], v[162:165], v[196:199], v[32:35]
	v_mfma_f32_16x16x32_bf16 v[16:19], v[154:157], v[204:207], v[16:19]
	v_mfma_f32_16x16x32_bf16 v[8:11], v[162:165], v[204:207], v[8:11]
	v_mfma_f32_16x16x32_bf16 v[4:7], v[154:157], v[212:215], v[4:7]
	v_mfma_f32_16x16x32_bf16 v[0:3], v[162:165], v[212:215], v[0:3]
	s_setprio 0
	s_setprio 1
	v_mfma_f32_16x16x32_bf16 v[52:55], v[166:169], v[184:187], v[52:55]
	v_mfma_f32_16x16x32_bf16 v[48:51], v[174:177], v[184:187], v[48:51]
	v_mfma_f32_16x16x32_bf16 v[28:31], v[166:169], v[192:195], v[28:31]
	v_mfma_f32_16x16x32_bf16 v[12:15], v[174:177], v[192:195], v[12:15]
	v_mfma_f32_16x16x32_bf16 v[36:39], v[166:169], v[200:203], v[36:39]
	v_mfma_f32_16x16x32_bf16 v[40:43], v[174:177], v[200:203], v[40:43]
	v_mfma_f32_16x16x32_bf16 v[20:23], v[166:169], v[208:211], v[20:23]
	v_mfma_f32_16x16x32_bf16 v[24:27], v[174:177], v[208:211], v[24:27]
	v_mfma_f32_16x16x32_bf16 v[52:55], v[170:173], v[188:191], v[52:55]
	v_mfma_f32_16x16x32_bf16 v[48:51], v[178:181], v[188:191], v[48:51]
	v_mfma_f32_16x16x32_bf16 v[28:31], v[170:173], v[196:199], v[28:31]
	v_mfma_f32_16x16x32_bf16 v[12:15], v[178:181], v[196:199], v[12:15]
	v_mfma_f32_16x16x32_bf16 v[36:39], v[170:173], v[204:207], v[36:39]
	v_mfma_f32_16x16x32_bf16 v[40:43], v[178:181], v[204:207], v[40:43]
	v_mfma_f32_16x16x32_bf16 v[20:23], v[170:173], v[212:215], v[20:23]
	v_mfma_f32_16x16x32_bf16 v[24:27], v[178:181], v[212:215], v[24:27]
	s_setprio 0
	s_barrier
	s_add_i32 s63, 0, 0x18000
	v_add_u32_e32 v96, s63, v139
	s_add_i32 s64, 0, 0x1c000
	ds_read_b128 v[150:153], v96
	ds_read_b128 v[154:157], v96 offset:1024
	ds_read_b128 v[158:161], v96 offset:2048
	ds_read_b128 v[162:165], v96 offset:3072
	v_add_u32_e32 v96, s64, v139
	ds_read_b128 v[166:169], v96
	ds_read_b128 v[170:173], v96 offset:1024
	ds_read_b128 v[174:177], v96 offset:2048
	ds_read_b128 v[178:181], v96 offset:3072
	v_mov_b32_e32 v96, v133
	s_mov_b32 m0, s55
	ds_read_b128 v[184:187], v149 offset:32768
	ds_read_b128 v[188:191], v149 offset:33792
	ds_read_b128 v[192:195], v149 offset:34816
	ds_read_b128 v[196:199], v149 offset:35840
	ds_read_b128 v[200:203], v149 offset:36864
	ds_read_b128 v[204:207], v149 offset:37888
	ds_read_b128 v[208:211], v149 offset:38912
	ds_read_b128 v[212:215], v149 offset:39936
	s_nop 0
	global_load_lds_dwordx4 v96, s[4:5]
	v_mov_b32_e32 v96, v136
	s_mov_b32 m0, s56
	s_nop 0
	global_load_lds_dwordx4 v96, s[4:5]
	s_waitcnt vmcnt(8)
	s_waitcnt lgkmcnt(0)
	s_barrier
	s_setprio 1
	s_waitcnt lgkmcnt(0)
	v_mfma_f32_16x16x32_bf16 v[126:129], v[150:153], v[184:187], v[126:129]
	v_mfma_f32_16x16x32_bf16 v[122:125], v[158:161], v[184:187], v[122:125]
	v_mfma_f32_16x16x32_bf16 v[110:113], v[150:153], v[192:195], v[110:113]
	v_mfma_f32_16x16x32_bf16 v[106:109], v[158:161], v[192:195], v[106:109]
	v_mfma_f32_16x16x32_bf16 v[92:95], v[150:153], v[200:203], v[92:95]
	v_mfma_f32_16x16x32_bf16 v[88:91], v[158:161], v[200:203], v[88:91]
	v_mfma_f32_16x16x32_bf16 v[76:79], v[150:153], v[208:211], v[76:79]
	v_mfma_f32_16x16x32_bf16 v[72:75], v[158:161], v[208:211], v[72:75]
	v_mfma_f32_16x16x32_bf16 v[126:129], v[154:157], v[188:191], v[126:129]
	v_mfma_f32_16x16x32_bf16 v[122:125], v[162:165], v[188:191], v[122:125]
	v_mfma_f32_16x16x32_bf16 v[110:113], v[154:157], v[196:199], v[110:113]
	v_mfma_f32_16x16x32_bf16 v[106:109], v[162:165], v[196:199], v[106:109]
	v_mfma_f32_16x16x32_bf16 v[92:95], v[154:157], v[204:207], v[92:95]
	v_mfma_f32_16x16x32_bf16 v[88:91], v[162:165], v[204:207], v[88:91]
	v_mfma_f32_16x16x32_bf16 v[76:79], v[154:157], v[212:215], v[76:79]
	v_mfma_f32_16x16x32_bf16 v[72:75], v[162:165], v[212:215], v[72:75]
	s_setprio 0
	s_setprio 1
	v_mfma_f32_16x16x32_bf16 v[118:121], v[166:169], v[184:187], v[118:121]
	v_mfma_f32_16x16x32_bf16 v[114:117], v[174:177], v[184:187], v[114:117]
	v_mfma_f32_16x16x32_bf16 v[102:105], v[166:169], v[192:195], v[102:105]
	v_mfma_f32_16x16x32_bf16 v[98:101], v[174:177], v[192:195], v[98:101]
	v_mfma_f32_16x16x32_bf16 v[84:87], v[166:169], v[200:203], v[84:87]
	v_mfma_f32_16x16x32_bf16 v[80:83], v[174:177], v[200:203], v[80:83]
	v_mfma_f32_16x16x32_bf16 v[68:71], v[166:169], v[208:211], v[68:71]
	v_mfma_f32_16x16x32_bf16 v[64:67], v[174:177], v[208:211], v[64:67]
	v_mfma_f32_16x16x32_bf16 v[118:121], v[170:173], v[188:191], v[118:121]
	v_mfma_f32_16x16x32_bf16 v[114:117], v[178:181], v[188:191], v[114:117]
	v_mfma_f32_16x16x32_bf16 v[102:105], v[170:173], v[196:199], v[102:105]
	v_mfma_f32_16x16x32_bf16 v[98:101], v[178:181], v[196:199], v[98:101]
	v_mfma_f32_16x16x32_bf16 v[84:87], v[170:173], v[204:207], v[84:87]
	v_mfma_f32_16x16x32_bf16 v[80:83], v[178:181], v[204:207], v[80:83]
	v_mfma_f32_16x16x32_bf16 v[68:71], v[170:173], v[212:215], v[68:71]
	v_mfma_f32_16x16x32_bf16 v[64:67], v[178:181], v[212:215], v[64:67]
	s_setprio 0
	s_barrier
; #define PG8_STAGE(bufoff, gbase, voff) do { _Pragma("unroll") for (int _i = 0; _i < 2; ++_i) \
;         __builtin_amdgcn_global_load_lds((const __attribute__((address_space(1))) unsigned*)((const __attribute__((address_space(1))) char*)(gbase) + (unsigned)lnd_v((int)(voff)[_i])), (LAS unsigned*)(lds + (bufoff) + ldsw + _i * 8192), 16, 0, 0); } while (0)
; #define PG8_LDA(dst, b, h) do { _Pragma("unroll") for (int m = 0; m < 4; ++m) _Pragma("unroll") for (int k = 0; k < 2; ++k) dst[m][k] = *(const LAS bf16x8*)(lds + PG8_SA(b, h) + aoff + m * 2048 + k * 1024); } while (0)
; #define PG8_MMA(ai, bj, At, Bt) do { __builtin_amdgcn_s_setprio(1); _Pragma("unroll") for (int m = 0; m < 4; ++m) _Pragma("unroll") for (int n = 0; n < 2; ++n) _Pragma("unroll") for (int k = 0; k < 2; ++k) \
;         acc[ai][bj][m][n] = __builtin_amdgcn_mfma_f32_16x16x32_bf16(Bt[n][k], At[m][k], acc[ai][bj][m][n], 0, 0, 0); __builtin_amdgcn_s_setprio(0); } while (0)
; #define PG8_WAIT_V(n) asm volatile("s_waitcnt vmcnt(" #n ")" ::: "memory")
; #define PG8_WAIT_L(n) asm volatile("s_waitcnt lgkmcnt(" #n ")" ::: "memory")
; #define PG8_BAR __builtin_amdgcn_s_barrier()
; #define PG8_SCHED __builtin_amdgcn_sched_barrier(0)
; template <class Desc, class Epi>
; __device__ __forceinline__ void gemm_phase(const int wv_, LAS unsigned char* lds, const Desc& d, const Epi& E) {
;     ...
;             PG8_LDA(At, 1, 1); PG8_STAGE(PG8_SB(1, 0), b3, voffB); PG8_STAGE(PG8_SB(1, 1), b3 + hstepB, voffB); PG8_STAGE(PG8_SA(1, 0), a3, sA0);
;             PG8_WAIT_V(8); PG8_WAIT_L(0); PG8_BAR; PG8_MMA(1, 0, At, B0); PG8_MMA(1, 1, At, B1); PG8_BAR; PG8_SCHED;
;         }
;         if (wr == 0) PG8_BAR;
	v_mov_b32_e32 v96, v134
	ds_read_b128 v[184:187], v149 offset:49152
	ds_read_b128 v[188:191], v149 offset:50176
	ds_read_b128 v[192:195], v149 offset:51200
	ds_read_b128 v[196:199], v149 offset:52224
	ds_read_b128 v[200:203], v149 offset:53248
	ds_read_b128 v[204:207], v149 offset:54272
	ds_read_b128 v[208:211], v149 offset:55296
	ds_read_b128 v[212:215], v149 offset:56320
	s_add_i32 s63, s63, s52
	v_lshl_add_u64 v[130:131], s[20:21], 0, v[96:97]
	v_lshl_add_u64 v[130:131], v[130:131], 0, s[30:31]
	s_mov_b32 m0, s63
	v_mov_b32_e32 v96, v137
	global_load_lds_dwordx4 v[130:131], off
	s_add_i32 m0, s63, 0x2000
	s_nop 0
	v_lshl_add_u64 v[130:131], s[20:21], 0, v[96:97]
	s_add_u32 s20, s20, 0x80080
	v_lshl_add_u64 v[130:131], v[130:131], 0, s[30:31]
	s_addc_u32 s21, s21, 0
	v_mov_b32_e32 v96, v134
	s_add_i32 s63, s64, s52
	global_load_lds_dwordx4 v[130:131], off
	s_mov_b32 m0, s63
	s_nop 0
	global_load_lds_dwordx4 v96, s[20:21]
	v_mov_b32_e32 v96, v137
	s_add_i32 m0, s63, 0x2000
	s_nop 0
	global_load_lds_dwordx4 v96, s[20:21]
	v_mov_b32_e32 v96, v132
	s_mov_b32 m0, s57
	v_lshl_add_u64 v[130:131], s[4:5], 0, v[96:97]
	v_lshl_add_u64 v[130:131], v[130:131], 0, s[30:31]
	v_mov_b32_e32 v96, v135
	global_load_lds_dwordx4 v[130:131], off
	s_mov_b32 m0, s58
	v_lshl_add_u64 v[130:131], s[4:5], 0, v[96:97]
	v_lshl_add_u64 v[130:131], v[130:131], 0, s[30:31]
	global_load_lds_dwordx4 v[130:131], off
	s_waitcnt vmcnt(8)
	s_waitcnt lgkmcnt(0)
	s_barrier
	s_setprio 1
	s_waitcnt lgkmcnt(0)
	v_mfma_f32_16x16x32_bf16 v[60:63], v[150:153], v[184:187], v[60:63]
	v_mfma_f32_16x16x32_bf16 v[56:59], v[158:161], v[184:187], v[56:59]
	v_mfma_f32_16x16x32_bf16 v[44:47], v[150:153], v[192:195], v[44:47]
	v_mfma_f32_16x16x32_bf16 v[32:35], v[158:161], v[192:195], v[32:35]
	v_mfma_f32_16x16x32_bf16 v[16:19], v[150:153], v[200:203], v[16:19]
	v_mfma_f32_16x16x32_bf16 v[8:11], v[158:161], v[200:203], v[8:11]
	v_mfma_f32_16x16x32_bf16 v[4:7], v[150:153], v[208:211], v[4:7]
	v_mfma_f32_16x16x32_bf16 v[0:3], v[158:161], v[208:211], v[0:3]
	v_mfma_f32_16x16x32_bf16 v[60:63], v[154:157], v[188:191], v[60:63]
	v_mfma_f32_16x16x32_bf16 v[56:59], v[162:165], v[188:191], v[56:59]
	v_mfma_f32_16x16x32_bf16 v[44:47], v[154:157], v[196:199], v[44:47]
	v_mfma_f32_16x16x32_bf16 v[32:35], v[162:165], v[196:199], v[32:35]
	v_mfma_f32_16x16x32_bf16 v[16:19], v[154:157], v[204:207], v[16:19]
	v_mfma_f32_16x16x32_bf16 v[8:11], v[162:165], v[204:207], v[8:11]
	v_mfma_f32_16x16x32_bf16 v[4:7], v[154:157], v[212:215], v[4:7]
	v_mfma_f32_16x16x32_bf16 v[0:3], v[162:165], v[212:215], v[0:3]
	s_setprio 0
	s_setprio 1
	v_mfma_f32_16x16x32_bf16 v[52:55], v[166:169], v[184:187], v[52:55]
	v_mfma_f32_16x16x32_bf16 v[48:51], v[174:177], v[184:187], v[48:51]
	v_mfma_f32_16x16x32_bf16 v[28:31], v[166:169], v[192:195], v[28:31]
	v_mfma_f32_16x16x32_bf16 v[12:15], v[174:177], v[192:195], v[12:15]
	v_mfma_f32_16x16x32_bf16 v[36:39], v[166:169], v[200:203], v[36:39]
	v_mfma_f32_16x16x32_bf16 v[40:43], v[174:177], v[200:203], v[40:43]
	v_mfma_f32_16x16x32_bf16 v[20:23], v[166:169], v[208:211], v[20:23]
	v_mfma_f32_16x16x32_bf16 v[24:27], v[174:177], v[208:211], v[24:27]
	v_mfma_f32_16x16x32_bf16 v[52:55], v[170:173], v[188:191], v[52:55]
	v_mfma_f32_16x16x32_bf16 v[48:51], v[178:181], v[188:191], v[48:51]
	v_mfma_f32_16x16x32_bf16 v[28:31], v[170:173], v[196:199], v[28:31]
	v_mfma_f32_16x16x32_bf16 v[12:15], v[178:181], v[196:199], v[12:15]
	v_mfma_f32_16x16x32_bf16 v[36:39], v[170:173], v[204:207], v[36:39]
	v_mfma_f32_16x16x32_bf16 v[40:43], v[178:181], v[204:207], v[40:43]
	v_mfma_f32_16x16x32_bf16 v[20:23], v[170:173], v[212:215], v[20:23]
	v_mfma_f32_16x16x32_bf16 v[24:27], v[178:181], v[212:215], v[24:27]
	s_setprio 0
	s_barrier
	s_add_i32 s62, s62, 2
	s_add_u32 s2, s2, 0x100
	s_addc_u32 s3, s3, 0
	s_add_u32 s29, s29, 0x100
	s_addc_u32 s43, s43, 0
	s_cmp_gt_u32 s62, 29
	s_cbranch_scc0 .LBB0_1942
	s_and_b64 vcc, exec, s[40:41]
	s_cbranch_vccz .LBB0_1945
	s_barrier
